# B3 router: the 16-way compare/select chains of the logit butterfly (index registers that only take two values per lane) collapsed to one compare plus one v_cndmask each
# speedup vs baseline: 1.0185x; 1.0076x over previous
.LBB0_1336:
	s_add_i32 s18, s2, s65
	s_max_i32 s13, s18, 4
	s_add_i32 s14, s13, -4
	s_mov_b32 s15, s60
	s_max_i32 s13, s18, 3
	s_lshl_b64 s[36:37], s[14:15], 12
	s_add_i32 s14, s13, -3
	s_max_i32 s13, s18, 2
	s_lshl_b64 s[52:53], s[14:15], 12
	s_add_i32 s14, s13, -2
	s_max_i32 s13, s18, 1
	s_lshl_b64 s[50:51], s[14:15], 12
	s_add_i32 s14, s13, -1
	s_and_b32 s12, s18, 0x7fc
	s_lshl_b64 s[26:27], s[14:15], 12
	s_max_i32 s14, s18, 0
	s_max_i32 s13, s18, -1
	s_lshl_b64 s[24:25], s[14:15], 12
	s_add_i32 s14, s13, 1
	s_min_u32 s13, s12, 15
	s_add_i32 s13, s13, 1
	s_lshl_b64 s[78:79], s[14:15], 12
	s_min_u32 s14, s12, 14
	v_cvt_f32_ubyte0_e32 v0, s13
	s_add_i32 s16, s14, 2
	v_div_scale_f32 v1, s[14:15], v0, v0, 1.0
	v_rcp_f32_e32 v2, v1
	s_min_u32 s13, s12, 7
	s_add_i32 s13, s13, 1
	s_waitcnt lgkmcnt(0)
	v_fma_f32 v3, -v1, v2, 1.0
	v_fmac_f32_e32 v2, v3, v2
	v_div_scale_f32 v3, vcc, 1.0, v0, 1.0
	v_mul_f32_e32 v4, v3, v2
	v_fma_f32 v5, -v1, v4, v3
	v_fmac_f32_e32 v4, v5, v2
	v_fma_f32 v1, -v1, v4, v3
	v_div_fmas_f32 v1, v1, v2, v4
	v_div_fixup_f32 v92, v1, v0, 1.0
	v_cvt_f32_ubyte0_e32 v0, s16
	v_div_scale_f32 v1, s[14:15], v0, v0, 1.0
	v_rcp_f32_e32 v2, v1
	s_min_u32 s14, s12, 6
	s_add_i32 s16, s14, 2
	s_waitcnt lgkmcnt(0)
	v_fma_f32 v3, -v1, v2, 1.0
	v_fmac_f32_e32 v2, v3, v2
	v_div_scale_f32 v3, vcc, 1.0, v0, 1.0
	v_mul_f32_e32 v4, v3, v2
	v_fma_f32 v5, -v1, v4, v3
	v_fmac_f32_e32 v4, v5, v2
	v_fma_f32 v1, -v1, v4, v3
	v_div_fmas_f32 v1, v1, v2, v4
	v_div_fixup_f32 v94, v1, v0, 1.0
	v_cvt_f32_ubyte0_e32 v0, s13
	v_div_scale_f32 v1, s[14:15], v0, v0, 1.0
	v_rcp_f32_e32 v2, v1
	s_min_u32 s13, s12, 3
	s_add_i32 s13, s13, 1
	s_barrier
	v_fma_f32 v3, -v1, v2, 1.0
	v_fmac_f32_e32 v2, v3, v2
	v_div_scale_f32 v3, vcc, 1.0, v0, 1.0
	v_mul_f32_e32 v4, v3, v2
	v_fma_f32 v5, -v1, v4, v3
	v_fmac_f32_e32 v4, v5, v2
	v_fma_f32 v1, -v1, v4, v3
	v_div_fmas_f32 v1, v1, v2, v4
	v_div_fixup_f32 v8, v1, v0, 1.0
	v_cvt_f32_ubyte0_e32 v0, s16
	v_div_scale_f32 v1, s[14:15], v0, v0, 1.0
	v_rcp_f32_e32 v2, v1
	s_min_u32 s14, s12, 2
	s_add_i32 s16, s14, 2
	v_fma_f32 v3, -v1, v2, 1.0
	v_fmac_f32_e32 v2, v3, v2
	v_div_scale_f32 v3, vcc, 1.0, v0, 1.0
	v_mul_f32_e32 v4, v3, v2
	v_fma_f32 v5, -v1, v4, v3
	v_fmac_f32_e32 v4, v5, v2
	v_fma_f32 v1, -v1, v4, v3
	v_div_fmas_f32 v1, v1, v2, v4
	v_div_fixup_f32 v10, v1, v0, 1.0
	v_cvt_f32_ubyte0_e32 v0, s13
	v_div_scale_f32 v1, s[14:15], v0, v0, 1.0
	v_rcp_f32_e32 v2, v1
	v_mov_b32_e32 v27, s7
	s_max_i32 s0, s18, 15
	s_add_i32 s0, s0, -15
	v_fma_f32 v3, -v1, v2, 1.0
	v_fmac_f32_e32 v2, v3, v2
	v_div_scale_f32 v3, vcc, 1.0, v0, 1.0
	v_mul_f32_e32 v4, v3, v2
	v_fma_f32 v5, -v1, v4, v3
	v_fmac_f32_e32 v4, v5, v2
	v_fma_f32 v1, -v1, v4, v3
	v_div_fmas_f32 v1, v1, v2, v4
	v_div_fixup_f32 v4, v1, v0, 1.0
	v_cvt_f32_ubyte0_e32 v0, s16
	v_div_scale_f32 v1, s[14:15], v0, v0, 1.0
	v_rcp_f32_e32 v2, v1
	s_mov_b32 s1, s60
	s_lshl_b64 s[76:77], s[0:1], 12
	s_max_i32 s0, s18, 14
	v_fma_f32 v3, -v1, v2, 1.0
	v_fmac_f32_e32 v2, v3, v2
	v_div_scale_f32 v3, vcc, 1.0, v0, 1.0
	v_mul_f32_e32 v5, v3, v2
	v_fma_f32 v6, -v1, v5, v3
	v_fmac_f32_e32 v5, v6, v2
	v_fma_f32 v1, -v1, v5, v3
	v_div_fmas_f32 v1, v1, v2, v5
	v_mov_b32_e32 v5, v21
	v_div_fixup_f32 v6, v1, v0, 1.0
	ds_read_b64 v[2:3], v27 offset:56
	ds_read_b32 v12, v27 offset:64
	v_lshlrev_b32_e32 v0, 2, v5
	v_ashrrev_i32_e32 v1, 31, v0
	v_lshlrev_b64 v[84:85], 1, v[0:1]
	v_lshl_add_u64 v[0:1], s[92:93], 0, v[84:85]
	v_lshl_add_u64 v[236:237], v[0:1], 0, s[78:79]
	global_load_dwordx2 v[236:237], v[236:237], off
	v_lshl_add_u64 v[238:239], v[0:1], 0, s[26:27]
	global_load_dwordx2 v[238:239], v[238:239], off
	v_lshl_add_u64 v[240:241], v[0:1], 0, s[24:25]
	global_load_dwordx2 v[240:241], v[240:241], off
	s_nop 0
	s_nop 0
	s_nop 0
	s_nop 0
	s_nop 0
	s_add_i32 s0, s0, -14
	s_nop 0
	s_lshl_b64 s[10:11], s[0:1], 12
	s_max_i32 s0, s18, 13
	s_add_i32 s0, s0, -13
	s_lshl_b64 s[8:9], s[0:1], 12
	s_max_i32 s0, s18, 12
	s_add_i32 s0, s0, -12
	s_lshl_b64 s[44:45], s[0:1], 12
	s_max_i32 s0, s18, 11
	s_add_i32 s0, s0, -11
	s_lshl_b64 s[48:49], s[0:1], 12
	s_max_i32 s0, s18, 10
	s_add_i32 s0, s0, -10
	s_lshl_b64 s[46:47], s[0:1], 12
	s_max_i32 s0, s18, 9
	s_add_i32 s0, s0, -9
	s_lshl_b64 s[30:31], s[0:1], 12
	s_max_i32 s0, s18, 8
	s_max_i32 s2, s18, 6
	s_add_i32 s0, s0, -8
	s_add_i32 s2, s2, -6
	s_mov_b32 s3, s60
	s_lshl_b64 s[28:29], s[0:1], 12
	s_max_i32 s0, s18, 7
	s_lshl_b64 s[42:43], s[2:3], 12
	s_max_i32 s2, s18, 5
	s_add_i32 s0, s0, -7
	s_add_i32 s2, s2, -5
	s_lshl_b64 s[0:1], s[0:1], 12
	s_lshl_b64 s[2:3], s[2:3], 12
	s_cmp_eq_u32 s12, 0
	s_cselect_b32 s54, 1.0, 0.5
	s_ashr_i32 s19, s18, 31
	s_lshl_b64 s[12:13], s[18:19], 12
	s_add_u32 s22, s4, s12
	s_addc_u32 s23, s5, s13
	s_or_b32 s16, s18, 1
	s_ashr_i32 s17, s16, 31
	s_lshl_b64 s[12:13], s[16:17], 12
	s_add_u32 s20, s4, s12
	s_addc_u32 s21, s5, s13
	s_add_i32 s17, 0, 0x12000
	s_add_u32 vcc_lo, s92, s78
	s_addc_u32 vcc_hi, s93, s79
	s_add_u32 s26, s92, s26
	s_addc_u32 s27, s93, s27
	s_add_u32 s24, s92, s24
	s_addc_u32 s25, s93, s25
	s_add_u32 s52, s92, s52
	s_addc_u32 s53, s93, s53
	s_add_u32 s50, s92, s50
	s_addc_u32 s51, s93, s51
	s_nop 0
	s_waitcnt vmcnt(2)
	v_lshlrev_b32_e32 v80, 16, v236
	v_and_b32_e32 v81, 0xffff0000, v236
	s_nop 0
	s_waitcnt vmcnt(1)
	v_lshlrev_b32_e32 v90, 16, v238
	v_and_b32_e32 v91, 0xffff0000, v238
	v_lshlrev_b32_e32 v88, 16, v239
	v_and_b32_e32 v89, 0xffff0000, v239
	s_waitcnt lgkmcnt(1)
	v_pk_fma_f32 v[96:97], v[2:3], v[90:91], 0 op_sel_hi:[0,1,0]
	v_pk_fma_f32 v[98:99], v[2:3], v[88:89], 0 op_sel_hi:[0,1,0]
	s_nop 0
	s_waitcnt vmcnt(0)
	v_lshlrev_b32_e32 v100, 16, v240
	v_and_b32_e32 v101, 0xffff0000, v240
	v_lshlrev_b32_e32 v0, 16, v241
	v_and_b32_e32 v1, 0xffff0000, v241
	v_pk_mul_f32 v[102:103], v[2:3], v[0:1] op_sel:[1,0]
	v_pk_fma_f32 v[0:1], v[2:3], v[0:1], v[98:99] op_sel:[1,0,0]
	v_pk_fma_f32 v[96:97], v[2:3], v[100:101], v[96:97] op_sel:[1,0,0]
	v_lshlrev_b32_e32 v14, 16, v237
	v_and_b32_e32 v15, 0xffff0000, v237
	v_pk_mul_f32 v[104:105], v[2:3], v[100:101] op_sel:[1,0]
	v_pk_fma_f32 v[90:91], v[2:3], v[90:91], v[96:97] op_sel_hi:[0,1,1] neg_lo:[1,0,0] neg_hi:[1,0,0]
	v_pk_fma_f32 v[2:3], v[2:3], v[88:89], v[0:1] op_sel_hi:[0,1,1] neg_lo:[1,0,0] neg_hi:[1,0,0]
	s_waitcnt lgkmcnt(0)
	v_pk_mul_f32 v[82:83], v[12:13], v[14:15] op_sel_hi:[0,1]
	v_pk_mul_f32 v[86:87], v[12:13], v[80:81] op_sel_hi:[0,1]
	v_pk_fma_f32 v[2:3], v[12:13], v[14:15], v[2:3] op_sel_hi:[0,1,1]
	v_pk_fma_f32 v[12:13], v[12:13], v[80:81], v[90:91] op_sel_hi:[0,1,1]
	v_lshl_add_u64 v[236:237], s[22:23], 0, v[84:85]
	global_load_dwordx2 v[236:237], v[236:237], off
	v_lshl_add_u64 v[238:239], s[20:21], 0, v[84:85]
	global_load_dwordx2 v[238:239], v[238:239], off
	v_lshl_add_u64 v[88:89], s[22:23], 0, v[84:85]
	v_pk_fma_f32 v[12:13], v[12:13], 0.5, v[86:87] op_sel_hi:[1,0,1] neg_lo:[0,0,1] neg_hi:[0,0,1]
	s_nop 0
	v_pk_fma_f32 v[80:81], s[54:55], v[0:1], v[102:103] op_sel_hi:[0,1,1] neg_lo:[0,0,1] neg_hi:[0,0,1]
	v_lshl_add_u32 v0, v5, 4, s17
	v_pk_fma_f32 v[14:15], v[2:3], 0.5, v[82:83] op_sel_hi:[1,0,1] neg_lo:[0,0,1] neg_hi:[0,0,1]
	ds_read_b128 v[0:3], v0
	v_pk_fma_f32 v[82:83], s[54:55], v[96:97], v[104:105] op_sel_hi:[0,1,1] neg_lo:[0,0,1] neg_hi:[0,0,1]
	s_nop 0
	s_waitcnt vmcnt(1)
	v_lshlrev_b32_e32 v90, 16, v236
	v_and_b32_e32 v91, 0xffff0000, v236
	s_waitcnt lgkmcnt(0)
	v_pk_fma_f32 v[82:83], v[0:1], v[82:83], v[90:91]
	v_lshl_add_u64 v[90:91], s[20:21], 0, v[84:85]
	s_nop 0
	v_lshlrev_b32_e32 v86, 16, v237
	v_and_b32_e32 v87, 0xffff0000, v237
	v_pk_fma_f32 v[80:81], v[2:3], v[80:81], v[86:87]
	s_nop 0
	s_waitcnt vmcnt(0)
	v_lshlrev_b32_e32 v86, 16, v238
	v_and_b32_e32 v87, 0xffff0000, v238
	v_lshlrev_b32_e32 v84, 16, v239
	v_and_b32_e32 v85, 0xffff0000, v239
	v_pk_fma_f32 v[86:87], v[0:1], v[12:13], v[86:87]
	v_cvt_pk_bf16_f32 v0, v82, v83
	v_cvt_pk_bf16_f32 v1, v80, v81
	v_pk_fma_f32 v[84:85], v[2:3], v[14:15], v[84:85]
	v_cvt_pk_bf16_f32 v2, v86, v87
	s_nop 0
	v_cvt_pk_bf16_f32 v3, v84, v85
	global_store_dwordx2 v[88:89], v[0:1], off
	global_store_dwordx2 v[90:91], v[2:3], off
	v_mov_b32_e32 v0, v21
	ds_read_b64 v[2:3], v27 offset:56
	ds_read_b32 v12, v27 offset:64
	v_lshlrev_b32_e32 v88, 2, v0
	v_add_u32_e32 v0, 0x100, v88
	v_ashrrev_i32_e32 v1, 31, v0
	v_lshlrev_b64 v[14:15], 1, v[0:1]
	v_lshl_add_u64 v[236:237], vcc, 0, v[14:15]
	global_load_dwordx2 v[236:237], v[236:237], off
	v_lshl_add_u64 v[238:239], s[26:27], 0, v[14:15]
	global_load_dwordx2 v[238:239], v[238:239], off
	v_lshl_add_u64 v[240:241], s[24:25], 0, v[14:15]
	global_load_dwordx2 v[240:241], v[240:241], off
	s_nop 0
	s_nop 0
	s_nop 0
	s_nop 0
	s_nop 0
	v_ashrrev_i32_e32 v89, 31, v88
	s_nop 0
	v_lshl_add_u32 v0, v0, 2, s17
	s_nop 0
	s_waitcnt vmcnt(2)
	v_lshlrev_b32_e32 v96, 16, v236
	v_and_b32_e32 v97, 0xffff0000, v236
	s_nop 0
	s_waitcnt vmcnt(1)
	v_lshlrev_b32_e32 v104, 16, v238
	v_and_b32_e32 v105, 0xffff0000, v238
	v_lshlrev_b32_e32 v102, 16, v239
	v_and_b32_e32 v103, 0xffff0000, v239
	s_waitcnt lgkmcnt(1)
	v_pk_fma_f32 v[106:107], v[2:3], v[104:105], 0 op_sel_hi:[0,1,0]
	v_pk_fma_f32 v[108:109], v[2:3], v[102:103], 0 op_sel_hi:[0,1,0]
	s_nop 0
	s_waitcnt vmcnt(0)
	v_lshlrev_b32_e32 v110, 16, v240
	v_and_b32_e32 v111, 0xffff0000, v240
	v_lshlrev_b32_e32 v14, 16, v241
	v_and_b32_e32 v15, 0xffff0000, v241
	v_pk_fma_f32 v[108:109], v[2:3], v[14:15], v[108:109] op_sel:[1,0,0]
	v_pk_fma_f32 v[106:107], v[2:3], v[110:111], v[106:107] op_sel:[1,0,0]
	v_lshlrev_b32_e32 v90, 16, v237
	v_and_b32_e32 v91, 0xffff0000, v237
	v_pk_mul_f32 v[112:113], v[2:3], v[14:15] op_sel:[1,0]
	v_pk_mul_f32 v[114:115], v[2:3], v[110:111] op_sel:[1,0]
	v_pk_fma_f32 v[14:15], v[2:3], v[104:105], v[106:107] op_sel_hi:[0,1,1] neg_lo:[1,0,0] neg_hi:[1,0,0]
	v_pk_fma_f32 v[2:3], v[2:3], v[102:103], v[108:109] op_sel_hi:[0,1,1] neg_lo:[1,0,0] neg_hi:[1,0,0]
	s_waitcnt lgkmcnt(0)
	v_pk_mul_f32 v[98:99], v[12:13], v[90:91] op_sel_hi:[0,1]
	v_pk_fma_f32 v[2:3], v[12:13], v[90:91], v[2:3] op_sel_hi:[0,1,1]
	v_pk_mul_f32 v[100:101], v[12:13], v[96:97] op_sel_hi:[0,1]
	v_pk_fma_f32 v[12:13], v[12:13], v[96:97], v[14:15] op_sel_hi:[0,1,1]
	v_pk_fma_f32 v[14:15], v[2:3], 0.5, v[98:99] op_sel_hi:[1,0,1] neg_lo:[0,0,1] neg_hi:[0,0,1]
	v_lshlrev_b64 v[98:99], 1, v[88:89]
	v_pk_fma_f32 v[12:13], v[12:13], 0.5, v[100:101] op_sel_hi:[1,0,1] neg_lo:[0,0,1] neg_hi:[0,0,1]
	v_lshl_add_u64 v[236:237], s[22:23], 0, v[98:99]
	global_load_dwordx2 v[236:237], v[236:237], off offset:512
	v_lshl_add_u64 v[238:239], s[20:21], 0, v[98:99]
	global_load_dwordx2 v[238:239], v[238:239], off offset:512
	v_lshl_add_u64 v[100:101], s[22:23], 0, v[98:99]
	s_nop 0
	ds_read_b128 v[0:3], v0
	v_pk_fma_f32 v[90:91], s[54:55], v[106:107], v[114:115] op_sel_hi:[0,1,1] neg_lo:[0,0,1] neg_hi:[0,0,1]
	v_pk_fma_f32 v[96:97], s[54:55], v[108:109], v[112:113] op_sel_hi:[0,1,1] neg_lo:[0,0,1] neg_hi:[0,0,1]
	s_nop 0
	s_waitcnt vmcnt(1)
	v_lshlrev_b32_e32 v102, 16, v236
	v_and_b32_e32 v103, 0xffff0000, v236
	v_lshlrev_b32_e32 v88, 16, v237
	v_and_b32_e32 v89, 0xffff0000, v237
	s_waitcnt lgkmcnt(0)
	v_pk_fma_f32 v[90:91], v[0:1], v[90:91], v[102:103]
	v_lshl_add_u64 v[102:103], s[20:21], 0, v[98:99]
	v_pk_fma_f32 v[88:89], v[2:3], v[96:97], v[88:89]
	s_nop 0
	s_nop 0
	s_waitcnt vmcnt(0)
	v_lshlrev_b32_e32 v98, 16, v238
	v_and_b32_e32 v99, 0xffff0000, v238
	v_lshlrev_b32_e32 v96, 16, v239
	v_and_b32_e32 v97, 0xffff0000, v239
	v_pk_fma_f32 v[98:99], v[0:1], v[12:13], v[98:99]
	v_cvt_pk_bf16_f32 v0, v90, v91
	v_cvt_pk_bf16_f32 v1, v88, v89
	v_pk_fma_f32 v[96:97], v[2:3], v[14:15], v[96:97]
	v_cvt_pk_bf16_f32 v2, v98, v99
	s_nop 0
	v_cvt_pk_bf16_f32 v3, v96, v97
	global_store_dwordx2 v[100:101], v[0:1], off offset:512
	global_store_dwordx2 v[102:103], v[2:3], off offset:512
	v_mov_b32_e32 v0, v21
	s_nop 0
	v_lshlrev_b32_e32 v100, 2, v0
	v_add_u32_e32 v102, 0x200, v100
	v_ashrrev_i32_e32 v103, 31, v102
	v_lshlrev_b64 v[14:15], 1, v[102:103]
	v_lshl_add_u64 v[236:237], vcc, 0, v[14:15]
	global_load_dwordx2 v[236:237], v[236:237], off
	v_lshl_add_u64 v[238:239], s[52:53], 0, v[14:15]
	global_load_dwordx2 v[238:239], v[238:239], off
	v_lshl_add_u64 v[240:241], s[50:51], 0, v[14:15]
	global_load_dwordx2 v[240:241], v[240:241], off
	v_lshl_add_u64 v[242:243], s[26:27], 0, v[14:15]
	global_load_dwordx2 v[242:243], v[242:243], off
	v_lshl_add_u64 v[244:245], s[24:25], 0, v[14:15]
	global_load_dwordx2 v[244:245], v[244:245], off
	s_nop 0
	s_nop 0
	ds_read_b128 v[0:3], v27 offset:48
	ds_read_b32 v12, v27 offset:64
	s_nop 0
	s_nop 0
	s_nop 0
	v_ashrrev_i32_e32 v101, 31, v100
	s_nop 0
	s_nop 0
	s_waitcnt vmcnt(3)
	v_lshlrev_b32_e32 v114, 16, v238
	v_and_b32_e32 v115, 0xffff0000, v238
	v_lshlrev_b32_e32 v112, 16, v239
	v_and_b32_e32 v113, 0xffff0000, v239
	s_waitcnt lgkmcnt(1)
	v_pk_fma_f32 v[118:119], v[0:1], v[112:113], 0 op_sel_hi:[0,1,0]
	s_nop 0
	s_waitcnt vmcnt(2)
	v_lshlrev_b32_e32 v122, 16, v240
	v_and_b32_e32 v123, 0xffff0000, v240
	v_lshlrev_b32_e32 v120, 16, v241
	v_and_b32_e32 v121, 0xffff0000, v241
	v_pk_fma_f32 v[118:119], v[0:1], v[120:121], v[118:119] op_sel:[1,0,0]
	s_nop 0
	s_nop 0
	s_nop 0
	s_nop 0
	v_pk_fma_f32 v[116:117], v[0:1], v[114:115], 0 op_sel_hi:[0,1,0]
	v_pk_fma_f32 v[116:117], v[0:1], v[122:123], v[116:117] op_sel:[1,0,0]
	v_lshlrev_b32_e32 v106, 16, v236
	v_and_b32_e32 v107, 0xffff0000, v236
	v_lshlrev_b32_e32 v104, 16, v237
	v_and_b32_e32 v105, 0xffff0000, v237
	s_waitcnt lgkmcnt(0)
	v_pk_mul_f32 v[108:109], v[12:13], v[104:105] op_sel_hi:[0,1]
	v_pk_mul_f32 v[110:111], v[12:13], v[106:107] op_sel_hi:[0,1]
	s_nop 0
	s_waitcnt vmcnt(1)
	v_lshlrev_b32_e32 v122, 16, v242
	v_and_b32_e32 v123, 0xffff0000, v242
	v_lshlrev_b32_e32 v120, 16, v243
	v_and_b32_e32 v121, 0xffff0000, v243
	v_pk_fma_f32 v[116:117], v[2:3], v[122:123], v[116:117] op_sel_hi:[0,1,1]
	v_pk_fma_f32 v[118:119], v[2:3], v[120:121], v[118:119] op_sel_hi:[0,1,1]
	s_nop 0
	s_waitcnt vmcnt(0)
	v_lshlrev_b32_e32 v120, 16, v244
	v_and_b32_e32 v121, 0xffff0000, v244
	v_lshlrev_b32_e32 v14, 16, v245
	v_and_b32_e32 v15, 0xffff0000, v245
	v_mov_b32_e32 v2, v3
	v_pk_mul_f32 v[122:123], v[2:3], v[14:15] op_sel_hi:[0,1]
	v_pk_mul_f32 v[124:125], v[2:3], v[120:121] op_sel_hi:[0,1]
	v_pk_fma_f32 v[118:119], v[2:3], v[14:15], v[118:119] op_sel_hi:[0,1,1]
	v_pk_fma_f32 v[2:3], v[2:3], v[120:121], v[116:117] op_sel_hi:[0,1,1]
	v_pk_fma_f32 v[14:15], v[0:1], v[114:115], v[2:3] op_sel_hi:[0,1,1] neg_lo:[1,0,0] neg_hi:[1,0,0]
	v_pk_fma_f32 v[0:1], v[0:1], v[112:113], v[118:119] op_sel_hi:[0,1,1] neg_lo:[1,0,0] neg_hi:[1,0,0]
	v_pk_fma_f32 v[0:1], v[12:13], v[104:105], v[0:1] op_sel_hi:[0,1,1]
	v_pk_fma_f32 v[12:13], v[12:13], v[106:107], v[14:15] op_sel_hi:[0,1,1]
	v_pk_fma_f32 v[12:13], v[6:7], v[12:13], v[110:111] op_sel_hi:[0,1,1] neg_lo:[0,0,1] neg_hi:[0,0,1]
	v_lshlrev_b64 v[110:111], 1, v[100:101]
	v_pk_fma_f32 v[14:15], v[6:7], v[0:1], v[108:109] op_sel_hi:[0,1,1] neg_lo:[0,0,1] neg_hi:[0,0,1]
	v_lshl_add_u64 v[108:109], s[22:23], 0, v[110:111]
	global_load_dwordx2 v[100:101], v[108:109], off offset:1024
	v_lshl_add_u32 v0, v102, 2, s17
	v_pk_fma_f32 v[104:105], v[4:5], v[2:3], v[124:125] op_sel_hi:[0,1,1] neg_lo:[0,0,1] neg_hi:[0,0,1]
	ds_read_b128 v[0:3], v0
	v_lshl_add_u64 v[110:111], s[20:21], 0, v[110:111]
	v_pk_fma_f32 v[106:107], v[4:5], v[118:119], v[122:123] op_sel_hi:[0,1,1] neg_lo:[0,0,1] neg_hi:[0,0,1]
	s_nop 0
	s_waitcnt vmcnt(0)
	v_lshlrev_b32_e32 v102, 16, v100
	v_and_b32_e32 v103, 0xffff0000, v100
	s_waitcnt lgkmcnt(0)
	v_pk_fma_f32 v[102:103], v[0:1], v[104:105], v[102:103]
	global_load_dwordx2 v[104:105], v[110:111], off offset:1024
	v_lshlrev_b32_e32 v100, 16, v101
	v_and_b32_e32 v101, 0xffff0000, v101
	v_pk_fma_f32 v[100:101], v[2:3], v[106:107], v[100:101]
	s_nop 0
	s_waitcnt vmcnt(0)
	v_lshlrev_b32_e32 v106, 16, v104
	v_and_b32_e32 v107, 0xffff0000, v104
	v_lshlrev_b32_e32 v104, 16, v105
	v_and_b32_e32 v105, 0xffff0000, v105
	v_pk_fma_f32 v[106:107], v[0:1], v[12:13], v[106:107]
	v_cvt_pk_bf16_f32 v0, v102, v103
	v_cvt_pk_bf16_f32 v1, v100, v101
	v_pk_fma_f32 v[104:105], v[2:3], v[14:15], v[104:105]
	v_cvt_pk_bf16_f32 v2, v106, v107
	s_nop 0
	v_cvt_pk_bf16_f32 v3, v104, v105
	global_store_dwordx2 v[108:109], v[0:1], off offset:1024
	global_store_dwordx2 v[110:111], v[2:3], off offset:1024
	v_mov_b32_e32 v0, v21
	s_nop 0
	v_lshlrev_b32_e32 v14, 2, v0
	v_add_u32_e32 v108, 0x300, v14
	v_ashrrev_i32_e32 v109, 31, v108
	v_lshlrev_b64 v[110:111], 1, v[108:109]
	v_lshl_add_u64 v[236:237], vcc, 0, v[110:111]
	global_load_dwordx2 v[236:237], v[236:237], off
	v_lshl_add_u64 v[238:239], s[52:53], 0, v[110:111]
	global_load_dwordx2 v[238:239], v[238:239], off
	v_lshl_add_u64 v[240:241], s[50:51], 0, v[110:111]
	global_load_dwordx2 v[240:241], v[240:241], off
	v_lshl_add_u64 v[242:243], s[26:27], 0, v[110:111]
	global_load_dwordx2 v[242:243], v[242:243], off
	v_lshl_add_u64 v[244:245], s[24:25], 0, v[110:111]
	global_load_dwordx2 v[244:245], v[244:245], off
	s_nop 0
	s_nop 0
	ds_read_b128 v[0:3], v27 offset:48
	ds_read_b32 v12, v27 offset:64
	s_nop 0
	s_nop 0
	s_nop 0
	v_ashrrev_i32_e32 v15, 31, v14
	s_nop 0
	v_lshlrev_b64 v[14:15], 1, v[14:15]
	s_nop 0
	s_waitcnt vmcnt(3)
	v_lshlrev_b32_e32 v122, 16, v238
	v_and_b32_e32 v123, 0xffff0000, v238
	v_lshlrev_b32_e32 v120, 16, v239
	v_and_b32_e32 v121, 0xffff0000, v239
	s_waitcnt lgkmcnt(1)
	v_pk_fma_f32 v[126:127], v[0:1], v[120:121], 0 op_sel_hi:[0,1,0]
	s_nop 0
	s_waitcnt vmcnt(2)
	v_lshlrev_b32_e32 v130, 16, v240
	v_and_b32_e32 v131, 0xffff0000, v240
	v_lshlrev_b32_e32 v128, 16, v241
	v_and_b32_e32 v129, 0xffff0000, v241
	v_pk_fma_f32 v[126:127], v[0:1], v[128:129], v[126:127] op_sel:[1,0,0]
	s_nop 0
	s_nop 0
	s_nop 0
	s_nop 0
	v_pk_fma_f32 v[124:125], v[0:1], v[122:123], 0 op_sel_hi:[0,1,0]
	v_pk_fma_f32 v[124:125], v[0:1], v[130:131], v[124:125] op_sel:[1,0,0]
	v_lshlrev_b32_e32 v114, 16, v236
	v_and_b32_e32 v115, 0xffff0000, v236
	v_lshlrev_b32_e32 v112, 16, v237
	v_and_b32_e32 v113, 0xffff0000, v237
	s_waitcnt lgkmcnt(0)
	v_pk_mul_f32 v[116:117], v[12:13], v[112:113] op_sel_hi:[0,1]
	v_pk_mul_f32 v[118:119], v[12:13], v[114:115] op_sel_hi:[0,1]
	s_nop 0
	s_waitcnt vmcnt(1)
	v_lshlrev_b32_e32 v130, 16, v242
	v_and_b32_e32 v131, 0xffff0000, v242
	v_lshlrev_b32_e32 v128, 16, v243
	v_and_b32_e32 v129, 0xffff0000, v243
	v_pk_fma_f32 v[124:125], v[2:3], v[130:131], v[124:125] op_sel_hi:[0,1,1]
	v_pk_fma_f32 v[126:127], v[2:3], v[128:129], v[126:127] op_sel_hi:[0,1,1]
	s_nop 0
	s_waitcnt vmcnt(0)
	v_lshlrev_b32_e32 v128, 16, v244
	v_and_b32_e32 v129, 0xffff0000, v244
	v_lshlrev_b32_e32 v110, 16, v245
	v_and_b32_e32 v111, 0xffff0000, v245
	v_mov_b32_e32 v2, v3
	v_pk_mul_f32 v[130:131], v[2:3], v[110:111] op_sel_hi:[0,1]
	v_pk_mul_f32 v[132:133], v[2:3], v[128:129] op_sel_hi:[0,1]
	v_pk_fma_f32 v[110:111], v[2:3], v[110:111], v[126:127] op_sel_hi:[0,1,1]
	v_pk_fma_f32 v[2:3], v[2:3], v[128:129], v[124:125] op_sel_hi:[0,1,1]
	v_pk_fma_f32 v[122:123], v[0:1], v[122:123], v[2:3] op_sel_hi:[0,1,1] neg_lo:[1,0,0] neg_hi:[1,0,0]
	v_pk_fma_f32 v[0:1], v[0:1], v[120:121], v[110:111] op_sel_hi:[0,1,1] neg_lo:[1,0,0] neg_hi:[1,0,0]
	v_pk_fma_f32 v[0:1], v[12:13], v[112:113], v[0:1] op_sel_hi:[0,1,1]
	v_pk_fma_f32 v[12:13], v[12:13], v[114:115], v[122:123] op_sel_hi:[0,1,1]
	v_pk_fma_f32 v[112:113], v[4:5], v[2:3], v[132:133] op_sel_hi:[0,1,1] neg_lo:[0,0,1] neg_hi:[0,0,1]
	v_pk_fma_f32 v[110:111], v[4:5], v[110:111], v[130:131] op_sel_hi:[0,1,1] neg_lo:[0,0,1] neg_hi:[0,0,1]
	v_lshl_add_u64 v[4:5], s[22:23], 0, v[14:15]
	v_pk_fma_f32 v[12:13], v[6:7], v[12:13], v[118:119] op_sel_hi:[0,1,1] neg_lo:[0,0,1] neg_hi:[0,0,1]
	v_pk_fma_f32 v[6:7], v[6:7], v[0:1], v[116:117] op_sel_hi:[0,1,1] neg_lo:[0,0,1] neg_hi:[0,0,1]
	v_lshl_add_u32 v0, v108, 2, s17
	global_load_dwordx2 v[108:109], v[4:5], off offset:1536
	ds_read_b128 v[0:3], v0
	v_lshl_add_u64 v[14:15], s[20:21], 0, v[14:15]
	s_nop 0
	s_waitcnt vmcnt(0)
	v_lshlrev_b32_e32 v114, 16, v108
	v_and_b32_e32 v115, 0xffff0000, v108
	v_lshlrev_b32_e32 v108, 16, v109
	v_and_b32_e32 v109, 0xffff0000, v109
	s_waitcnt lgkmcnt(0)
	v_pk_fma_f32 v[108:109], v[2:3], v[110:111], v[108:109]
	v_pk_fma_f32 v[110:111], v[0:1], v[112:113], v[114:115]
	global_load_dwordx2 v[112:113], v[14:15], off offset:1536
	s_nop 0
	s_waitcnt vmcnt(0)
	v_lshlrev_b32_e32 v114, 16, v112
	v_and_b32_e32 v115, 0xffff0000, v112
	v_lshlrev_b32_e32 v112, 16, v113
	v_and_b32_e32 v113, 0xffff0000, v113
	v_pk_fma_f32 v[114:115], v[0:1], v[12:13], v[114:115]
	v_cvt_pk_bf16_f32 v0, v110, v111
	v_cvt_pk_bf16_f32 v1, v108, v109
	v_pk_fma_f32 v[112:113], v[2:3], v[6:7], v[112:113]
	v_cvt_pk_bf16_f32 v2, v114, v115
	s_nop 0
	v_cvt_pk_bf16_f32 v3, v112, v113
	global_store_dwordx2 v[4:5], v[0:1], off offset:1536
	global_store_dwordx2 v[14:15], v[2:3], off offset:1536
	v_mov_b32_e32 v0, v21
	s_add_u32 s0, s92, s0
	v_lshlrev_b32_e32 v12, 2, v0
	v_add_u32_e32 v14, 0x400, v12
	v_ashrrev_i32_e32 v15, 31, v14
	s_addc_u32 s1, s93, s1
	v_lshlrev_b64 v[126:127], 1, v[14:15]
	s_add_u32 s42, s92, s42
	v_lshl_add_u64 v[128:129], s[0:1], 0, v[126:127]
	s_addc_u32 s43, s93, s43
	ds_read_b128 v[0:3], v27 offset:32
	ds_read_b128 v[4:7], v27 offset:48
	ds_read_b32 v116, v27 offset:64
	global_load_dwordx2 v[130:131], v[128:129], off
	v_lshl_add_u64 v[238:239], s[42:43], 0, v[126:127]
	global_load_dwordx2 v[238:239], v[238:239], off
	v_lshl_add_u64 v[240:241], vcc, 0, v[126:127]
	global_load_dwordx2 v[240:241], v[240:241], off
	s_nop 0
	s_nop 0
	s_add_u32 s2, s92, s2
	s_addc_u32 s3, s93, s3
	s_add_u32 s36, s92, s36
	s_addc_u32 s37, s93, s37
	v_lshl_add_u64 v[118:119], vcc, 0, v[126:127]
	s_nop 0
	v_ashrrev_i32_e32 v13, 31, v12
	s_add_u32 s76, s92, s76
	s_addc_u32 s77, s93, s77
	s_add_u32 s10, s92, s10
	s_addc_u32 s11, s93, s11
	s_add_u32 s8, s92, s8
	s_addc_u32 s9, s93, s9
	s_add_u32 s44, s92, s44
	s_addc_u32 s45, s93, s45
	s_add_u32 s48, s92, s48
	s_addc_u32 s49, s93, s49
	s_add_u32 s46, s92, s46
	s_addc_u32 s47, s93, s47
	s_add_u32 s30, s92, s30
	s_addc_u32 s31, s93, s31
	s_add_u32 s28, s92, s28
	s_addc_u32 s29, s93, s29
	s_nop 0
	s_waitcnt vmcnt(2)
	v_lshlrev_b32_e32 v128, 16, v130
	v_and_b32_e32 v129, 0xffff0000, v130
	v_lshlrev_b32_e32 v130, 16, v131
	v_and_b32_e32 v131, 0xffff0000, v131
	s_waitcnt lgkmcnt(2)
	v_pk_fma_f32 v[134:135], v[0:1], v[130:131], 0 op_sel_hi:[0,1,0]
	s_nop 0
	s_waitcnt vmcnt(1)
	v_lshlrev_b32_e32 v138, 16, v238
	v_and_b32_e32 v139, 0xffff0000, v238
	v_lshlrev_b32_e32 v136, 16, v239
	v_and_b32_e32 v137, 0xffff0000, v239
	v_pk_fma_f32 v[134:135], v[0:1], v[136:137], v[134:135] op_sel:[1,0,0]
	v_lshl_add_u64 v[236:237], s[2:3], 0, v[126:127]
	global_load_dwordx2 v[236:237], v[236:237], off
	v_lshl_add_u64 v[238:239], s[36:37], 0, v[126:127]
	global_load_dwordx2 v[238:239], v[238:239], off
	v_lshl_add_u64 v[242:243], s[52:53], 0, v[126:127]
	global_load_dwordx2 v[242:243], v[242:243], off
	v_lshl_add_u64 v[244:245], s[50:51], 0, v[126:127]
	global_load_dwordx2 v[244:245], v[244:245], off
	v_lshl_add_u64 v[246:247], s[24:25], 0, v[126:127]
	global_load_dwordx2 v[246:247], v[246:247], off
	v_lshl_add_u64 v[230:231], s[26:27], 0, v[126:127]
	global_load_dwordx2 v[230:231], v[230:231], off
	s_nop 0
	s_nop 0
	v_pk_fma_f32 v[132:133], v[0:1], v[128:129], 0 op_sel_hi:[0,1,0]
	v_pk_fma_f32 v[132:133], v[0:1], v[138:139], v[132:133] op_sel:[1,0,0]
	s_nop 0
	s_waitcnt vmcnt(5)
	v_lshlrev_b32_e32 v138, 16, v236
	v_and_b32_e32 v139, 0xffff0000, v236
	v_lshlrev_b32_e32 v136, 16, v237
	v_and_b32_e32 v137, 0xffff0000, v237
	v_pk_fma_f32 v[134:135], v[2:3], v[136:137], v[134:135] op_sel_hi:[0,1,1]
	s_nop 0
	s_nop 0
	v_pk_fma_f32 v[132:133], v[2:3], v[138:139], v[132:133] op_sel_hi:[0,1,1]
	v_mov_b32_e32 v2, v3
	s_nop 0
	s_waitcnt vmcnt(4)
	v_lshlrev_b32_e32 v138, 16, v238
	v_and_b32_e32 v139, 0xffff0000, v238
	v_lshlrev_b32_e32 v136, 16, v239
	v_and_b32_e32 v137, 0xffff0000, v239
	v_pk_fma_f32 v[134:135], v[2:3], v[136:137], v[134:135] op_sel_hi:[0,1,1]
	v_pk_fma_f32 v[2:3], v[2:3], v[138:139], v[132:133] op_sel_hi:[0,1,1]
	s_nop 0
	s_nop 0
	s_nop 0
	s_waitcnt vmcnt(3)
	v_lshlrev_b32_e32 v136, 16, v242
	v_and_b32_e32 v137, 0xffff0000, v242
	v_lshlrev_b32_e32 v132, 16, v243
	v_and_b32_e32 v133, 0xffff0000, v243
	s_waitcnt lgkmcnt(1)
	v_pk_fma_f32 v[132:133], v[4:5], v[132:133], v[134:135] op_sel_hi:[0,1,1]
	s_nop 0
	s_nop 0
	v_pk_fma_f32 v[2:3], v[4:5], v[136:137], v[2:3] op_sel_hi:[0,1,1]
	s_nop 0
	s_waitcnt vmcnt(2)
	v_lshlrev_b32_e32 v136, 16, v244
	v_and_b32_e32 v137, 0xffff0000, v244
	v_lshlrev_b32_e32 v134, 16, v245
	v_and_b32_e32 v135, 0xffff0000, v245
	v_pk_fma_f32 v[132:133], v[4:5], v[134:135], v[132:133] op_sel:[1,0,0]
	v_pk_fma_f32 v[2:3], v[4:5], v[136:137], v[2:3] op_sel:[1,0,0]
	s_nop 0
	s_nop 0
	s_nop 0
	s_nop 0
	s_nop 0
	v_lshlrev_b32_e32 v122, 16, v241
	v_and_b32_e32 v123, 0xffff0000, v241
	v_lshlrev_b32_e32 v118, 16, v240
	v_and_b32_e32 v119, 0xffff0000, v240
	s_waitcnt lgkmcnt(0)
	v_pk_mul_f32 v[120:121], v[116:117], v[122:123] op_sel_hi:[0,1]
	v_pk_mul_f32 v[124:125], v[116:117], v[118:119] op_sel_hi:[0,1]
	s_nop 0
	s_waitcnt vmcnt(0)
	v_lshlrev_b32_e32 v134, 16, v230
	v_and_b32_e32 v135, 0xffff0000, v230
	v_lshlrev_b32_e32 v4, 16, v231
	v_and_b32_e32 v5, 0xffff0000, v231
	v_pk_fma_f32 v[2:3], v[6:7], v[134:135], v[2:3] op_sel_hi:[0,1,1]
	v_pk_fma_f32 v[4:5], v[6:7], v[4:5], v[132:133] op_sel_hi:[0,1,1]
	v_lshlrev_b32_e32 v132, 16, v246
	v_and_b32_e32 v133, 0xffff0000, v246
	v_lshlrev_b32_e32 v126, 16, v247
	v_and_b32_e32 v127, 0xffff0000, v247
	v_mov_b32_e32 v6, v7
	v_pk_mul_f32 v[134:135], v[6:7], v[126:127] op_sel_hi:[0,1]
	v_pk_fma_f32 v[126:127], v[6:7], v[126:127], v[4:5] op_sel_hi:[0,1,1]
	v_pk_fma_f32 v[2:3], v[6:7], v[132:133], v[2:3] op_sel_hi:[0,1,1]
	v_pk_fma_f32 v[4:5], v[0:1], v[128:129], v[2:3] op_sel_hi:[0,1,1] neg_lo:[1,0,0] neg_hi:[1,0,0]
	v_pk_fma_f32 v[0:1], v[0:1], v[130:131], v[126:127] op_sel_hi:[0,1,1] neg_lo:[1,0,0] neg_hi:[1,0,0]
	v_pk_fma_f32 v[0:1], v[116:117], v[122:123], v[0:1] op_sel_hi:[0,1,1]
	v_pk_mul_f32 v[136:137], v[6:7], v[132:133] op_sel_hi:[0,1]
	v_pk_fma_f32 v[6:7], v[10:11], v[0:1], v[120:121] op_sel_hi:[0,1,1] neg_lo:[0,0,1] neg_hi:[0,0,1]
	v_lshl_add_u32 v0, v14, 2, s17
	v_lshlrev_b64 v[14:15], 1, v[12:13]
	v_lshl_add_u64 v[12:13], s[22:23], 0, v[14:15]
	global_load_dwordx2 v[120:121], v[12:13], off offset:2048
	v_pk_fma_f32 v[4:5], v[116:117], v[118:119], v[4:5] op_sel_hi:[0,1,1]
	v_pk_fma_f32 v[118:119], v[8:9], v[2:3], v[136:137] op_sel_hi:[0,1,1] neg_lo:[0,0,1] neg_hi:[0,0,1]
	ds_read_b128 v[0:3], v0
	v_pk_fma_f32 v[116:117], v[8:9], v[126:127], v[134:135] op_sel_hi:[0,1,1] neg_lo:[0,0,1] neg_hi:[0,0,1]
	v_lshl_add_u64 v[14:15], s[20:21], 0, v[14:15]
	v_pk_fma_f32 v[4:5], v[10:11], v[4:5], v[124:125] op_sel_hi:[0,1,1] neg_lo:[0,0,1] neg_hi:[0,0,1]
	s_nop 0
	s_waitcnt vmcnt(0)
	v_lshlrev_b32_e32 v122, 16, v120
	v_and_b32_e32 v123, 0xffff0000, v120
	v_lshlrev_b32_e32 v120, 16, v121
	v_and_b32_e32 v121, 0xffff0000, v121
	s_waitcnt lgkmcnt(0)
	v_pk_fma_f32 v[116:117], v[2:3], v[116:117], v[120:121]
	global_load_dwordx2 v[120:121], v[14:15], off offset:2048
	v_pk_fma_f32 v[118:119], v[0:1], v[118:119], v[122:123]
	s_nop 0
	s_waitcnt vmcnt(0)
	v_lshlrev_b32_e32 v122, 16, v120
	v_and_b32_e32 v123, 0xffff0000, v120
	v_lshlrev_b32_e32 v120, 16, v121
	v_and_b32_e32 v121, 0xffff0000, v121
	v_pk_fma_f32 v[122:123], v[0:1], v[4:5], v[122:123]
	v_cvt_pk_bf16_f32 v0, v118, v119
	v_cvt_pk_bf16_f32 v1, v116, v117
	v_pk_fma_f32 v[120:121], v[2:3], v[6:7], v[120:121]
	v_cvt_pk_bf16_f32 v2, v122, v123
	s_nop 0
	v_cvt_pk_bf16_f32 v3, v120, v121
	global_store_dwordx2 v[12:13], v[0:1], off offset:2048
	global_store_dwordx2 v[14:15], v[2:3], off offset:2048
	v_mov_b32_e32 v0, v21
	s_nop 0
	v_lshlrev_b32_e32 v12, 2, v0
	v_add_u32_e32 v14, 0x500, v12
	v_ashrrev_i32_e32 v15, 31, v14
	v_lshlrev_b64 v[134:135], 1, v[14:15]
	v_lshl_add_u64 v[236:237], s[0:1], 0, v[134:135]
	global_load_dwordx2 v[236:237], v[236:237], off
	v_lshl_add_u64 v[238:239], s[42:43], 0, v[134:135]
	global_load_dwordx2 v[238:239], v[238:239], off
	v_lshl_add_u64 v[240:241], vcc, 0, v[134:135]
	global_load_dwordx2 v[240:241], v[240:241], off
	v_lshl_add_u64 v[242:243], s[2:3], 0, v[134:135]
	global_load_dwordx2 v[242:243], v[242:243], off
	v_lshl_add_u64 v[244:245], s[36:37], 0, v[134:135]
	global_load_dwordx2 v[244:245], v[244:245], off
	v_lshl_add_u64 v[246:247], s[52:53], 0, v[134:135]
	global_load_dwordx2 v[246:247], v[246:247], off
	v_lshl_add_u64 v[230:231], s[50:51], 0, v[134:135]
	global_load_dwordx2 v[230:231], v[230:231], off
	v_lshl_add_u64 v[232:233], s[24:25], 0, v[134:135]
	global_load_dwordx2 v[232:233], v[232:233], off
	v_lshl_add_u64 v[234:235], s[26:27], 0, v[134:135]
	global_load_dwordx2 v[234:235], v[234:235], off
	v_lshl_add_u64 v[136:137], s[0:1], 0, v[134:135]
	ds_read_b128 v[0:3], v27 offset:32
	ds_read_b128 v[4:7], v27 offset:48
	ds_read_b32 v124, v27 offset:64
	s_nop 0
	s_nop 0
	s_nop 0
	v_lshl_add_u64 v[126:127], vcc, 0, v[134:135]
	s_nop 0
	v_ashrrev_i32_e32 v13, 31, v12
	v_lshlrev_b64 v[12:13], 1, v[12:13]
	s_nop 0
	s_waitcnt vmcnt(8)
	v_lshlrev_b32_e32 v136, 16, v236
	v_and_b32_e32 v137, 0xffff0000, v236
	v_lshlrev_b32_e32 v138, 16, v237
	v_and_b32_e32 v139, 0xffff0000, v237
	s_waitcnt lgkmcnt(2)
	v_pk_fma_f32 v[142:143], v[0:1], v[138:139], 0 op_sel_hi:[0,1,0]
	s_nop 0
	s_waitcnt vmcnt(7)
	v_lshlrev_b32_e32 v146, 16, v238
	v_and_b32_e32 v147, 0xffff0000, v238
	v_lshlrev_b32_e32 v144, 16, v239
	v_and_b32_e32 v145, 0xffff0000, v239
	v_pk_fma_f32 v[142:143], v[0:1], v[144:145], v[142:143] op_sel:[1,0,0]
	s_nop 0
	s_nop 0
	v_pk_fma_f32 v[140:141], v[0:1], v[136:137], 0 op_sel_hi:[0,1,0]
	v_pk_fma_f32 v[140:141], v[0:1], v[146:147], v[140:141] op_sel:[1,0,0]
	s_nop 0
	s_waitcnt vmcnt(5)
	v_lshlrev_b32_e32 v146, 16, v242
	v_and_b32_e32 v147, 0xffff0000, v242
	v_lshlrev_b32_e32 v144, 16, v243
	v_and_b32_e32 v145, 0xffff0000, v243
	v_pk_fma_f32 v[142:143], v[2:3], v[144:145], v[142:143] op_sel_hi:[0,1,1]
	s_nop 0
	s_nop 0
	v_pk_fma_f32 v[140:141], v[2:3], v[146:147], v[140:141] op_sel_hi:[0,1,1]
	v_mov_b32_e32 v2, v3
	s_nop 0
	s_waitcnt vmcnt(4)
	v_lshlrev_b32_e32 v146, 16, v244
	v_and_b32_e32 v147, 0xffff0000, v244
	v_lshlrev_b32_e32 v144, 16, v245
	v_and_b32_e32 v145, 0xffff0000, v245
	v_pk_fma_f32 v[142:143], v[2:3], v[144:145], v[142:143] op_sel_hi:[0,1,1]
	v_pk_fma_f32 v[2:3], v[2:3], v[146:147], v[140:141] op_sel_hi:[0,1,1]
	s_nop 0
	s_nop 0
	s_nop 0
	s_waitcnt vmcnt(3)
	v_lshlrev_b32_e32 v144, 16, v246
	v_and_b32_e32 v145, 0xffff0000, v246
	v_lshlrev_b32_e32 v140, 16, v247
	v_and_b32_e32 v141, 0xffff0000, v247
	s_waitcnt lgkmcnt(1)
	v_pk_fma_f32 v[140:141], v[4:5], v[140:141], v[142:143] op_sel_hi:[0,1,1]
	s_nop 0
	s_nop 0
	v_pk_fma_f32 v[2:3], v[4:5], v[144:145], v[2:3] op_sel_hi:[0,1,1]
	s_nop 0
	s_waitcnt vmcnt(2)
	v_lshlrev_b32_e32 v144, 16, v230
	v_and_b32_e32 v145, 0xffff0000, v230
	v_lshlrev_b32_e32 v142, 16, v231
	v_and_b32_e32 v143, 0xffff0000, v231
	v_pk_fma_f32 v[140:141], v[4:5], v[142:143], v[140:141] op_sel:[1,0,0]
	v_pk_fma_f32 v[2:3], v[4:5], v[144:145], v[2:3] op_sel:[1,0,0]
	s_nop 0
	s_nop 0
	s_nop 0
	s_nop 0
	s_nop 0
	v_lshlrev_b32_e32 v126, 16, v240
	v_and_b32_e32 v127, 0xffff0000, v240
	v_lshlrev_b32_e32 v130, 16, v241
	v_and_b32_e32 v131, 0xffff0000, v241
	s_waitcnt lgkmcnt(0)
	v_pk_mul_f32 v[128:129], v[124:125], v[130:131] op_sel_hi:[0,1]
	v_pk_mul_f32 v[132:133], v[124:125], v[126:127] op_sel_hi:[0,1]
	s_nop 0
	s_waitcnt vmcnt(0)
	v_lshlrev_b32_e32 v142, 16, v234
	v_and_b32_e32 v143, 0xffff0000, v234
	v_lshlrev_b32_e32 v4, 16, v235
	v_and_b32_e32 v5, 0xffff0000, v235
	v_pk_fma_f32 v[2:3], v[6:7], v[142:143], v[2:3] op_sel_hi:[0,1,1]
	v_pk_fma_f32 v[4:5], v[6:7], v[4:5], v[140:141] op_sel_hi:[0,1,1]
	v_lshlrev_b32_e32 v140, 16, v232
	v_and_b32_e32 v141, 0xffff0000, v232
	v_lshlrev_b32_e32 v134, 16, v233
	v_and_b32_e32 v135, 0xffff0000, v233
	v_mov_b32_e32 v6, v7
	v_pk_mul_f32 v[142:143], v[6:7], v[134:135] op_sel_hi:[0,1]
	v_pk_fma_f32 v[134:135], v[6:7], v[134:135], v[4:5] op_sel_hi:[0,1,1]
	v_pk_fma_f32 v[2:3], v[6:7], v[140:141], v[2:3] op_sel_hi:[0,1,1]
	v_pk_fma_f32 v[4:5], v[0:1], v[136:137], v[2:3] op_sel_hi:[0,1,1] neg_lo:[1,0,0] neg_hi:[1,0,0]
	v_pk_fma_f32 v[0:1], v[0:1], v[138:139], v[134:135] op_sel_hi:[0,1,1] neg_lo:[1,0,0] neg_hi:[1,0,0]
	v_pk_mul_f32 v[144:145], v[6:7], v[140:141] op_sel_hi:[0,1]
	v_pk_fma_f32 v[0:1], v[124:125], v[130:131], v[0:1] op_sel_hi:[0,1,1]
	v_pk_fma_f32 v[4:5], v[124:125], v[126:127], v[4:5] op_sel_hi:[0,1,1]
	v_pk_fma_f32 v[4:5], v[10:11], v[4:5], v[132:133] op_sel_hi:[0,1,1] neg_lo:[0,0,1] neg_hi:[0,0,1]
	v_pk_fma_f32 v[6:7], v[10:11], v[0:1], v[128:129] op_sel_hi:[0,1,1] neg_lo:[0,0,1] neg_hi:[0,0,1]
	v_pk_fma_f32 v[10:11], v[8:9], v[2:3], v[144:145] op_sel_hi:[0,1,1] neg_lo:[0,0,1] neg_hi:[0,0,1]
	v_pk_fma_f32 v[124:125], v[8:9], v[134:135], v[142:143] op_sel_hi:[0,1,1] neg_lo:[0,0,1] neg_hi:[0,0,1]
	v_lshl_add_u64 v[236:237], s[22:23], 0, v[12:13]
	global_load_dwordx2 v[236:237], v[236:237], off offset:2560
	v_lshl_add_u64 v[238:239], s[20:21], 0, v[12:13]
	global_load_dwordx2 v[238:239], v[238:239], off offset:2560
	v_lshl_add_u64 v[8:9], s[22:23], 0, v[12:13]
	v_lshl_add_u32 v0, v14, 2, s17
	s_nop 0
	ds_read_b128 v[0:3], v0
	s_nop 0
	s_waitcnt vmcnt(1)
	v_lshlrev_b32_e32 v126, 16, v236
	v_and_b32_e32 v127, 0xffff0000, v236
	s_waitcnt lgkmcnt(0)
	v_pk_fma_f32 v[126:127], v[0:1], v[10:11], v[126:127]
	v_lshl_add_u64 v[10:11], s[20:21], 0, v[12:13]
	s_nop 0
	v_lshlrev_b32_e32 v14, 16, v237
	v_and_b32_e32 v15, 0xffff0000, v237
	v_pk_fma_f32 v[124:125], v[2:3], v[124:125], v[14:15]
	s_nop 0
	s_waitcnt vmcnt(0)
	v_lshlrev_b32_e32 v14, 16, v238
	v_and_b32_e32 v15, 0xffff0000, v238
	v_lshlrev_b32_e32 v12, 16, v239
	v_and_b32_e32 v13, 0xffff0000, v239
	v_pk_fma_f32 v[130:131], v[0:1], v[4:5], v[14:15]
	v_cvt_pk_bf16_f32 v0, v126, v127
	v_cvt_pk_bf16_f32 v1, v124, v125
	v_pk_fma_f32 v[128:129], v[2:3], v[6:7], v[12:13]
	v_cvt_pk_bf16_f32 v2, v130, v131
	s_nop 0
	v_cvt_pk_bf16_f32 v3, v128, v129
	global_store_dwordx2 v[8:9], v[0:1], off offset:2560
	global_store_dwordx2 v[10:11], v[2:3], off offset:2560
	v_mov_b32_e32 v0, v21
	ds_read_b32 v136, v27 offset:64
	v_lshlrev_b32_e32 v132, 2, v0
	v_add_u32_e32 v134, 0x600, v132
	v_ashrrev_i32_e32 v135, 31, v134
	v_lshlrev_b64 v[146:147], 1, v[134:135]
	v_lshl_add_u64 v[0:1], vcc, 0, v[146:147]
	global_load_dwordx2 v[0:1], v[0:1], off
	v_lshl_add_u64 v[148:149], s[76:77], 0, v[146:147]
	v_lshl_add_u64 v[156:157], s[10:11], 0, v[146:147]
	v_ashrrev_i32_e32 v133, 31, v132
	s_nop 0
	s_waitcnt vmcnt(0)
	v_lshlrev_b32_e32 v138, 16, v0
	v_and_b32_e32 v139, 0xffff0000, v0
	v_lshlrev_b32_e32 v142, 16, v1
	v_and_b32_e32 v143, 0xffff0000, v1
	ds_read_b128 v[0:3], v27
	ds_read_b128 v[12:15], v27 offset:16
	ds_read_b128 v[8:11], v27 offset:32
	ds_read_b128 v[4:7], v27 offset:48
	global_load_dwordx2 v[150:151], v[148:149], off
	s_waitcnt lgkmcnt(4)
	v_pk_mul_f32 v[140:141], v[136:137], v[142:143] op_sel_hi:[0,1]
	global_load_dwordx2 v[156:157], v[156:157], off
	v_pk_mul_f32 v[144:145], v[136:137], v[138:139] op_sel_hi:[0,1]
	s_nop 0
	s_waitcnt vmcnt(1)
	v_lshlrev_b32_e32 v148, 16, v150
	v_and_b32_e32 v149, 0xffff0000, v150
	v_lshlrev_b32_e32 v150, 16, v151
	v_and_b32_e32 v151, 0xffff0000, v151
	s_waitcnt lgkmcnt(3)
	v_pk_fma_f32 v[154:155], v[0:1], v[150:151], 0 op_sel_hi:[0,1,0]
	s_nop 0
	s_waitcnt vmcnt(0)
	v_lshlrev_b32_e32 v158, 16, v156
	v_and_b32_e32 v159, 0xffff0000, v156
	v_lshlrev_b32_e32 v156, 16, v157
	v_and_b32_e32 v157, 0xffff0000, v157
	v_pk_fma_f32 v[154:155], v[0:1], v[156:157], v[154:155] op_sel:[1,0,0]
	v_lshl_add_u64 v[236:237], s[8:9], 0, v[146:147]
	global_load_dwordx2 v[236:237], v[236:237], off
	v_lshl_add_u64 v[238:239], s[44:45], 0, v[146:147]
	global_load_dwordx2 v[238:239], v[238:239], off
	v_lshl_add_u64 v[240:241], s[48:49], 0, v[146:147]
	global_load_dwordx2 v[240:241], v[240:241], off
	v_lshl_add_u64 v[242:243], s[46:47], 0, v[146:147]
	global_load_dwordx2 v[242:243], v[242:243], off
	v_lshl_add_u64 v[244:245], s[30:31], 0, v[146:147]
	global_load_dwordx2 v[244:245], v[244:245], off
	v_lshl_add_u64 v[246:247], s[28:29], 0, v[146:147]
	global_load_dwordx2 v[246:247], v[246:247], off
	v_lshl_add_u64 v[230:231], s[0:1], 0, v[146:147]
	global_load_dwordx2 v[230:231], v[230:231], off
	v_lshl_add_u64 v[232:233], s[42:43], 0, v[146:147]
	global_load_dwordx2 v[232:233], v[232:233], off
	v_lshl_add_u64 v[234:235], s[2:3], 0, v[146:147]
	global_load_dwordx2 v[234:235], v[234:235], off
	s_nop 0
	s_nop 0
	v_pk_fma_f32 v[152:153], v[0:1], v[148:149], 0 op_sel_hi:[0,1,0]
	v_pk_fma_f32 v[152:153], v[0:1], v[158:159], v[152:153] op_sel:[1,0,0]
	s_nop 0
	s_waitcnt vmcnt(8)
	v_lshlrev_b32_e32 v158, 16, v236
	v_and_b32_e32 v159, 0xffff0000, v236
	v_lshlrev_b32_e32 v156, 16, v237
	v_and_b32_e32 v157, 0xffff0000, v237
	v_pk_fma_f32 v[154:155], v[2:3], v[156:157], v[154:155] op_sel_hi:[0,1,1]
	s_nop 0
	s_nop 0
	v_pk_fma_f32 v[152:153], v[2:3], v[158:159], v[152:153] op_sel_hi:[0,1,1]
	v_mov_b32_e32 v2, v3
	s_nop 0
	s_waitcnt vmcnt(7)
	v_lshlrev_b32_e32 v158, 16, v238
	v_and_b32_e32 v159, 0xffff0000, v238
	v_lshlrev_b32_e32 v156, 16, v239
	v_and_b32_e32 v157, 0xffff0000, v239
	v_pk_fma_f32 v[154:155], v[2:3], v[156:157], v[154:155] op_sel_hi:[0,1,1]
	v_pk_fma_f32 v[2:3], v[2:3], v[158:159], v[152:153] op_sel_hi:[0,1,1]
	s_nop 0
	s_nop 0
	s_nop 0
	s_waitcnt vmcnt(6)
	v_lshlrev_b32_e32 v156, 16, v240
	v_and_b32_e32 v157, 0xffff0000, v240
	v_lshlrev_b32_e32 v152, 16, v241
	v_and_b32_e32 v153, 0xffff0000, v241
	s_waitcnt lgkmcnt(2)
	v_pk_fma_f32 v[152:153], v[12:13], v[152:153], v[154:155] op_sel_hi:[0,1,1]
	s_nop 0
	s_nop 0
	v_pk_fma_f32 v[2:3], v[12:13], v[156:157], v[2:3] op_sel_hi:[0,1,1]
	s_nop 0
	s_waitcnt vmcnt(5)
	v_lshlrev_b32_e32 v156, 16, v242
	v_and_b32_e32 v157, 0xffff0000, v242
	v_lshlrev_b32_e32 v154, 16, v243
	v_and_b32_e32 v155, 0xffff0000, v243
	v_pk_fma_f32 v[152:153], v[12:13], v[154:155], v[152:153] op_sel:[1,0,0]
	v_pk_fma_f32 v[2:3], v[12:13], v[156:157], v[2:3] op_sel:[1,0,0]
	s_nop 0
	s_nop 0
	s_nop 0
	s_waitcnt vmcnt(4)
	v_lshlrev_b32_e32 v154, 16, v244
	v_and_b32_e32 v155, 0xffff0000, v244
	v_lshlrev_b32_e32 v12, 16, v245
	v_and_b32_e32 v13, 0xffff0000, v245
	v_pk_fma_f32 v[12:13], v[14:15], v[12:13], v[152:153] op_sel_hi:[0,1,1]
	s_nop 0
	s_nop 0
	v_pk_fma_f32 v[2:3], v[14:15], v[154:155], v[2:3] op_sel_hi:[0,1,1]
	v_mov_b32_e32 v14, v15
	s_nop 0
	s_waitcnt vmcnt(3)
	v_lshlrev_b32_e32 v154, 16, v246
	v_and_b32_e32 v155, 0xffff0000, v246
	v_lshlrev_b32_e32 v152, 16, v247
	v_and_b32_e32 v153, 0xffff0000, v247
	v_pk_fma_f32 v[12:13], v[14:15], v[152:153], v[12:13] op_sel_hi:[0,1,1]
	v_pk_fma_f32 v[2:3], v[14:15], v[154:155], v[2:3] op_sel_hi:[0,1,1]
	s_nop 0
	s_nop 0
	s_nop 0
	s_waitcnt vmcnt(2)
	v_lshlrev_b32_e32 v152, 16, v230
	v_and_b32_e32 v153, 0xffff0000, v230
	v_lshlrev_b32_e32 v14, 16, v231
	v_and_b32_e32 v15, 0xffff0000, v231
	s_waitcnt lgkmcnt(1)
	v_pk_fma_f32 v[12:13], v[8:9], v[14:15], v[12:13] op_sel_hi:[0,1,1]
	s_nop 0
	s_nop 0
	v_pk_fma_f32 v[2:3], v[8:9], v[152:153], v[2:3] op_sel_hi:[0,1,1]
	s_nop 0
	s_waitcnt vmcnt(1)
	v_lshlrev_b32_e32 v152, 16, v232
	v_and_b32_e32 v153, 0xffff0000, v232
	v_lshlrev_b32_e32 v14, 16, v233
	v_and_b32_e32 v15, 0xffff0000, v233
	v_pk_fma_f32 v[12:13], v[8:9], v[14:15], v[12:13] op_sel:[1,0,0]
	v_pk_fma_f32 v[2:3], v[8:9], v[152:153], v[2:3] op_sel:[1,0,0]
	s_nop 0
	s_nop 0
	s_nop 0
	s_waitcnt vmcnt(0)
	v_lshlrev_b32_e32 v14, 16, v234
	v_and_b32_e32 v15, 0xffff0000, v234
	v_lshlrev_b32_e32 v8, 16, v235
	v_and_b32_e32 v9, 0xffff0000, v235
	v_pk_fma_f32 v[8:9], v[10:11], v[8:9], v[12:13] op_sel_hi:[0,1,1]
	v_lshl_add_u64 v[236:237], s[36:37], 0, v[146:147]
	global_load_dwordx2 v[236:237], v[236:237], off
	v_lshl_add_u64 v[238:239], s[52:53], 0, v[146:147]
	global_load_dwordx2 v[238:239], v[238:239], off
	v_lshl_add_u64 v[240:241], s[50:51], 0, v[146:147]
	global_load_dwordx2 v[240:241], v[240:241], off
	v_lshl_add_u64 v[242:243], s[26:27], 0, v[146:147]
	global_load_dwordx2 v[242:243], v[242:243], off
	v_lshl_add_u64 v[244:245], s[24:25], 0, v[146:147]
	global_load_dwordx2 v[244:245], v[244:245], off
	s_nop 0
	s_nop 0
	v_pk_fma_f32 v[2:3], v[10:11], v[14:15], v[2:3] op_sel_hi:[0,1,1]
	v_mov_b32_e32 v10, v11
	s_nop 0
	s_waitcnt vmcnt(4)
	v_lshlrev_b32_e32 v14, 16, v236
	v_and_b32_e32 v15, 0xffff0000, v236
	v_lshlrev_b32_e32 v12, 16, v237
	v_and_b32_e32 v13, 0xffff0000, v237
	v_pk_fma_f32 v[8:9], v[10:11], v[12:13], v[8:9] op_sel_hi:[0,1,1]
	v_pk_fma_f32 v[2:3], v[10:11], v[14:15], v[2:3] op_sel_hi:[0,1,1]
	s_nop 0
	s_nop 0
	s_nop 0
	s_waitcnt vmcnt(3)
	v_lshlrev_b32_e32 v12, 16, v238
	v_and_b32_e32 v13, 0xffff0000, v238
	v_lshlrev_b32_e32 v10, 16, v239
	v_and_b32_e32 v11, 0xffff0000, v239
	s_waitcnt lgkmcnt(0)
	v_pk_fma_f32 v[8:9], v[4:5], v[10:11], v[8:9] op_sel_hi:[0,1,1]
	s_nop 0
	s_nop 0
	v_pk_fma_f32 v[2:3], v[4:5], v[12:13], v[2:3] op_sel_hi:[0,1,1]
	s_nop 0
	s_waitcnt vmcnt(2)
	v_lshlrev_b32_e32 v12, 16, v240
	v_and_b32_e32 v13, 0xffff0000, v240
	v_lshlrev_b32_e32 v10, 16, v241
	v_and_b32_e32 v11, 0xffff0000, v241
	v_pk_fma_f32 v[8:9], v[4:5], v[10:11], v[8:9] op_sel:[1,0,0]
	v_pk_fma_f32 v[2:3], v[4:5], v[12:13], v[2:3] op_sel:[1,0,0]
	s_nop 0
	s_nop 0
	s_nop 0
	s_waitcnt vmcnt(1)
	v_lshlrev_b32_e32 v10, 16, v242
	v_and_b32_e32 v11, 0xffff0000, v242
	v_lshlrev_b32_e32 v4, 16, v243
	v_and_b32_e32 v5, 0xffff0000, v243
	v_pk_fma_f32 v[4:5], v[6:7], v[4:5], v[8:9] op_sel_hi:[0,1,1]
	s_nop 0
	s_nop 0
	v_pk_fma_f32 v[2:3], v[6:7], v[10:11], v[2:3] op_sel_hi:[0,1,1]
	v_mov_b32_e32 v6, v7
	s_nop 0
	s_waitcnt vmcnt(0)
	v_lshlrev_b32_e32 v10, 16, v244
	v_and_b32_e32 v11, 0xffff0000, v244
	v_lshlrev_b32_e32 v8, 16, v245
	v_and_b32_e32 v9, 0xffff0000, v245
	v_pk_mul_f32 v[14:15], v[6:7], v[10:11] op_sel_hi:[0,1]
	v_pk_fma_f32 v[2:3], v[6:7], v[10:11], v[2:3] op_sel_hi:[0,1,1]
	v_pk_mul_f32 v[12:13], v[6:7], v[8:9] op_sel_hi:[0,1]
	v_pk_fma_f32 v[8:9], v[6:7], v[8:9], v[4:5] op_sel_hi:[0,1,1]
	v_pk_fma_f32 v[10:11], v[92:93], v[2:3], v[14:15] op_sel_hi:[0,1,1] neg_lo:[0,0,1] neg_hi:[0,0,1]
	v_lshlrev_b64 v[14:15], 1, v[132:133]
	v_pk_fma_f32 v[4:5], v[0:1], v[148:149], v[2:3] op_sel_hi:[0,1,1] neg_lo:[1,0,0] neg_hi:[1,0,0]
	v_pk_fma_f32 v[0:1], v[0:1], v[150:151], v[8:9] op_sel_hi:[0,1,1] neg_lo:[1,0,0] neg_hi:[1,0,0]
	v_pk_fma_f32 v[12:13], v[92:93], v[8:9], v[12:13] op_sel_hi:[0,1,1] neg_lo:[0,0,1] neg_hi:[0,0,1]
	v_lshl_add_u64 v[236:237], s[22:23], 0, v[14:15]
	global_load_dwordx2 v[236:237], v[236:237], off offset:3072
	v_lshl_add_u64 v[238:239], s[20:21], 0, v[14:15]
	global_load_dwordx2 v[238:239], v[238:239], off offset:3072
	v_lshl_add_u64 v[8:9], s[22:23], 0, v[14:15]
	s_nop 0
	v_pk_fma_f32 v[0:1], v[136:137], v[142:143], v[0:1] op_sel_hi:[0,1,1]
	v_pk_fma_f32 v[6:7], v[94:95], v[0:1], v[140:141] op_sel_hi:[0,1,1] neg_lo:[0,0,1] neg_hi:[0,0,1]
	v_lshl_add_u32 v0, v134, 2, s17
	ds_read_b128 v[0:3], v0
	v_pk_fma_f32 v[4:5], v[136:137], v[138:139], v[4:5] op_sel_hi:[0,1,1]
	v_pk_fma_f32 v[4:5], v[94:95], v[4:5], v[144:145] op_sel_hi:[0,1,1] neg_lo:[0,0,1] neg_hi:[0,0,1]
	s_nop 0
	s_waitcnt vmcnt(1)
	v_lshlrev_b32_e32 v134, 16, v236
	v_and_b32_e32 v135, 0xffff0000, v236
	v_lshlrev_b32_e32 v132, 16, v237
	v_and_b32_e32 v133, 0xffff0000, v237
	s_waitcnt lgkmcnt(0)
	v_pk_fma_f32 v[134:135], v[0:1], v[10:11], v[134:135]
	v_lshl_add_u64 v[10:11], s[20:21], 0, v[14:15]
	v_pk_fma_f32 v[132:133], v[2:3], v[12:13], v[132:133]
	s_nop 0
	s_nop 0
	s_waitcnt vmcnt(0)
	v_lshlrev_b32_e32 v14, 16, v238
	v_and_b32_e32 v15, 0xffff0000, v238
	v_lshlrev_b32_e32 v12, 16, v239
	v_and_b32_e32 v13, 0xffff0000, v239
	v_pk_fma_f32 v[138:139], v[0:1], v[4:5], v[14:15]
	v_cvt_pk_bf16_f32 v0, v134, v135
	v_cvt_pk_bf16_f32 v1, v132, v133
	v_pk_fma_f32 v[136:137], v[2:3], v[6:7], v[12:13]
	v_cvt_pk_bf16_f32 v2, v138, v139
	s_nop 0
	v_cvt_pk_bf16_f32 v3, v136, v137
	global_store_dwordx2 v[8:9], v[0:1], off offset:3072
	global_store_dwordx2 v[10:11], v[2:3], off offset:3072
	v_mov_b32_e32 v0, v21
	ds_read_b32 v144, v27 offset:64
	v_lshlrev_b32_e32 v140, 2, v0
	v_add_u32_e32 v142, 0x700, v140
	v_ashrrev_i32_e32 v143, 31, v142
	v_lshlrev_b64 v[154:155], 1, v[142:143]
	v_lshl_add_u64 v[0:1], vcc, 0, v[154:155]
	global_load_dwordx2 v[0:1], v[0:1], off
	v_lshl_add_u64 v[156:157], s[76:77], 0, v[154:155]
	v_lshl_add_u64 v[164:165], s[10:11], 0, v[154:155]
	v_ashrrev_i32_e32 v141, 31, v140
	s_nop 0
	s_waitcnt vmcnt(0)
	v_lshlrev_b32_e32 v146, 16, v0
	v_and_b32_e32 v147, 0xffff0000, v0
	v_lshlrev_b32_e32 v150, 16, v1
	v_and_b32_e32 v151, 0xffff0000, v1
	ds_read_b128 v[0:3], v27
	ds_read_b128 v[12:15], v27 offset:16
	ds_read_b128 v[8:11], v27 offset:32
	ds_read_b128 v[4:7], v27 offset:48
	global_load_dwordx2 v[158:159], v[156:157], off
	s_waitcnt lgkmcnt(4)
	v_pk_mul_f32 v[152:153], v[144:145], v[146:147] op_sel_hi:[0,1]
	global_load_dwordx2 v[164:165], v[164:165], off
	v_pk_mul_f32 v[148:149], v[144:145], v[150:151] op_sel_hi:[0,1]
	s_nop 0
	s_waitcnt vmcnt(1)
	v_lshlrev_b32_e32 v156, 16, v158
	v_and_b32_e32 v157, 0xffff0000, v158
	v_lshlrev_b32_e32 v158, 16, v159
	v_and_b32_e32 v159, 0xffff0000, v159
	s_waitcnt lgkmcnt(3)
	v_pk_fma_f32 v[162:163], v[0:1], v[158:159], 0 op_sel_hi:[0,1,0]
	s_nop 0
	s_waitcnt vmcnt(0)
	v_lshlrev_b32_e32 v166, 16, v164
	v_and_b32_e32 v167, 0xffff0000, v164
	v_lshlrev_b32_e32 v164, 16, v165
	v_and_b32_e32 v165, 0xffff0000, v165
	v_pk_fma_f32 v[162:163], v[0:1], v[164:165], v[162:163] op_sel:[1,0,0]
	v_lshl_add_u64 v[236:237], s[8:9], 0, v[154:155]
	global_load_dwordx2 v[236:237], v[236:237], off
	v_lshl_add_u64 v[238:239], s[44:45], 0, v[154:155]
	global_load_dwordx2 v[238:239], v[238:239], off
	v_lshl_add_u64 v[240:241], s[48:49], 0, v[154:155]
	global_load_dwordx2 v[240:241], v[240:241], off
	v_lshl_add_u64 v[242:243], s[46:47], 0, v[154:155]
	global_load_dwordx2 v[242:243], v[242:243], off
	v_lshl_add_u64 v[244:245], s[30:31], 0, v[154:155]
	global_load_dwordx2 v[244:245], v[244:245], off
	v_lshl_add_u64 v[246:247], s[28:29], 0, v[154:155]
	global_load_dwordx2 v[246:247], v[246:247], off
	v_lshl_add_u64 v[230:231], s[0:1], 0, v[154:155]
	global_load_dwordx2 v[230:231], v[230:231], off
	v_lshl_add_u64 v[232:233], s[42:43], 0, v[154:155]
	global_load_dwordx2 v[232:233], v[232:233], off
	v_lshl_add_u64 v[234:235], s[2:3], 0, v[154:155]
	global_load_dwordx2 v[234:235], v[234:235], off
	s_nop 0
	s_nop 0
	v_pk_fma_f32 v[160:161], v[0:1], v[156:157], 0 op_sel_hi:[0,1,0]
	v_pk_fma_f32 v[160:161], v[0:1], v[166:167], v[160:161] op_sel:[1,0,0]
	s_nop 0
	s_waitcnt vmcnt(8)
	v_lshlrev_b32_e32 v166, 16, v236
	v_and_b32_e32 v167, 0xffff0000, v236
	v_lshlrev_b32_e32 v164, 16, v237
	v_and_b32_e32 v165, 0xffff0000, v237
	v_pk_fma_f32 v[162:163], v[2:3], v[164:165], v[162:163] op_sel_hi:[0,1,1]
	s_nop 0
	s_nop 0
	v_pk_fma_f32 v[160:161], v[2:3], v[166:167], v[160:161] op_sel_hi:[0,1,1]
	v_mov_b32_e32 v2, v3
	s_nop 0
	s_waitcnt vmcnt(7)
	v_lshlrev_b32_e32 v166, 16, v238
	v_and_b32_e32 v167, 0xffff0000, v238
	v_lshlrev_b32_e32 v164, 16, v239
	v_and_b32_e32 v165, 0xffff0000, v239
	v_pk_fma_f32 v[162:163], v[2:3], v[164:165], v[162:163] op_sel_hi:[0,1,1]
	v_pk_fma_f32 v[2:3], v[2:3], v[166:167], v[160:161] op_sel_hi:[0,1,1]
	s_nop 0
	s_nop 0
	s_nop 0
	s_waitcnt vmcnt(6)
	v_lshlrev_b32_e32 v164, 16, v240
	v_and_b32_e32 v165, 0xffff0000, v240
	v_lshlrev_b32_e32 v160, 16, v241
	v_and_b32_e32 v161, 0xffff0000, v241
	s_waitcnt lgkmcnt(2)
	v_pk_fma_f32 v[160:161], v[12:13], v[160:161], v[162:163] op_sel_hi:[0,1,1]
	s_nop 0
	s_nop 0
	v_pk_fma_f32 v[2:3], v[12:13], v[164:165], v[2:3] op_sel_hi:[0,1,1]
	s_nop 0
	s_waitcnt vmcnt(5)
	v_lshlrev_b32_e32 v164, 16, v242
	v_and_b32_e32 v165, 0xffff0000, v242
	v_lshlrev_b32_e32 v162, 16, v243
	v_and_b32_e32 v163, 0xffff0000, v243
	v_pk_fma_f32 v[160:161], v[12:13], v[162:163], v[160:161] op_sel:[1,0,0]
	v_pk_fma_f32 v[2:3], v[12:13], v[164:165], v[2:3] op_sel:[1,0,0]
	s_nop 0
	s_nop 0
	s_nop 0
	s_waitcnt vmcnt(4)
	v_lshlrev_b32_e32 v162, 16, v244
	v_and_b32_e32 v163, 0xffff0000, v244
	v_lshlrev_b32_e32 v12, 16, v245
	v_and_b32_e32 v13, 0xffff0000, v245
	v_pk_fma_f32 v[12:13], v[14:15], v[12:13], v[160:161] op_sel_hi:[0,1,1]
	s_nop 0
	s_nop 0
	v_pk_fma_f32 v[2:3], v[14:15], v[162:163], v[2:3] op_sel_hi:[0,1,1]
	v_mov_b32_e32 v14, v15
	s_nop 0
	s_waitcnt vmcnt(3)
	v_lshlrev_b32_e32 v162, 16, v246
	v_and_b32_e32 v163, 0xffff0000, v246
	v_lshlrev_b32_e32 v160, 16, v247
	v_and_b32_e32 v161, 0xffff0000, v247
	v_pk_fma_f32 v[12:13], v[14:15], v[160:161], v[12:13] op_sel_hi:[0,1,1]
	v_pk_fma_f32 v[2:3], v[14:15], v[162:163], v[2:3] op_sel_hi:[0,1,1]
	s_nop 0
	s_nop 0
	s_nop 0
	s_waitcnt vmcnt(2)
	v_lshlrev_b32_e32 v160, 16, v230
	v_and_b32_e32 v161, 0xffff0000, v230
	v_lshlrev_b32_e32 v14, 16, v231
	v_and_b32_e32 v15, 0xffff0000, v231
	s_waitcnt lgkmcnt(1)
	v_pk_fma_f32 v[12:13], v[8:9], v[14:15], v[12:13] op_sel_hi:[0,1,1]
	s_nop 0
	s_nop 0
	v_pk_fma_f32 v[2:3], v[8:9], v[160:161], v[2:3] op_sel_hi:[0,1,1]
	s_nop 0
	s_waitcnt vmcnt(1)
	v_lshlrev_b32_e32 v160, 16, v232
	v_and_b32_e32 v161, 0xffff0000, v232
	v_lshlrev_b32_e32 v14, 16, v233
	v_and_b32_e32 v15, 0xffff0000, v233
	v_pk_fma_f32 v[12:13], v[8:9], v[14:15], v[12:13] op_sel:[1,0,0]
	v_pk_fma_f32 v[2:3], v[8:9], v[160:161], v[2:3] op_sel:[1,0,0]
	s_nop 0
	s_nop 0
	s_nop 0
	s_waitcnt vmcnt(0)
	v_lshlrev_b32_e32 v14, 16, v234
	v_and_b32_e32 v15, 0xffff0000, v234
	v_lshlrev_b32_e32 v8, 16, v235
	v_and_b32_e32 v9, 0xffff0000, v235
	v_pk_fma_f32 v[8:9], v[10:11], v[8:9], v[12:13] op_sel_hi:[0,1,1]
	v_lshl_add_u64 v[236:237], s[36:37], 0, v[154:155]
	global_load_dwordx2 v[236:237], v[236:237], off
	v_lshl_add_u64 v[238:239], s[52:53], 0, v[154:155]
	global_load_dwordx2 v[238:239], v[238:239], off
	v_lshl_add_u64 v[240:241], s[50:51], 0, v[154:155]
	global_load_dwordx2 v[240:241], v[240:241], off
	v_lshl_add_u64 v[242:243], s[26:27], 0, v[154:155]
	global_load_dwordx2 v[242:243], v[242:243], off
	v_lshl_add_u64 v[244:245], s[24:25], 0, v[154:155]
	global_load_dwordx2 v[244:245], v[244:245], off
	s_nop 0
	s_nop 0
	v_pk_fma_f32 v[2:3], v[10:11], v[14:15], v[2:3] op_sel_hi:[0,1,1]
	v_mov_b32_e32 v10, v11
	s_nop 0
	s_waitcnt vmcnt(4)
	v_lshlrev_b32_e32 v14, 16, v236
	v_and_b32_e32 v15, 0xffff0000, v236
	v_lshlrev_b32_e32 v12, 16, v237
	v_and_b32_e32 v13, 0xffff0000, v237
	v_pk_fma_f32 v[8:9], v[10:11], v[12:13], v[8:9] op_sel_hi:[0,1,1]
	v_pk_fma_f32 v[2:3], v[10:11], v[14:15], v[2:3] op_sel_hi:[0,1,1]
	s_nop 0
	s_nop 0
	s_nop 0
	s_waitcnt vmcnt(3)
	v_lshlrev_b32_e32 v12, 16, v238
	v_and_b32_e32 v13, 0xffff0000, v238
	v_lshlrev_b32_e32 v10, 16, v239
	v_and_b32_e32 v11, 0xffff0000, v239
	s_waitcnt lgkmcnt(0)
	v_pk_fma_f32 v[8:9], v[4:5], v[10:11], v[8:9] op_sel_hi:[0,1,1]
	s_nop 0
	s_nop 0
	v_pk_fma_f32 v[2:3], v[4:5], v[12:13], v[2:3] op_sel_hi:[0,1,1]
	s_nop 0
	s_waitcnt vmcnt(2)
	v_lshlrev_b32_e32 v12, 16, v240
	v_and_b32_e32 v13, 0xffff0000, v240
	v_lshlrev_b32_e32 v10, 16, v241
	v_and_b32_e32 v11, 0xffff0000, v241
	v_pk_fma_f32 v[8:9], v[4:5], v[10:11], v[8:9] op_sel:[1,0,0]
	v_pk_fma_f32 v[2:3], v[4:5], v[12:13], v[2:3] op_sel:[1,0,0]
	s_nop 0
	s_nop 0
	s_nop 0
	s_waitcnt vmcnt(1)
	v_lshlrev_b32_e32 v10, 16, v242
	v_and_b32_e32 v11, 0xffff0000, v242
	v_lshlrev_b32_e32 v4, 16, v243
	v_and_b32_e32 v5, 0xffff0000, v243
	v_pk_fma_f32 v[4:5], v[6:7], v[4:5], v[8:9] op_sel_hi:[0,1,1]
	s_nop 0
	s_nop 0
	v_pk_fma_f32 v[2:3], v[6:7], v[10:11], v[2:3] op_sel_hi:[0,1,1]
	v_mov_b32_e32 v6, v7
	s_nop 0
	s_waitcnt vmcnt(0)
	v_lshlrev_b32_e32 v10, 16, v244
	v_and_b32_e32 v11, 0xffff0000, v244
	v_lshlrev_b32_e32 v8, 16, v245
	v_and_b32_e32 v9, 0xffff0000, v245
	v_pk_fma_f32 v[2:3], v[6:7], v[10:11], v[2:3] op_sel_hi:[0,1,1]
	v_pk_mul_f32 v[12:13], v[6:7], v[8:9] op_sel_hi:[0,1]
	v_pk_mul_f32 v[14:15], v[6:7], v[10:11] op_sel_hi:[0,1]
	v_pk_fma_f32 v[4:5], v[6:7], v[8:9], v[4:5] op_sel_hi:[0,1,1]
	v_pk_fma_f32 v[6:7], v[0:1], v[156:157], v[2:3] op_sel_hi:[0,1,1] neg_lo:[1,0,0] neg_hi:[1,0,0]
	v_pk_fma_f32 v[0:1], v[0:1], v[158:159], v[4:5] op_sel_hi:[0,1,1] neg_lo:[1,0,0] neg_hi:[1,0,0]
	v_pk_fma_f32 v[6:7], v[144:145], v[146:147], v[6:7] op_sel_hi:[0,1,1]
	v_pk_fma_f32 v[4:5], v[92:93], v[4:5], v[12:13] op_sel_hi:[0,1,1] neg_lo:[0,0,1] neg_hi:[0,0,1]
	v_lshlrev_b64 v[12:13], 1, v[140:141]
	v_pk_fma_f32 v[8:9], v[94:95], v[6:7], v[152:153] op_sel_hi:[0,1,1] neg_lo:[0,0,1] neg_hi:[0,0,1]
	v_pk_fma_f32 v[6:7], v[92:93], v[2:3], v[14:15] op_sel_hi:[0,1,1] neg_lo:[0,0,1] neg_hi:[0,0,1]
	v_lshl_add_u64 v[236:237], s[22:23], 0, v[12:13]
	global_load_dwordx2 v[236:237], v[236:237], off offset:3584
	v_lshl_add_u64 v[238:239], s[20:21], 0, v[12:13]
	global_load_dwordx2 v[238:239], v[238:239], off offset:3584
	v_lshl_add_u64 v[14:15], s[22:23], 0, v[12:13]
	s_nop 0
	v_pk_fma_f32 v[0:1], v[144:145], v[150:151], v[0:1] op_sel_hi:[0,1,1]
	v_pk_fma_f32 v[10:11], v[94:95], v[0:1], v[148:149] op_sel_hi:[0,1,1] neg_lo:[0,0,1] neg_hi:[0,0,1]
	v_lshl_add_u32 v0, v142, 2, s17
	ds_read_b128 v[0:3], v0
	s_nop 0
	s_waitcnt vmcnt(1)
	v_lshlrev_b32_e32 v94, 16, v236
	v_and_b32_e32 v95, 0xffff0000, v236
	v_lshlrev_b32_e32 v92, 16, v237
	v_and_b32_e32 v93, 0xffff0000, v237
	s_waitcnt lgkmcnt(0)
	v_pk_fma_f32 v[4:5], v[2:3], v[4:5], v[92:93]
	v_lshl_add_u64 v[92:93], s[20:21], 0, v[12:13]
	s_nop 0
	v_pk_fma_f32 v[6:7], v[0:1], v[6:7], v[94:95]
	s_nop 0
	s_waitcnt vmcnt(0)
	v_lshlrev_b32_e32 v94, 16, v238
	v_and_b32_e32 v95, 0xffff0000, v238
	v_lshlrev_b32_e32 v12, 16, v239
	v_and_b32_e32 v13, 0xffff0000, v239
	v_pk_fma_f32 v[10:11], v[2:3], v[10:11], v[12:13]
	v_pk_fma_f32 v[12:13], v[0:1], v[8:9], v[94:95]
	v_cvt_pk_bf16_f32 v0, v6, v7
	v_cvt_pk_bf16_f32 v1, v4, v5
	s_nop 0
	v_cvt_pk_bf16_f32 v2, v12, v13
	v_cvt_pk_bf16_f32 v3, v10, v11
	global_store_dwordx2 v[14:15], v[0:1], off offset:3584
	global_store_dwordx2 v[92:93], v[2:3], off offset:3584
	v_mul_f32_e32 v0, v87, v87
	v_mul_f32_e32 v1, v85, v85
	v_fmac_f32_e32 v0, v86, v86
	v_fmac_f32_e32 v1, v84, v84
	v_mov_b32_e32 v2, v83
	v_mov_b32_e32 v3, v91
	v_add_f32_e32 v14, v0, v1
	v_mov_b32_e32 v0, v82
	v_mov_b32_e32 v1, v90
	v_pk_mul_f32 v[2:3], v[2:3], v[2:3]
	v_mov_b32_e32 v8, v81
	v_mov_b32_e32 v9, v89
	v_pk_fma_f32 v[0:1], v[0:1], v[0:1], v[2:3]
	v_mov_b32_e32 v2, v80
	v_mov_b32_e32 v3, v88
	v_pk_mul_f32 v[8:9], v[8:9], v[8:9]
	v_mul_f32_e32 v29, v115, v115
	v_pk_fma_f32 v[2:3], v[2:3], v[2:3], v[8:9]
	v_pk_mul_f32 v[8:9], v[102:103], v[102:103]
	v_pk_add_f32 v[0:1], v[0:1], v[2:3]
	v_mul_f32_e32 v2, v99, v99
	v_mul_f32_e32 v3, v97, v97
	v_fmac_f32_e32 v2, v98, v98
	v_fmac_f32_e32 v3, v96, v96
	v_add_f32_e32 v2, v2, v3
	v_add_f32_e32 v27, v14, v2
	v_pk_mul_f32 v[2:3], v[100:101], v[100:101]
	v_pk_add_f32 v[0:1], v[0:1], v[0:1] op_sel:[0,1] op_sel_hi:[1,0]
	v_pk_mov_b32 v[14:15], v[8:9], v[2:3] op_sel:[1,0]
	v_mov_b32_e32 v9, v3
	v_pk_add_f32 v[2:3], v[14:15], v[8:9]
	v_mul_f32_e32 v8, v107, v107
	v_mul_f32_e32 v9, v105, v105
	v_fmac_f32_e32 v8, v106, v106
	v_fmac_f32_e32 v9, v104, v104
	v_add_f32_e32 v8, v8, v9
	v_add_f32_e32 v27, v27, v8
	v_mul_f32_e32 v8, v118, v118
	v_mul_f32_e32 v9, v119, v119
	v_pk_add_f32 v[2:3], v[2:3], v[2:3] op_sel:[0,1] op_sel_hi:[1,0]
	v_mov_b32_e32 v1, v8
	v_mov_b32_e32 v3, v9
	v_pk_add_f32 v[0:1], v[0:1], v[2:3]
	v_mul_f32_e32 v2, v111, v111
	v_mul_f32_e32 v8, v109, v109
	v_mul_f32_e32 v14, v116, v116
	v_mul_f32_e32 v15, v117, v117
	v_pk_fma_f32 v[2:3], v[110:111], v[110:111], v[2:3] op_sel_hi:[1,1,0]
	v_pk_fma_f32 v[8:9], v[108:109], v[108:109], v[8:9] op_sel_hi:[1,1,0]
	v_mov_b32_e32 v3, v14
	v_mov_b32_e32 v9, v15
	v_pk_add_f32 v[2:3], v[2:3], v[8:9]
	v_pk_mul_f32 v[8:9], v[126:127], v[126:127]
	v_pk_add_f32 v[0:1], v[0:1], v[2:3]
	v_pk_mul_f32 v[2:3], v[124:125], v[124:125]
	v_pk_add_f32 v[0:1], v[0:1], v[0:1] op_sel:[0,1] op_sel_hi:[1,0]
	v_pk_mov_b32 v[14:15], v[8:9], v[2:3] op_sel:[1,0]
	v_mov_b32_e32 v9, v3
	v_pk_add_f32 v[2:3], v[14:15], v[8:9]
	v_mul_f32_e32 v8, v6, v6
	v_mul_f32_e32 v9, v7, v7
	v_pk_add_f32 v[2:3], v[2:3], v[2:3] op_sel:[0,1] op_sel_hi:[1,0]
	v_mov_b32_e32 v1, v8
	v_mov_b32_e32 v3, v9
	v_pk_add_f32 v[0:1], v[0:1], v[2:3]
	v_mul_f32_e32 v2, v135, v135
	v_mul_f32_e32 v8, v133, v133
	v_mul_f32_e32 v14, v4, v4
	v_mul_f32_e32 v15, v5, v5
	v_pk_fma_f32 v[2:3], v[134:135], v[134:135], v[2:3] op_sel_hi:[1,1,0]
	v_pk_fma_f32 v[8:9], v[132:133], v[132:133], v[8:9] op_sel_hi:[1,1,0]
	v_mov_b32_e32 v3, v14
	v_mov_b32_e32 v9, v15
	v_pk_add_f32 v[2:3], v[2:3], v[8:9]
	v_mul_f32_e32 v33, v113, v113
	v_pk_add_f32 v[0:1], v[0:1], v[2:3]
	v_xor_b32_e32 v2, 1, v188
	v_add_f32_e32 v0, v0, v1
	v_and_b32_e32 v1, 64, v188
	v_add_u32_e32 v1, 64, v1
	v_cmp_lt_i32_e32 vcc, v2, v1
	v_fmac_f32_e32 v29, v114, v114
	v_fmac_f32_e32 v33, v112, v112
	v_cndmask_b32_e32 v2, v188, v2, vcc
	v_lshlrev_b32_e32 v31, 2, v2
	ds_bpermute_b32 v2, v31, v0
	v_add_f32_e32 v3, v29, v33
	v_mul_f32_e32 v8, v123, v123
	v_mul_f32_e32 v9, v121, v121
	v_fmac_f32_e32 v8, v122, v122
	s_waitcnt lgkmcnt(0)
	v_add_f32_e32 v0, v0, v2
	v_xor_b32_e32 v2, 2, v188
	v_cmp_lt_i32_e32 vcc, v2, v1
	v_fmac_f32_e32 v9, v120, v120
	v_add_f32_e32 v3, v27, v3
	v_cndmask_b32_e32 v2, v188, v2, vcc
	v_lshlrev_b32_e32 v33, 2, v2
	ds_bpermute_b32 v2, v33, v0
	v_add_f32_e32 v8, v8, v9
	v_add_f32_e32 v3, v3, v8
	v_mul_f32_e32 v8, v131, v131
	v_mul_f32_e32 v9, v129, v129
	s_waitcnt lgkmcnt(0)
	v_add_f32_e32 v0, v0, v2
	v_xor_b32_e32 v2, 4, v188
	v_cmp_lt_i32_e32 vcc, v2, v1
	v_fmac_f32_e32 v8, v130, v130
	v_fmac_f32_e32 v9, v128, v128
	v_cndmask_b32_e32 v2, v188, v2, vcc
	v_lshlrev_b32_e32 v35, 2, v2
	ds_bpermute_b32 v2, v35, v0
	v_add_f32_e32 v8, v8, v9
	v_add_f32_e32 v3, v3, v8
	v_mul_f32_e32 v8, v139, v139
	v_mul_f32_e32 v9, v137, v137
	s_waitcnt lgkmcnt(0)
	v_add_f32_e32 v0, v0, v2
	v_xor_b32_e32 v2, 8, v188
	v_cmp_lt_i32_e32 vcc, v2, v1
	v_fmac_f32_e32 v8, v138, v138
	v_fmac_f32_e32 v9, v136, v136
	v_cndmask_b32_e32 v2, v188, v2, vcc
	v_lshlrev_b32_e32 v41, 2, v2
	ds_bpermute_b32 v2, v41, v0
	v_add_f32_e32 v8, v8, v9
	s_waitcnt lgkmcnt(0)
	v_add_f32_e32 v0, v0, v2
	v_xor_b32_e32 v2, 16, v188
	v_cmp_lt_i32_e32 vcc, v2, v1
	s_nop 1
	v_cndmask_b32_e32 v2, v188, v2, vcc
	v_lshlrev_b32_e32 v37, 2, v2
	ds_bpermute_b32 v2, v37, v0
	s_waitcnt lgkmcnt(0)
	v_add_f32_e32 v0, v0, v2
	v_xor_b32_e32 v2, 32, v188
	v_cmp_lt_i32_e32 vcc, v2, v1
	s_nop 1
	v_cndmask_b32_e32 v1, v188, v2, vcc
	v_lshlrev_b32_e32 v39, 2, v1
	ds_bpermute_b32 v1, v39, v0
	v_add_f32_e32 v2, v3, v8
	v_mul_f32_e32 v3, v13, v13
	v_mul_f32_e32 v8, v11, v11
	v_fmac_f32_e32 v3, v12, v12
	s_waitcnt lgkmcnt(0)
	v_add_f32_e32 v0, v0, v1
	v_fmamk_f32 v0, v0, 0x3a000000, v189
	v_mul_f32_e32 v1, 0x4f800000, v0
	v_cmp_gt_f32_e32 vcc, s84, v0
	v_fmac_f32_e32 v8, v10, v10
	v_add_f32_e32 v3, v3, v8
	v_cndmask_b32_e32 v0, v0, v1, vcc
	v_sqrt_f32_e32 v1, v0
	v_add_f32_e32 v2, v2, v3
	v_add_u32_e32 v3, -1, v1
	v_fma_f32 v8, -v3, v1, v0
	v_cmp_ge_f32_e64 s[46:47], 0, v8
	v_add_u32_e32 v8, 1, v1
	s_nop 0
	v_cndmask_b32_e64 v3, v1, v3, s[46:47]
	v_fma_f32 v1, -v8, v1, v0
	v_cmp_lt_f32_e64 s[46:47], 0, v1
	s_nop 1
	v_cndmask_b32_e64 v1, v3, v8, s[46:47]
	v_mul_f32_e32 v3, 0x37800000, v1
	v_cndmask_b32_e32 v1, v1, v3, vcc
	ds_bpermute_b32 v3, v31, v2
	v_cmp_class_f32_e32 vcc, v0, v190
	v_cndmask_b32_e32 v27, v1, v0, vcc
	s_waitcnt lgkmcnt(0)
	v_add_f32_e32 v0, v2, v3
	ds_bpermute_b32 v1, v33, v0
	v_div_scale_f32 v43, s[0:1], v27, v27, 1.0
	v_rcp_f32_e32 v29, v43
	v_div_scale_f32 v47, vcc, 1.0, v27, 1.0
	s_waitcnt lgkmcnt(0)
	v_add_f32_e32 v0, v0, v1
	ds_bpermute_b32 v1, v35, v0
	v_fma_f32 v2, -v43, v29, 1.0
	v_fmac_f32_e32 v29, v2, v29
	v_mul_f32_e32 v45, v47, v29
	v_fma_f32 v51, -v43, v45, v47
	s_waitcnt lgkmcnt(0)
	v_add_f32_e32 v49, v0, v1
	ds_read_b128 v[0:3], v25
	ds_read_b128 v[92:95], v25 offset:1024
	ds_read_b128 v[140:143], v25 offset:2048
	ds_read_b128 v[144:147], v25 offset:3072
	ds_read_b128 v[148:151], v25 offset:4096
	ds_read_b128 v[152:155], v25 offset:5120
	ds_read_b128 v[156:159], v25 offset:6144
	ds_read_b128 v[160:163], v25 offset:7168
	ds_read_b128 v[164:167], v25 offset:8192
	ds_read_b128 v[174:177], v25 offset:9216
	ds_read_b128 v[178:181], v25 offset:10240
	ds_read_b128 v[182:185], v25 offset:11264
	ds_read_b128 v[198:201], v25 offset:12288
	ds_read_b128 v[202:205], v25 offset:13312
	ds_read_b128 v[206:209], v25 offset:14336
	ds_read_b128 v[210:213], v25 offset:15360
	s_waitcnt lgkmcnt(7)
	v_mov_b32_e32 v8, v164
	v_mov_b32_e32 v9, v1
	v_mov_b32_e32 v1, v165
	v_mov_b32_e32 v164, v166
	v_mov_b32_e32 v165, v3
	v_pk_mul_f32 v[14:15], v[82:83], v[8:9]
	v_pk_mul_f32 v[214:215], v[80:81], v[164:165]
	v_mov_b32_e32 v3, v167
	v_pk_fma_f32 v[14:15], v[82:83], v[0:1], v[14:15] op_sel:[0,0,1] op_sel_hi:[1,1,0]
	v_pk_fma_f32 v[166:167], v[80:81], v[2:3], v[214:215] op_sel:[0,0,1] op_sel_hi:[1,1,0]
	v_pk_mul_f32 v[8:9], v[86:87], v[8:9]
	v_pk_add_f32 v[14:15], v[14:15], v[166:167]
	s_waitcnt lgkmcnt(6)
	v_mov_b32_e32 v166, v174
	v_mov_b32_e32 v167, v93
	v_pk_mul_f32 v[214:215], v[90:91], v[166:167]
	v_mov_b32_e32 v93, v175
	v_pk_fma_f32 v[174:175], v[90:91], v[92:93], v[214:215] op_sel:[0,0,1] op_sel_hi:[1,1,0]
	v_mov_b32_e32 v214, v176
	v_mov_b32_e32 v215, v95
	v_pk_mul_f32 v[216:217], v[88:89], v[214:215]
	v_mov_b32_e32 v95, v177
	v_pk_fma_f32 v[176:177], v[88:89], v[94:95], v[216:217] op_sel:[0,0,1] op_sel_hi:[1,1,0]
	v_pk_add_f32 v[14:15], v[14:15], 0 op_sel_hi:[1,0]
	v_pk_add_f32 v[174:175], v[174:175], v[176:177]
	v_pk_fma_f32 v[0:1], v[86:87], v[0:1], v[8:9] op_sel:[0,0,1] op_sel_hi:[1,1,0]
	v_pk_add_f32 v[14:15], v[14:15], v[174:175]
	s_waitcnt lgkmcnt(5)
	v_mov_b32_e32 v174, v178
	v_mov_b32_e32 v175, v141
	v_mov_b32_e32 v141, v179
	v_mov_b32_e32 v178, v180
	v_mov_b32_e32 v179, v143
	v_pk_mul_f32 v[176:177], v[102:103], v[174:175]
	v_pk_mul_f32 v[216:217], v[100:101], v[178:179]
	v_mov_b32_e32 v143, v181
	v_pk_mul_f32 v[8:9], v[84:85], v[164:165]
	v_pk_fma_f32 v[176:177], v[102:103], v[140:141], v[176:177] op_sel:[0,0,1] op_sel_hi:[1,1,0]
	v_pk_fma_f32 v[180:181], v[100:101], v[142:143], v[216:217] op_sel:[0,0,1] op_sel_hi:[1,1,0]
	v_pk_fma_f32 v[2:3], v[84:85], v[2:3], v[8:9] op_sel:[0,0,1] op_sel_hi:[1,1,0]
	v_pk_add_f32 v[176:177], v[176:177], v[180:181]
	v_pk_add_f32 v[0:1], v[0:1], v[2:3]
	v_pk_mul_f32 v[2:3], v[98:99], v[166:167]
	v_pk_mul_f32 v[8:9], v[96:97], v[214:215]
	v_pk_add_f32 v[14:15], v[14:15], v[176:177]
	s_waitcnt lgkmcnt(4)
	v_mov_b32_e32 v176, v182
	v_mov_b32_e32 v177, v145
	v_mov_b32_e32 v145, v183
	v_mov_b32_e32 v182, v184
	v_mov_b32_e32 v183, v147
	v_pk_fma_f32 v[2:3], v[98:99], v[92:93], v[2:3] op_sel:[0,0,1] op_sel_hi:[1,1,0]
	v_pk_fma_f32 v[8:9], v[96:97], v[94:95], v[8:9] op_sel:[0,0,1] op_sel_hi:[1,1,0]
	v_pk_mul_f32 v[180:181], v[110:111], v[176:177]
	v_pk_mul_f32 v[216:217], v[108:109], v[182:183]
	v_mov_b32_e32 v147, v185
	v_pk_add_f32 v[0:1], v[0:1], 0 op_sel_hi:[1,0]
	v_pk_add_f32 v[2:3], v[2:3], v[8:9]
	v_pk_fma_f32 v[180:181], v[110:111], v[144:145], v[180:181] op_sel:[0,0,1] op_sel_hi:[1,1,0]
	v_pk_fma_f32 v[184:185], v[108:109], v[146:147], v[216:217] op_sel:[0,0,1] op_sel_hi:[1,1,0]
	v_pk_add_f32 v[0:1], v[0:1], v[2:3]
	v_pk_mul_f32 v[2:3], v[106:107], v[174:175]
	v_pk_mul_f32 v[8:9], v[104:105], v[178:179]
	v_pk_add_f32 v[180:181], v[180:181], v[184:185]
	v_pk_fma_f32 v[2:3], v[106:107], v[140:141], v[2:3] op_sel:[0,0,1] op_sel_hi:[1,1,0]
	v_pk_fma_f32 v[8:9], v[104:105], v[142:143], v[8:9] op_sel:[0,0,1] op_sel_hi:[1,1,0]
	v_pk_add_f32 v[14:15], v[14:15], v[180:181]
	s_waitcnt lgkmcnt(3)
	v_mov_b32_e32 v180, v198
	v_mov_b32_e32 v181, v149
	v_mov_b32_e32 v149, v199
	v_mov_b32_e32 v198, v200
	v_mov_b32_e32 v199, v151
	v_pk_add_f32 v[2:3], v[2:3], v[8:9]
	v_pk_mul_f32 v[184:185], v[118:119], v[180:181]
	v_pk_mul_f32 v[216:217], v[116:117], v[198:199]
	v_mov_b32_e32 v151, v201
	v_pk_add_f32 v[0:1], v[0:1], v[2:3]
	v_pk_mul_f32 v[2:3], v[114:115], v[176:177]
	v_pk_mul_f32 v[8:9], v[112:113], v[182:183]
	v_pk_fma_f32 v[184:185], v[118:119], v[148:149], v[184:185] op_sel:[0,0,1] op_sel_hi:[1,1,0]
	v_pk_fma_f32 v[200:201], v[116:117], v[150:151], v[216:217] op_sel:[0,0,1] op_sel_hi:[1,1,0]
	v_pk_fma_f32 v[2:3], v[114:115], v[144:145], v[2:3] op_sel:[0,0,1] op_sel_hi:[1,1,0]
	v_pk_fma_f32 v[8:9], v[112:113], v[146:147], v[8:9] op_sel:[0,0,1] op_sel_hi:[1,1,0]
	v_pk_add_f32 v[184:185], v[184:185], v[200:201]
	v_pk_add_f32 v[2:3], v[2:3], v[8:9]
	v_pk_add_f32 v[14:15], v[14:15], v[184:185]
	s_waitcnt lgkmcnt(2)
	v_mov_b32_e32 v184, v202
	v_mov_b32_e32 v185, v153
	v_mov_b32_e32 v153, v203
	v_mov_b32_e32 v202, v204
	v_mov_b32_e32 v203, v155
	v_pk_add_f32 v[0:1], v[0:1], v[2:3]
	v_pk_mul_f32 v[2:3], v[122:123], v[180:181]
	v_pk_mul_f32 v[8:9], v[120:121], v[198:199]
	v_pk_mul_f32 v[200:201], v[126:127], v[184:185]
	v_pk_mul_f32 v[216:217], v[124:125], v[202:203]
	v_mov_b32_e32 v155, v205
	v_pk_fma_f32 v[2:3], v[122:123], v[148:149], v[2:3] op_sel:[0,0,1] op_sel_hi:[1,1,0]
	v_pk_fma_f32 v[8:9], v[120:121], v[150:151], v[8:9] op_sel:[0,0,1] op_sel_hi:[1,1,0]
	v_pk_fma_f32 v[200:201], v[126:127], v[152:153], v[200:201] op_sel:[0,0,1] op_sel_hi:[1,1,0]
	v_pk_fma_f32 v[204:205], v[124:125], v[154:155], v[216:217] op_sel:[0,0,1] op_sel_hi:[1,1,0]
	v_pk_add_f32 v[2:3], v[2:3], v[8:9]
	v_pk_add_f32 v[200:201], v[200:201], v[204:205]
	v_pk_add_f32 v[0:1], v[0:1], v[2:3]
	v_pk_mul_f32 v[2:3], v[130:131], v[184:185]
	v_pk_mul_f32 v[8:9], v[128:129], v[202:203]
	v_pk_add_f32 v[14:15], v[14:15], v[200:201]
	s_waitcnt lgkmcnt(1)
	v_mov_b32_e32 v200, v206
	v_mov_b32_e32 v201, v157
	v_mov_b32_e32 v157, v207
	v_mov_b32_e32 v206, v208
	v_mov_b32_e32 v207, v159
	v_pk_fma_f32 v[2:3], v[130:131], v[152:153], v[2:3] op_sel:[0,0,1] op_sel_hi:[1,1,0]
	v_pk_fma_f32 v[8:9], v[128:129], v[154:155], v[8:9] op_sel:[0,0,1] op_sel_hi:[1,1,0]
	v_pk_mul_f32 v[204:205], v[134:135], v[200:201]
	v_pk_mul_f32 v[216:217], v[132:133], v[206:207]
	v_mov_b32_e32 v159, v209
	v_pk_add_f32 v[2:3], v[2:3], v[8:9]
	v_pk_fma_f32 v[204:205], v[134:135], v[156:157], v[204:205] op_sel:[0,0,1] op_sel_hi:[1,1,0]
	v_pk_fma_f32 v[208:209], v[132:133], v[158:159], v[216:217] op_sel:[0,0,1] op_sel_hi:[1,1,0]
	v_pk_add_f32 v[0:1], v[0:1], v[2:3]
	v_pk_mul_f32 v[2:3], v[138:139], v[200:201]
	v_pk_mul_f32 v[8:9], v[136:137], v[206:207]
	v_pk_add_f32 v[204:205], v[204:205], v[208:209]
	v_pk_fma_f32 v[2:3], v[138:139], v[156:157], v[2:3] op_sel:[0,0,1] op_sel_hi:[1,1,0]
	v_pk_fma_f32 v[8:9], v[136:137], v[158:159], v[8:9] op_sel:[0,0,1] op_sel_hi:[1,1,0]
	v_pk_add_f32 v[14:15], v[14:15], v[204:205]
	s_waitcnt lgkmcnt(0)
	v_mov_b32_e32 v204, v210
	v_mov_b32_e32 v205, v161
	v_mov_b32_e32 v161, v211
	v_mov_b32_e32 v210, v212
	v_mov_b32_e32 v211, v163
	v_pk_add_f32 v[2:3], v[2:3], v[8:9]
	v_pk_mul_f32 v[208:209], v[6:7], v[204:205]
	v_pk_mul_f32 v[216:217], v[4:5], v[210:211]
	v_mov_b32_e32 v163, v213
	v_pk_add_f32 v[0:1], v[0:1], v[2:3]
	v_pk_mul_f32 v[2:3], v[12:13], v[204:205]
	v_pk_mul_f32 v[8:9], v[10:11], v[210:211]
	v_pk_fma_f32 v[208:209], v[6:7], v[160:161], v[208:209] op_sel:[0,0,1] op_sel_hi:[1,1,0]
	v_pk_fma_f32 v[212:213], v[4:5], v[162:163], v[216:217] op_sel:[0,0,1] op_sel_hi:[1,1,0]
	v_pk_fma_f32 v[2:3], v[12:13], v[160:161], v[2:3] op_sel:[0,0,1] op_sel_hi:[1,1,0]
	v_pk_fma_f32 v[8:9], v[10:11], v[162:163], v[8:9] op_sel:[0,0,1] op_sel_hi:[1,1,0]
	v_pk_add_f32 v[208:209], v[208:209], v[212:213]
	v_pk_add_f32 v[2:3], v[2:3], v[8:9]
	v_pk_add_f32 v[14:15], v[14:15], v[208:209]
	v_pk_add_f32 v[0:1], v[0:1], v[2:3]
	ds_read_b128 v[140:143], v25 offset:16384
	ds_read_b128 v[144:147], v25 offset:17408
	ds_read_b128 v[148:151], v25 offset:18432
	ds_read_b128 v[152:155], v25 offset:19456
	ds_read_b128 v[156:159], v25 offset:20480
	ds_read_b128 v[160:163], v25 offset:21504
	ds_read_b128 v[164:167], v25 offset:22528
	ds_read_b128 v[174:177], v25 offset:23552
	ds_read_b128 v[92:95], v25 offset:24576
	ds_read_b128 v[178:181], v25 offset:25600
	ds_read_b128 v[182:185], v25 offset:26624
	ds_read_b128 v[198:201], v25 offset:27648
	ds_read_b128 v[202:205], v25 offset:28672
	ds_read_b128 v[206:209], v25 offset:29696
	ds_read_b128 v[210:213], v25 offset:30720
	ds_read_b128 v[214:217], v25 offset:31744
	s_waitcnt lgkmcnt(7)
	v_mov_b32_e32 v2, v92
	v_mov_b32_e32 v3, v141
	v_mov_b32_e32 v218, v94
	v_mov_b32_e32 v219, v143
	v_pk_mul_f32 v[8:9], v[82:83], v[2:3]
	v_mov_b32_e32 v141, v93
	v_pk_mul_f32 v[92:93], v[80:81], v[218:219]
	v_mov_b32_e32 v143, v95
	v_pk_fma_f32 v[8:9], v[82:83], v[140:141], v[8:9] op_sel:[0,0,1] op_sel_hi:[1,1,0]
	v_pk_fma_f32 v[92:93], v[80:81], v[142:143], v[92:93] op_sel:[0,0,1] op_sel_hi:[1,1,0]
	s_waitcnt lgkmcnt(6)
	v_mov_b32_e32 v94, v178
	v_mov_b32_e32 v95, v145
	v_mov_b32_e32 v145, v179
	v_mov_b32_e32 v178, v180
	v_mov_b32_e32 v179, v147
	v_pk_add_f32 v[8:9], v[8:9], v[92:93]
	v_pk_mul_f32 v[92:93], v[90:91], v[94:95]
	v_pk_mul_f32 v[224:225], v[88:89], v[178:179]
	v_mov_b32_e32 v147, v181
	v_pk_fma_f32 v[92:93], v[90:91], v[144:145], v[92:93] op_sel:[0,0,1] op_sel_hi:[1,1,0]
	v_pk_fma_f32 v[180:181], v[88:89], v[146:147], v[224:225] op_sel:[0,0,1] op_sel_hi:[1,1,0]
	v_pk_add_f32 v[8:9], v[8:9], 0 op_sel_hi:[1,0]
	v_pk_add_f32 v[92:93], v[92:93], v[180:181]
	s_waitcnt lgkmcnt(5)
	v_mov_b32_e32 v180, v182
	v_mov_b32_e32 v181, v149
	v_mov_b32_e32 v149, v183
	v_mov_b32_e32 v182, v184
	v_mov_b32_e32 v183, v151
	v_pk_add_f32 v[8:9], v[8:9], v[92:93]
	v_pk_mul_f32 v[92:93], v[102:103], v[180:181]
	v_pk_mul_f32 v[224:225], v[100:101], v[182:183]
	v_mov_b32_e32 v151, v185
	v_pk_fma_f32 v[92:93], v[102:103], v[148:149], v[92:93] op_sel:[0,0,1] op_sel_hi:[1,1,0]
	v_pk_fma_f32 v[184:185], v[100:101], v[150:151], v[224:225] op_sel:[0,0,1] op_sel_hi:[1,1,0]
	v_pk_mul_f32 v[2:3], v[86:87], v[2:3]
	v_pk_add_f32 v[92:93], v[92:93], v[184:185]
	s_waitcnt lgkmcnt(4)
	v_mov_b32_e32 v184, v198
	v_mov_b32_e32 v185, v153
	v_mov_b32_e32 v153, v199
	v_mov_b32_e32 v198, v200
	v_mov_b32_e32 v199, v155
	v_pk_add_f32 v[8:9], v[8:9], v[92:93]
	v_pk_mul_f32 v[92:93], v[110:111], v[184:185]
	v_pk_mul_f32 v[224:225], v[108:109], v[198:199]
	v_mov_b32_e32 v155, v201
	v_pk_fma_f32 v[92:93], v[110:111], v[152:153], v[92:93] op_sel:[0,0,1] op_sel_hi:[1,1,0]
	v_pk_fma_f32 v[200:201], v[108:109], v[154:155], v[224:225] op_sel:[0,0,1] op_sel_hi:[1,1,0]
	v_pk_fma_f32 v[2:3], v[86:87], v[140:141], v[2:3] op_sel:[0,0,1] op_sel_hi:[1,1,0]
	v_pk_add_f32 v[92:93], v[92:93], v[200:201]
	s_waitcnt lgkmcnt(3)
	v_mov_b32_e32 v200, v202
	v_mov_b32_e32 v201, v157
	v_mov_b32_e32 v157, v203
	v_mov_b32_e32 v202, v204
	v_mov_b32_e32 v203, v159
	v_pk_add_f32 v[8:9], v[8:9], v[92:93]
	v_pk_mul_f32 v[92:93], v[118:119], v[200:201]
	v_pk_mul_f32 v[224:225], v[116:117], v[202:203]
	v_mov_b32_e32 v159, v205
	v_pk_fma_f32 v[92:93], v[118:119], v[156:157], v[92:93] op_sel:[0,0,1] op_sel_hi:[1,1,0]
	v_pk_fma_f32 v[204:205], v[116:117], v[158:159], v[224:225] op_sel:[0,0,1] op_sel_hi:[1,1,0]
	ds_bpermute_b32 v53, v41, v49
	v_pk_add_f32 v[92:93], v[92:93], v[204:205]
	s_waitcnt lgkmcnt(3)
	v_mov_b32_e32 v204, v206
	v_mov_b32_e32 v205, v161
	v_mov_b32_e32 v161, v207
	v_mov_b32_e32 v206, v208
	v_mov_b32_e32 v207, v163
	v_pk_add_f32 v[8:9], v[8:9], v[92:93]
	v_pk_mul_f32 v[92:93], v[126:127], v[204:205]
	v_pk_mul_f32 v[224:225], v[124:125], v[206:207]
	v_mov_b32_e32 v163, v209
	v_pk_fma_f32 v[92:93], v[126:127], v[160:161], v[92:93] op_sel:[0,0,1] op_sel_hi:[1,1,0]
	v_pk_fma_f32 v[208:209], v[124:125], v[162:163], v[224:225] op_sel:[0,0,1] op_sel_hi:[1,1,0]
	v_fmac_f32_e32 v45, v51, v29
	v_pk_add_f32 v[92:93], v[92:93], v[208:209]
	s_waitcnt lgkmcnt(2)
	v_mov_b32_e32 v208, v210
	v_mov_b32_e32 v209, v165
	v_mov_b32_e32 v165, v211
	v_mov_b32_e32 v210, v212
	v_mov_b32_e32 v211, v167
	v_pk_add_f32 v[8:9], v[8:9], v[92:93]
	v_pk_mul_f32 v[92:93], v[134:135], v[208:209]
	v_pk_mul_f32 v[224:225], v[132:133], v[210:211]
	v_mov_b32_e32 v167, v213
	v_pk_fma_f32 v[92:93], v[134:135], v[164:165], v[92:93] op_sel:[0,0,1] op_sel_hi:[1,1,0]
	v_pk_fma_f32 v[212:213], v[132:133], v[166:167], v[224:225] op_sel:[0,0,1] op_sel_hi:[1,1,0]
	v_pk_add_f32 v[92:93], v[92:93], v[212:213]
	s_waitcnt lgkmcnt(1)
	v_mov_b32_e32 v212, v214
	v_mov_b32_e32 v213, v175
	v_mov_b32_e32 v175, v215
	v_mov_b32_e32 v214, v216
	v_mov_b32_e32 v215, v177
	v_pk_add_f32 v[8:9], v[8:9], v[92:93]
	v_pk_mul_f32 v[92:93], v[6:7], v[212:213]
	v_pk_mul_f32 v[224:225], v[4:5], v[214:215]
	v_mov_b32_e32 v177, v217
	v_pk_fma_f32 v[92:93], v[6:7], v[174:175], v[92:93] op_sel:[0,0,1] op_sel_hi:[1,1,0]
	v_pk_fma_f32 v[216:217], v[4:5], v[176:177], v[224:225] op_sel:[0,0,1] op_sel_hi:[1,1,0]
	v_pk_add_f32 v[92:93], v[92:93], v[216:217]
	v_pk_add_f32 v[92:93], v[8:9], v[92:93]
	v_pk_mul_f32 v[8:9], v[84:85], v[218:219]
	v_pk_fma_f32 v[8:9], v[84:85], v[142:143], v[8:9] op_sel:[0,0,1] op_sel_hi:[1,1,0]
	v_pk_add_f32 v[2:3], v[2:3], v[8:9]
	v_pk_mul_f32 v[8:9], v[98:99], v[94:95]
	v_pk_mul_f32 v[94:95], v[96:97], v[178:179]
	v_pk_fma_f32 v[8:9], v[98:99], v[144:145], v[8:9] op_sel:[0,0,1] op_sel_hi:[1,1,0]
	v_pk_fma_f32 v[94:95], v[96:97], v[146:147], v[94:95] op_sel:[0,0,1] op_sel_hi:[1,1,0]
	v_pk_add_f32 v[2:3], v[2:3], 0 op_sel_hi:[1,0]
	v_pk_add_f32 v[8:9], v[8:9], v[94:95]
	v_pk_mul_f32 v[94:95], v[104:105], v[182:183]
	v_pk_add_f32 v[2:3], v[2:3], v[8:9]
	v_pk_mul_f32 v[8:9], v[106:107], v[180:181]
	v_pk_fma_f32 v[94:95], v[104:105], v[150:151], v[94:95] op_sel:[0,0,1] op_sel_hi:[1,1,0]
	v_pk_fma_f32 v[8:9], v[106:107], v[148:149], v[8:9] op_sel:[0,0,1] op_sel_hi:[1,1,0]
	v_pk_add_f32 v[8:9], v[8:9], v[94:95]
	v_pk_mul_f32 v[94:95], v[112:113], v[198:199]
	v_pk_add_f32 v[2:3], v[2:3], v[8:9]
	v_pk_mul_f32 v[8:9], v[114:115], v[184:185]
	v_pk_fma_f32 v[94:95], v[112:113], v[154:155], v[94:95] op_sel:[0,0,1] op_sel_hi:[1,1,0]
	v_pk_fma_f32 v[8:9], v[114:115], v[152:153], v[8:9] op_sel:[0,0,1] op_sel_hi:[1,1,0]
	v_pk_add_f32 v[8:9], v[8:9], v[94:95]
	v_pk_mul_f32 v[94:95], v[120:121], v[202:203]
	v_pk_add_f32 v[2:3], v[2:3], v[8:9]
	v_pk_mul_f32 v[8:9], v[122:123], v[200:201]
	v_pk_fma_f32 v[94:95], v[120:121], v[158:159], v[94:95] op_sel:[0,0,1] op_sel_hi:[1,1,0]
	v_pk_fma_f32 v[8:9], v[122:123], v[156:157], v[8:9] op_sel:[0,0,1] op_sel_hi:[1,1,0]
	v_pk_add_f32 v[8:9], v[8:9], v[94:95]
	v_pk_mul_f32 v[94:95], v[128:129], v[206:207]
	v_pk_add_f32 v[2:3], v[2:3], v[8:9]
	v_pk_mul_f32 v[8:9], v[130:131], v[204:205]
	v_pk_fma_f32 v[94:95], v[128:129], v[162:163], v[94:95] op_sel:[0,0,1] op_sel_hi:[1,1,0]
	v_pk_fma_f32 v[8:9], v[130:131], v[160:161], v[8:9] op_sel:[0,0,1] op_sel_hi:[1,1,0]
	v_pk_add_f32 v[8:9], v[8:9], v[94:95]
	v_pk_mul_f32 v[94:95], v[136:137], v[210:211]
	v_pk_add_f32 v[2:3], v[2:3], v[8:9]
	v_pk_mul_f32 v[8:9], v[138:139], v[208:209]
	v_pk_fma_f32 v[94:95], v[136:137], v[166:167], v[94:95] op_sel:[0,0,1] op_sel_hi:[1,1,0]
	v_pk_fma_f32 v[8:9], v[138:139], v[164:165], v[8:9] op_sel:[0,0,1] op_sel_hi:[1,1,0]
	v_pk_add_f32 v[8:9], v[8:9], v[94:95]
	v_pk_mul_f32 v[94:95], v[10:11], v[214:215]
	v_pk_add_f32 v[2:3], v[2:3], v[8:9]
	v_pk_mul_f32 v[8:9], v[12:13], v[212:213]
	v_pk_fma_f32 v[94:95], v[10:11], v[176:177], v[94:95] op_sel:[0,0,1] op_sel_hi:[1,1,0]
	v_pk_fma_f32 v[8:9], v[12:13], v[174:175], v[8:9] op_sel:[0,0,1] op_sel_hi:[1,1,0]
	ds_read_b128 v[140:143], v25 offset:32768
	ds_read_b128 v[144:147], v25 offset:33792
	ds_read_b128 v[148:151], v25 offset:34816
	ds_read_b128 v[152:155], v25 offset:35840
	ds_read_b128 v[156:159], v25 offset:36864
	ds_read_b128 v[160:163], v25 offset:37888
	ds_read_b128 v[164:167], v25 offset:38912
	ds_read_b128 v[174:177], v25 offset:39936
	ds_read_b128 v[178:181], v25 offset:40960
	ds_read_b128 v[182:185], v25 offset:41984
	ds_read_b128 v[198:201], v25 offset:43008
	ds_read_b128 v[202:205], v25 offset:44032
	ds_read_b128 v[206:209], v25 offset:45056
	ds_read_b128 v[210:213], v25 offset:46080
	ds_read_b128 v[214:217], v25 offset:47104
	ds_read_b128 v[224:227], v25 offset:48128
	v_pk_add_f32 v[8:9], v[8:9], v[94:95]
	v_pk_add_f32 v[2:3], v[2:3], v[8:9]
	s_waitcnt lgkmcnt(7)
	v_mov_b32_e32 v8, v178
	v_mov_b32_e32 v9, v141
	v_mov_b32_e32 v141, v179
	v_mov_b32_e32 v178, v180
	v_mov_b32_e32 v179, v143
	v_pk_mul_f32 v[94:95], v[82:83], v[8:9]
	v_pk_mul_f32 v[218:219], v[80:81], v[178:179]
	v_mov_b32_e32 v143, v181
	v_pk_fma_f32 v[94:95], v[82:83], v[140:141], v[94:95] op_sel:[0,0,1] op_sel_hi:[1,1,0]
	v_pk_fma_f32 v[180:181], v[80:81], v[142:143], v[218:219] op_sel:[0,0,1] op_sel_hi:[1,1,0]
	v_pk_mul_f32 v[8:9], v[86:87], v[8:9]
	v_pk_add_f32 v[94:95], v[94:95], v[180:181]
	s_waitcnt lgkmcnt(6)
	v_mov_b32_e32 v180, v182
	v_mov_b32_e32 v181, v145
	v_pk_mul_f32 v[218:219], v[90:91], v[180:181]
	v_mov_b32_e32 v145, v183
	v_pk_fma_f32 v[182:183], v[90:91], v[144:145], v[218:219] op_sel:[0,0,1] op_sel_hi:[1,1,0]
	v_mov_b32_e32 v218, v184
	v_mov_b32_e32 v219, v147
	v_pk_mul_f32 v[228:229], v[88:89], v[218:219]
	v_mov_b32_e32 v147, v185
	v_pk_fma_f32 v[184:185], v[88:89], v[146:147], v[228:229] op_sel:[0,0,1] op_sel_hi:[1,1,0]
	v_pk_add_f32 v[94:95], v[94:95], 0 op_sel_hi:[1,0]
	v_pk_add_f32 v[182:183], v[182:183], v[184:185]
	v_pk_fma_f32 v[8:9], v[86:87], v[140:141], v[8:9] op_sel:[0,0,1] op_sel_hi:[1,1,0]
	v_pk_add_f32 v[94:95], v[94:95], v[182:183]
	s_waitcnt lgkmcnt(5)
	v_mov_b32_e32 v182, v198
	v_mov_b32_e32 v183, v149
	v_mov_b32_e32 v149, v199
	v_mov_b32_e32 v198, v200
	v_mov_b32_e32 v199, v151
	v_pk_mul_f32 v[184:185], v[102:103], v[182:183]
	v_pk_mul_f32 v[228:229], v[100:101], v[198:199]
	v_mov_b32_e32 v151, v201
	v_pk_mul_f32 v[140:141], v[84:85], v[178:179]
	v_pk_fma_f32 v[184:185], v[102:103], v[148:149], v[184:185] op_sel:[0,0,1] op_sel_hi:[1,1,0]
	v_pk_fma_f32 v[200:201], v[100:101], v[150:151], v[228:229] op_sel:[0,0,1] op_sel_hi:[1,1,0]
	v_pk_fma_f32 v[140:141], v[84:85], v[142:143], v[140:141] op_sel:[0,0,1] op_sel_hi:[1,1,0]
	v_pk_add_f32 v[184:185], v[184:185], v[200:201]
	v_pk_add_f32 v[8:9], v[8:9], v[140:141]
	v_pk_mul_f32 v[140:141], v[98:99], v[180:181]
	v_pk_mul_f32 v[142:143], v[96:97], v[218:219]
	v_pk_add_f32 v[94:95], v[94:95], v[184:185]
	s_waitcnt lgkmcnt(4)
	v_mov_b32_e32 v184, v202
	v_mov_b32_e32 v185, v153
	v_mov_b32_e32 v153, v203
	v_mov_b32_e32 v202, v204
	v_mov_b32_e32 v203, v155
	v_pk_fma_f32 v[140:141], v[98:99], v[144:145], v[140:141] op_sel:[0,0,1] op_sel_hi:[1,1,0]
	v_pk_fma_f32 v[142:143], v[96:97], v[146:147], v[142:143] op_sel:[0,0,1] op_sel_hi:[1,1,0]
	v_pk_mul_f32 v[200:201], v[110:111], v[184:185]
	v_pk_mul_f32 v[228:229], v[108:109], v[202:203]
	v_mov_b32_e32 v155, v205
	v_pk_add_f32 v[8:9], v[8:9], 0 op_sel_hi:[1,0]
	v_pk_add_f32 v[140:141], v[140:141], v[142:143]
	v_pk_fma_f32 v[200:201], v[110:111], v[152:153], v[200:201] op_sel:[0,0,1] op_sel_hi:[1,1,0]
	v_pk_fma_f32 v[204:205], v[108:109], v[154:155], v[228:229] op_sel:[0,0,1] op_sel_hi:[1,1,0]
	v_pk_add_f32 v[8:9], v[8:9], v[140:141]
	v_pk_mul_f32 v[140:141], v[106:107], v[182:183]
	v_pk_mul_f32 v[142:143], v[104:105], v[198:199]
	v_pk_add_f32 v[200:201], v[200:201], v[204:205]
	v_pk_fma_f32 v[140:141], v[106:107], v[148:149], v[140:141] op_sel:[0,0,1] op_sel_hi:[1,1,0]
	v_pk_fma_f32 v[142:143], v[104:105], v[150:151], v[142:143] op_sel:[0,0,1] op_sel_hi:[1,1,0]
	v_pk_add_f32 v[94:95], v[94:95], v[200:201]
	s_waitcnt lgkmcnt(3)
	v_mov_b32_e32 v200, v206
	v_mov_b32_e32 v201, v157
	v_mov_b32_e32 v157, v207
	v_mov_b32_e32 v206, v208
	v_mov_b32_e32 v207, v159
	v_pk_add_f32 v[140:141], v[140:141], v[142:143]
	v_pk_mul_f32 v[204:205], v[118:119], v[200:201]
	v_pk_mul_f32 v[228:229], v[116:117], v[206:207]
	v_mov_b32_e32 v159, v209
	v_pk_add_f32 v[8:9], v[8:9], v[140:141]
	v_pk_mul_f32 v[140:141], v[114:115], v[184:185]
	v_pk_mul_f32 v[142:143], v[112:113], v[202:203]
	v_pk_fma_f32 v[204:205], v[118:119], v[156:157], v[204:205] op_sel:[0,0,1] op_sel_hi:[1,1,0]
	v_pk_fma_f32 v[208:209], v[116:117], v[158:159], v[228:229] op_sel:[0,0,1] op_sel_hi:[1,1,0]
	v_pk_fma_f32 v[140:141], v[114:115], v[152:153], v[140:141] op_sel:[0,0,1] op_sel_hi:[1,1,0]
	v_pk_fma_f32 v[142:143], v[112:113], v[154:155], v[142:143] op_sel:[0,0,1] op_sel_hi:[1,1,0]
	v_pk_add_f32 v[204:205], v[204:205], v[208:209]
	v_pk_add_f32 v[140:141], v[140:141], v[142:143]
	v_pk_add_f32 v[94:95], v[94:95], v[204:205]
	s_waitcnt lgkmcnt(2)
	v_mov_b32_e32 v204, v210
	v_mov_b32_e32 v205, v161
	v_mov_b32_e32 v161, v211
	v_mov_b32_e32 v210, v212
	v_mov_b32_e32 v211, v163
	v_pk_add_f32 v[8:9], v[8:9], v[140:141]
	v_pk_mul_f32 v[140:141], v[122:123], v[200:201]
	v_pk_mul_f32 v[142:143], v[120:121], v[206:207]
	v_pk_mul_f32 v[208:209], v[126:127], v[204:205]
	v_pk_mul_f32 v[228:229], v[124:125], v[210:211]
	v_mov_b32_e32 v163, v213
	v_pk_fma_f32 v[140:141], v[122:123], v[156:157], v[140:141] op_sel:[0,0,1] op_sel_hi:[1,1,0]
	v_pk_fma_f32 v[142:143], v[120:121], v[158:159], v[142:143] op_sel:[0,0,1] op_sel_hi:[1,1,0]
	v_pk_fma_f32 v[208:209], v[126:127], v[160:161], v[208:209] op_sel:[0,0,1] op_sel_hi:[1,1,0]
	v_pk_fma_f32 v[212:213], v[124:125], v[162:163], v[228:229] op_sel:[0,0,1] op_sel_hi:[1,1,0]
	v_pk_add_f32 v[140:141], v[140:141], v[142:143]
	v_pk_add_f32 v[208:209], v[208:209], v[212:213]
	v_pk_add_f32 v[8:9], v[8:9], v[140:141]
	v_pk_mul_f32 v[140:141], v[130:131], v[204:205]
	v_pk_mul_f32 v[142:143], v[128:129], v[210:211]
	v_pk_add_f32 v[94:95], v[94:95], v[208:209]
	s_waitcnt lgkmcnt(1)
	v_mov_b32_e32 v208, v214
	v_mov_b32_e32 v209, v165
	v_mov_b32_e32 v165, v215
	v_mov_b32_e32 v214, v216
	v_mov_b32_e32 v215, v167
	v_pk_fma_f32 v[140:141], v[130:131], v[160:161], v[140:141] op_sel:[0,0,1] op_sel_hi:[1,1,0]
	v_pk_fma_f32 v[142:143], v[128:129], v[162:163], v[142:143] op_sel:[0,0,1] op_sel_hi:[1,1,0]
	v_pk_mul_f32 v[212:213], v[134:135], v[208:209]
	v_pk_mul_f32 v[228:229], v[132:133], v[214:215]
	v_mov_b32_e32 v167, v217
	v_pk_add_f32 v[140:141], v[140:141], v[142:143]
	v_pk_fma_f32 v[212:213], v[134:135], v[164:165], v[212:213] op_sel:[0,0,1] op_sel_hi:[1,1,0]
	v_pk_fma_f32 v[216:217], v[132:133], v[166:167], v[228:229] op_sel:[0,0,1] op_sel_hi:[1,1,0]
	v_pk_add_f32 v[8:9], v[8:9], v[140:141]
	v_pk_mul_f32 v[140:141], v[138:139], v[208:209]
	v_pk_mul_f32 v[142:143], v[136:137], v[214:215]
	v_pk_add_f32 v[212:213], v[212:213], v[216:217]
	v_pk_fma_f32 v[140:141], v[138:139], v[164:165], v[140:141] op_sel:[0,0,1] op_sel_hi:[1,1,0]
	v_pk_fma_f32 v[142:143], v[136:137], v[166:167], v[142:143] op_sel:[0,0,1] op_sel_hi:[1,1,0]
	v_pk_add_f32 v[94:95], v[94:95], v[212:213]
	s_waitcnt lgkmcnt(0)
	v_mov_b32_e32 v212, v224
	v_mov_b32_e32 v213, v175
	v_mov_b32_e32 v175, v225
	v_mov_b32_e32 v224, v226
	v_mov_b32_e32 v225, v177
	v_pk_add_f32 v[140:141], v[140:141], v[142:143]
	v_pk_mul_f32 v[216:217], v[6:7], v[212:213]
	v_pk_mul_f32 v[228:229], v[4:5], v[224:225]
	v_mov_b32_e32 v177, v227
	v_pk_add_f32 v[8:9], v[8:9], v[140:141]
	v_pk_mul_f32 v[140:141], v[12:13], v[212:213]
	v_pk_mul_f32 v[142:143], v[10:11], v[224:225]
	v_pk_fma_f32 v[216:217], v[6:7], v[174:175], v[216:217] op_sel:[0,0,1] op_sel_hi:[1,1,0]
	v_pk_fma_f32 v[226:227], v[4:5], v[176:177], v[228:229] op_sel:[0,0,1] op_sel_hi:[1,1,0]
	v_pk_fma_f32 v[140:141], v[12:13], v[174:175], v[140:141] op_sel:[0,0,1] op_sel_hi:[1,1,0]
	v_pk_fma_f32 v[142:143], v[10:11], v[176:177], v[142:143] op_sel:[0,0,1] op_sel_hi:[1,1,0]
	v_pk_add_f32 v[216:217], v[216:217], v[226:227]
	v_pk_add_f32 v[140:141], v[140:141], v[142:143]
	v_pk_add_f32 v[94:95], v[94:95], v[216:217]
	v_pk_add_f32 v[8:9], v[8:9], v[140:141]
	ds_read_b128 v[140:143], v25 offset:49152
	ds_read_b128 v[144:147], v25 offset:50176
	ds_read_b128 v[148:151], v25 offset:51200
	ds_read_b128 v[152:155], v25 offset:52224
	ds_read_b128 v[156:159], v25 offset:53248
	ds_read_b128 v[160:163], v25 offset:54272
	ds_read_b128 v[164:167], v25 offset:55296
	ds_read_b128 v[174:177], v25 offset:56320
	ds_read_b128 v[178:181], v25 offset:57344
	ds_read_b128 v[182:185], v25 offset:58368
	ds_read_b128 v[198:201], v25 offset:59392
	ds_read_b128 v[202:205], v25 offset:60416
	ds_read_b128 v[206:209], v25 offset:61440
	ds_read_b128 v[210:213], v25 offset:62464
	ds_read_b128 v[214:217], v25 offset:63488
	ds_read_b128 v[224:227], v25 offset:64512
	s_waitcnt lgkmcnt(7)
	v_mov_b32_e32 v218, v178
	v_mov_b32_e32 v219, v141
	v_pk_mul_f32 v[228:229], v[82:83], v[218:219]
	v_mov_b32_e32 v141, v179
	v_mov_b32_e32 v178, v180
	v_mov_b32_e32 v179, v143
	v_pk_fma_f32 v[82:83], v[82:83], v[140:141], v[228:229] op_sel:[0,0,1] op_sel_hi:[1,1,0]
	v_pk_mul_f32 v[228:229], v[80:81], v[178:179]
	v_mov_b32_e32 v143, v181
	v_pk_fma_f32 v[80:81], v[80:81], v[142:143], v[228:229] op_sel:[0,0,1] op_sel_hi:[1,1,0]
	v_pk_add_f32 v[80:81], v[82:83], v[80:81]
	s_waitcnt lgkmcnt(6)
	v_mov_b32_e32 v82, v182
	v_mov_b32_e32 v83, v145
	v_pk_mul_f32 v[180:181], v[90:91], v[82:83]
	v_mov_b32_e32 v145, v183
	v_pk_fma_f32 v[90:91], v[90:91], v[144:145], v[180:181] op_sel:[0,0,1] op_sel_hi:[1,1,0]
	v_mov_b32_e32 v180, v184
	v_mov_b32_e32 v181, v147
	v_pk_mul_f32 v[182:183], v[88:89], v[180:181]
	v_mov_b32_e32 v147, v185
	v_pk_fma_f32 v[88:89], v[88:89], v[146:147], v[182:183] op_sel:[0,0,1] op_sel_hi:[1,1,0]
	v_pk_add_f32 v[80:81], v[80:81], 0 op_sel_hi:[1,0]
	v_pk_add_f32 v[88:89], v[90:91], v[88:89]
	v_pk_add_f32 v[80:81], v[80:81], v[88:89]
	s_waitcnt lgkmcnt(5)
	v_mov_b32_e32 v88, v198
	v_mov_b32_e32 v89, v149
	v_pk_mul_f32 v[90:91], v[102:103], v[88:89]
	v_mov_b32_e32 v149, v199
	v_pk_fma_f32 v[90:91], v[102:103], v[148:149], v[90:91] op_sel:[0,0,1] op_sel_hi:[1,1,0]
	v_mov_b32_e32 v102, v200
	v_mov_b32_e32 v103, v151
	v_pk_mul_f32 v[182:183], v[100:101], v[102:103]
	v_mov_b32_e32 v151, v201
	v_pk_fma_f32 v[100:101], v[100:101], v[150:151], v[182:183] op_sel:[0,0,1] op_sel_hi:[1,1,0]
	v_pk_add_f32 v[90:91], v[90:91], v[100:101]
	v_pk_add_f32 v[80:81], v[80:81], v[90:91]
	s_waitcnt lgkmcnt(4)
	v_mov_b32_e32 v90, v202
	v_mov_b32_e32 v91, v153
	v_pk_mul_f32 v[100:101], v[110:111], v[90:91]
	v_mov_b32_e32 v153, v203
	v_pk_fma_f32 v[100:101], v[110:111], v[152:153], v[100:101] op_sel:[0,0,1] op_sel_hi:[1,1,0]
	v_mov_b32_e32 v110, v204
	v_mov_b32_e32 v111, v155
	v_pk_mul_f32 v[182:183], v[108:109], v[110:111]
	v_mov_b32_e32 v155, v205
	v_pk_fma_f32 v[108:109], v[108:109], v[154:155], v[182:183] op_sel:[0,0,1] op_sel_hi:[1,1,0]
	v_pk_add_f32 v[100:101], v[100:101], v[108:109]
	v_pk_add_f32 v[80:81], v[80:81], v[100:101]
	s_waitcnt lgkmcnt(3)
	v_mov_b32_e32 v100, v206
	v_mov_b32_e32 v101, v157
	v_pk_mul_f32 v[108:109], v[118:119], v[100:101]
	v_mov_b32_e32 v157, v207
	v_pk_fma_f32 v[108:109], v[118:119], v[156:157], v[108:109] op_sel:[0,0,1] op_sel_hi:[1,1,0]
	v_mov_b32_e32 v118, v208
	v_mov_b32_e32 v119, v159
	v_pk_mul_f32 v[182:183], v[116:117], v[118:119]
	v_mov_b32_e32 v159, v209
	v_pk_fma_f32 v[116:117], v[116:117], v[158:159], v[182:183] op_sel:[0,0,1] op_sel_hi:[1,1,0]
	v_pk_add_f32 v[108:109], v[108:109], v[116:117]
	v_pk_add_f32 v[80:81], v[80:81], v[108:109]
	s_waitcnt lgkmcnt(2)
	v_mov_b32_e32 v108, v210
	v_mov_b32_e32 v109, v161
	v_pk_mul_f32 v[116:117], v[126:127], v[108:109]
	v_mov_b32_e32 v161, v211
	v_pk_fma_f32 v[116:117], v[126:127], v[160:161], v[116:117] op_sel:[0,0,1] op_sel_hi:[1,1,0]
	v_mov_b32_e32 v126, v212
	v_mov_b32_e32 v127, v163
	v_pk_mul_f32 v[182:183], v[124:125], v[126:127]
	v_mov_b32_e32 v163, v213
	v_pk_fma_f32 v[124:125], v[124:125], v[162:163], v[182:183] op_sel:[0,0,1] op_sel_hi:[1,1,0]
	v_pk_add_f32 v[116:117], v[116:117], v[124:125]
	v_pk_add_f32 v[80:81], v[80:81], v[116:117]
	s_waitcnt lgkmcnt(1)
	v_mov_b32_e32 v116, v214
	v_mov_b32_e32 v117, v165
	v_pk_mul_f32 v[124:125], v[134:135], v[116:117]
	v_mov_b32_e32 v165, v215
	v_pk_fma_f32 v[124:125], v[134:135], v[164:165], v[124:125] op_sel:[0,0,1] op_sel_hi:[1,1,0]
	v_mov_b32_e32 v134, v216
	v_mov_b32_e32 v135, v167
	v_pk_mul_f32 v[182:183], v[132:133], v[134:135]
	v_mov_b32_e32 v167, v217
	v_pk_fma_f32 v[132:133], v[132:133], v[166:167], v[182:183] op_sel:[0,0,1] op_sel_hi:[1,1,0]
	v_pk_add_f32 v[124:125], v[124:125], v[132:133]
	v_pk_add_f32 v[80:81], v[80:81], v[124:125]
	s_waitcnt lgkmcnt(0)
	v_mov_b32_e32 v124, v224
	v_mov_b32_e32 v125, v175
	v_pk_mul_f32 v[132:133], v[6:7], v[124:125]
	v_mov_b32_e32 v175, v225
	v_pk_fma_f32 v[6:7], v[6:7], v[174:175], v[132:133] op_sel:[0,0,1] op_sel_hi:[1,1,0]
	v_mov_b32_e32 v132, v226
	v_mov_b32_e32 v133, v177
	v_pk_mul_f32 v[182:183], v[4:5], v[132:133]
	v_mov_b32_e32 v177, v227
	v_pk_fma_f32 v[4:5], v[4:5], v[176:177], v[182:183] op_sel:[0,0,1] op_sel_hi:[1,1,0]
	v_pk_add_f32 v[4:5], v[6:7], v[4:5]
	v_pk_add_f32 v[6:7], v[80:81], v[4:5]
	v_pk_mul_f32 v[4:5], v[86:87], v[218:219]
	v_pk_mul_f32 v[80:81], v[84:85], v[178:179]
	v_pk_fma_f32 v[4:5], v[86:87], v[140:141], v[4:5] op_sel:[0,0,1] op_sel_hi:[1,1,0]
	v_pk_fma_f32 v[80:81], v[84:85], v[142:143], v[80:81] op_sel:[0,0,1] op_sel_hi:[1,1,0]
	v_pk_add_f32 v[4:5], v[4:5], v[80:81]
	v_pk_mul_f32 v[80:81], v[98:99], v[82:83]
	v_pk_mul_f32 v[82:83], v[96:97], v[180:181]
	v_pk_fma_f32 v[80:81], v[98:99], v[144:145], v[80:81] op_sel:[0,0,1] op_sel_hi:[1,1,0]
	v_pk_fma_f32 v[82:83], v[96:97], v[146:147], v[82:83] op_sel:[0,0,1] op_sel_hi:[1,1,0]
	v_pk_add_f32 v[4:5], v[4:5], 0 op_sel_hi:[1,0]
	v_pk_add_f32 v[80:81], v[80:81], v[82:83]
	v_pk_mul_f32 v[82:83], v[104:105], v[102:103]
	v_pk_add_f32 v[4:5], v[4:5], v[80:81]
	v_pk_mul_f32 v[80:81], v[106:107], v[88:89]
	v_pk_fma_f32 v[82:83], v[104:105], v[150:151], v[82:83] op_sel:[0,0,1] op_sel_hi:[1,1,0]
	v_pk_fma_f32 v[80:81], v[106:107], v[148:149], v[80:81] op_sel:[0,0,1] op_sel_hi:[1,1,0]
	v_pk_add_f32 v[80:81], v[80:81], v[82:83]
	v_pk_mul_f32 v[82:83], v[112:113], v[110:111]
	v_pk_add_f32 v[4:5], v[4:5], v[80:81]
	v_pk_mul_f32 v[80:81], v[114:115], v[90:91]
	v_pk_fma_f32 v[82:83], v[112:113], v[154:155], v[82:83] op_sel:[0,0,1] op_sel_hi:[1,1,0]
	v_pk_fma_f32 v[80:81], v[114:115], v[152:153], v[80:81] op_sel:[0,0,1] op_sel_hi:[1,1,0]
	v_pk_add_f32 v[80:81], v[80:81], v[82:83]
	v_pk_mul_f32 v[82:83], v[120:121], v[118:119]
	v_pk_add_f32 v[4:5], v[4:5], v[80:81]
	v_pk_mul_f32 v[80:81], v[122:123], v[100:101]
	v_pk_fma_f32 v[82:83], v[120:121], v[158:159], v[82:83] op_sel:[0,0,1] op_sel_hi:[1,1,0]
	v_pk_fma_f32 v[80:81], v[122:123], v[156:157], v[80:81] op_sel:[0,0,1] op_sel_hi:[1,1,0]
	v_pk_add_f32 v[80:81], v[80:81], v[82:83]
	v_pk_mul_f32 v[82:83], v[128:129], v[126:127]
	v_pk_add_f32 v[4:5], v[4:5], v[80:81]
	v_pk_mul_f32 v[80:81], v[130:131], v[108:109]
	v_pk_fma_f32 v[82:83], v[128:129], v[162:163], v[82:83] op_sel:[0,0,1] op_sel_hi:[1,1,0]
	v_pk_fma_f32 v[80:81], v[130:131], v[160:161], v[80:81] op_sel:[0,0,1] op_sel_hi:[1,1,0]
	v_pk_add_f32 v[80:81], v[80:81], v[82:83]
	v_pk_mul_f32 v[82:83], v[136:137], v[134:135]
	v_pk_add_f32 v[4:5], v[4:5], v[80:81]
	v_pk_mul_f32 v[80:81], v[138:139], v[116:117]
	v_pk_fma_f32 v[82:83], v[136:137], v[166:167], v[82:83] op_sel:[0,0,1] op_sel_hi:[1,1,0]
	v_pk_fma_f32 v[80:81], v[138:139], v[164:165], v[80:81] op_sel:[0,0,1] op_sel_hi:[1,1,0]
	v_pk_add_f32 v[80:81], v[80:81], v[82:83]
	v_pk_add_f32 v[4:5], v[4:5], v[80:81]
	v_pk_mul_f32 v[80:81], v[12:13], v[124:125]
	v_pk_fma_f32 v[12:13], v[12:13], v[174:175], v[80:81] op_sel:[0,0,1] op_sel_hi:[1,1,0]
	v_pk_mul_f32 v[80:81], v[10:11], v[132:133]
	v_pk_fma_f32 v[10:11], v[10:11], v[176:177], v[80:81] op_sel:[0,0,1] op_sel_hi:[1,1,0]
	v_pk_add_f32 v[10:11], v[12:13], v[10:11]
	v_pk_add_f32 v[4:5], v[4:5], v[10:11]
	v_cmp_eq_u32_e64 s[46:47], 8, v20
	s_nop 1
	v_cndmask_b32_e64 v10, v14, v0, s[46:47]
	ds_bpermute_b32 v10, v39, v10
	v_cmp_eq_u32_e64 s[46:47], 8, v22
	s_nop 1
	v_cndmask_b32_e64 v11, v14, v0, s[46:47]
	s_waitcnt lgkmcnt(0)
	v_add_f32_e32 v12, v11, v10
	v_cmp_eq_u32_e64 s[46:47], 9, v24
	s_nop 1
	v_cndmask_b32_e64 v10, v15, v1, s[46:47]
	ds_bpermute_b32 v10, v39, v10
	v_cmp_eq_u32_e64 s[46:47], 9, v26
	s_nop 1
	v_cndmask_b32_e64 v11, v15, v1, s[46:47]
	s_waitcnt lgkmcnt(0)
	v_add_f32_e32 v13, v11, v10
	v_cmp_eq_u32_e64 s[46:47], 10, v28
	s_nop 1
	v_cndmask_b32_e64 v10, v92, v2, s[46:47]
	ds_bpermute_b32 v10, v39, v10
	v_cmp_eq_u32_e64 s[46:47], 10, v30
	s_nop 1
	v_cndmask_b32_e64 v11, v92, v2, s[46:47]
	s_waitcnt lgkmcnt(0)
	v_add_f32_e32 v14, v11, v10
	v_cmp_eq_u32_e64 s[46:47], 11, v32
	s_nop 1
	v_cndmask_b32_e64 v10, v93, v3, s[46:47]
	ds_bpermute_b32 v10, v39, v10
	v_cmp_eq_u32_e64 s[46:47], 11, v34
	s_nop 1
	v_cndmask_b32_e64 v11, v93, v3, s[46:47]
	s_waitcnt lgkmcnt(0)
	v_add_f32_e32 v15, v11, v10
	v_cmp_eq_u32_e64 s[46:47], 12, v36
	s_nop 1
	v_cndmask_b32_e64 v10, v94, v8, s[46:47]
	ds_bpermute_b32 v10, v39, v10
	v_cmp_eq_u32_e64 s[46:47], 12, v38
	s_nop 1
	v_cndmask_b32_e64 v11, v94, v8, s[46:47]
	s_waitcnt lgkmcnt(0)
	v_add_f32_e32 v10, v11, v10
	v_cmp_eq_u32_e64 s[46:47], 13, v40
	s_nop 1
	v_cndmask_b32_e64 v11, v95, v9, s[46:47]
	ds_bpermute_b32 v11, v39, v11
	v_cmp_eq_u32_e64 s[46:47], 13, v42
	s_nop 1
	v_cndmask_b32_e64 v55, v95, v9, s[46:47]
	s_waitcnt lgkmcnt(0)
	v_add_f32_e32 v11, v55, v11
	v_cmp_eq_u32_e64 s[46:47], 14, v44
	s_nop 1
	v_cndmask_b32_e64 v55, v6, v4, s[46:47]
	ds_bpermute_b32 v55, v39, v55
	v_cmp_eq_u32_e64 s[46:47], 14, v46
	s_nop 1
	v_cndmask_b32_e64 v6, v6, v4, s[46:47]
	s_waitcnt lgkmcnt(0)
	v_add_f32_e32 v6, v6, v55
	v_cmp_eq_u32_e64 s[46:47], 15, v48
	s_nop 1
	v_cndmask_b32_e64 v55, v7, v5, s[46:47]
	ds_bpermute_b32 v55, v39, v55
	v_cmp_eq_u32_e64 s[46:47], 15, v50
	s_nop 1
	v_cndmask_b32_e64 v7, v7, v5, s[46:47]
	s_waitcnt lgkmcnt(0)
	v_add_f32_e32 v7, v7, v55
	v_cmp_eq_u32_e64 s[46:47], 4, v52
	s_nop 1
	v_cndmask_b32_e64 v55, v12, v10, s[46:47]
	ds_bpermute_b32 v55, v37, v55
	v_cmp_eq_u32_e64 s[46:47], 4, v54
	s_nop 1
	v_cndmask_b32_e64 v12, v12, v10, s[46:47]
	s_waitcnt lgkmcnt(0)
	v_add_f32_e32 v12, v12, v55
	v_cmp_eq_u32_e64 s[46:47], 5, v56
	s_nop 1
	v_cndmask_b32_e64 v55, v13, v11, s[46:47]
	ds_bpermute_b32 v55, v37, v55
	v_cmp_eq_u32_e64 s[46:47], 5, v58
	s_nop 1
	v_cndmask_b32_e64 v13, v13, v11, s[46:47]
	s_waitcnt lgkmcnt(0)
	v_add_f32_e32 v13, v13, v55
	v_cmp_eq_u32_e64 s[46:47], 6, v60
	s_nop 1
	v_cndmask_b32_e64 v55, v14, v6, s[46:47]
	ds_bpermute_b32 v55, v37, v55
	v_cmp_eq_u32_e64 s[46:47], 6, v62
	s_nop 1
	v_cndmask_b32_e64 v14, v14, v6, s[46:47]
	s_waitcnt lgkmcnt(0)
	v_add_f32_e32 v14, v14, v55
	v_cmp_eq_u32_e64 s[46:47], 7, v64
	s_nop 1
	v_cndmask_b32_e64 v55, v15, v7, s[46:47]
	ds_bpermute_b32 v55, v37, v55
	v_cmp_eq_u32_e64 s[46:47], 7, v66
	s_nop 1
	v_cndmask_b32_e64 v15, v15, v7, s[46:47]
	s_waitcnt lgkmcnt(0)
	v_add_f32_e32 v15, v15, v55
	v_cmp_eq_u32_e64 s[46:47], 2, v68
	s_nop 1
	v_cndmask_b32_e64 v55, v12, v14, s[46:47]
	ds_bpermute_b32 v55, v41, v55
	v_cmp_eq_u32_e64 s[46:47], 2, v70
	s_nop 1
	v_cndmask_b32_e64 v12, v12, v14, s[46:47]
	s_waitcnt lgkmcnt(0)
	v_add_f32_e32 v12, v12, v55
	v_cmp_eq_u32_e64 s[46:47], 3, v72
	s_nop 1
	v_cndmask_b32_e64 v55, v13, v15, s[46:47]
	ds_bpermute_b32 v55, v41, v55
	v_cmp_eq_u32_e64 s[46:47], 3, v74
	s_nop 1
	v_cndmask_b32_e64 v13, v13, v15, s[46:47]
	s_waitcnt lgkmcnt(0)
	v_add_f32_e32 v13, v13, v55
	v_cmp_ne_u64_e64 s[46:47], 0, v[76:77]
	s_nop 1
	v_cndmask_b32_e64 v55, v12, v13, s[46:47]
	v_cmp_eq_u32_e64 s[46:47], 2, v76
	s_nop 1
	v_cndmask_b32_e64 v55, v55, v14, s[46:47]
	v_cmp_eq_u32_e64 s[46:47], 3, v76
	s_nop 1
	v_cndmask_b32_e64 v55, v55, v15, s[46:47]
	v_cmp_eq_u32_e64 s[46:47], 4, v76
	s_nop 1
	v_cndmask_b32_e64 v55, v55, v10, s[46:47]
	v_cmp_eq_u32_e64 s[46:47], 5, v76
	s_nop 1
	v_cndmask_b32_e64 v55, v55, v11, s[46:47]
	v_cmp_eq_u32_e64 s[46:47], 6, v76
	s_nop 1
	v_cndmask_b32_e64 v55, v55, v6, s[46:47]
	v_cmp_eq_u32_e64 s[46:47], 7, v76
	s_nop 1
	v_cndmask_b32_e64 v55, v55, v7, s[46:47]
	v_cmp_eq_u32_e64 s[46:47], 8, v76
	s_nop 1
	v_cndmask_b32_e64 v55, v55, v0, s[46:47]
	v_cmp_eq_u32_e64 s[46:47], 9, v76
	s_nop 1
	v_cndmask_b32_e64 v55, v55, v1, s[46:47]
	v_cmp_eq_u32_e64 s[46:47], 10, v76
	s_nop 1
	v_cndmask_b32_e64 v55, v55, v2, s[46:47]
	v_cmp_eq_u32_e64 s[46:47], 11, v76
	s_nop 1
	v_cndmask_b32_e64 v55, v55, v3, s[46:47]
	v_cmp_eq_u32_e64 s[46:47], 12, v76
	s_nop 1
	v_cndmask_b32_e64 v55, v55, v8, s[46:47]
	v_cmp_eq_u32_e64 s[46:47], 13, v76
	s_nop 1
	v_cndmask_b32_e64 v55, v55, v9, s[46:47]
	v_cmp_ne_u64_e64 s[46:47], 0, v[78:79]
	s_nop 1
	v_cndmask_b32_e64 v12, v12, v13, s[46:47]
	v_cmp_eq_u32_e64 s[46:47], 2, v78
	s_nop 1
	v_cndmask_b32_e64 v12, v12, v14, s[46:47]
	v_cmp_eq_u32_e64 s[46:47], 3, v78
	s_nop 1
	v_cndmask_b32_e64 v12, v12, v15, s[46:47]
	v_cmp_eq_u32_e64 s[46:47], 4, v78
	s_nop 1
	v_cndmask_b32_e64 v10, v12, v10, s[46:47]
	v_cmp_eq_u32_e64 s[46:47], 5, v78
	s_nop 1
	v_cndmask_b32_e64 v10, v10, v11, s[46:47]
	v_cmp_eq_u32_e64 s[46:47], 6, v78
	s_nop 1
	v_cndmask_b32_e64 v6, v10, v6, s[46:47]
	v_cmp_eq_u32_e64 s[46:47], 7, v78
	s_nop 1
	v_cndmask_b32_e64 v6, v6, v7, s[46:47]
	v_cmp_eq_u32_e64 s[46:47], 8, v78
	s_nop 1
	v_cndmask_b32_e64 v0, v6, v0, s[46:47]
	v_cmp_eq_u32_e64 s[46:47], 9, v78
	s_nop 1
	v_cndmask_b32_e64 v0, v0, v1, s[46:47]
	v_cmp_eq_u32_e64 s[46:47], 10, v78
	s_nop 1
	v_cndmask_b32_e64 v0, v0, v2, s[46:47]
	v_cmp_eq_u32_e64 s[46:47], 11, v78
	v_fma_f32 v2, -v43, v45, v47
	s_nop 0
	v_cndmask_b32_e64 v0, v0, v3, s[46:47]
	v_cmp_eq_u32_e64 s[46:47], 12, v78
	v_add_f32_e32 v3, v49, v53
	s_nop 0
	v_cndmask_b32_e64 v0, v0, v8, s[46:47]
	v_cmp_eq_u32_e64 s[46:47], 13, v78
	s_nop 1
	v_cndmask_b32_e64 v0, v0, v9, s[46:47]
	v_cmp_eq_u32_e64 s[46:47], 14, v78
	s_nop 1
	v_cndmask_b32_e64 v0, v0, v4, s[46:47]
	v_cmp_eq_u32_e64 s[46:47], 15, v78
	s_nop 1
	v_cndmask_b32_e64 v0, v0, v5, s[46:47]
	ds_bpermute_b32 v0, v35, v0
	v_cmp_eq_u32_e64 s[46:47], 14, v76
	s_nop 1
	v_cndmask_b32_e64 v1, v55, v4, s[46:47]
	v_cmp_eq_u32_e64 s[46:47], 15, v76
	ds_bpermute_b32 v4, v37, v3
	s_nop 0
	v_cndmask_b32_e64 v1, v1, v5, s[46:47]
	s_waitcnt lgkmcnt(1)
	v_add_f32_e32 v0, v1, v0
	ds_bpermute_b32 v1, v33, v0
	s_waitcnt lgkmcnt(0)
	v_add_f32_e32 v5, v0, v1
	ds_bpermute_b32 v6, v31, v5
	v_div_fmas_f32 v0, v2, v29, v45
	v_div_fixup_f32 v8, v0, v27, 1.0
	v_add_f32_e32 v0, v3, v4
	ds_bpermute_b32 v1, v39, v0
	s_waitcnt lgkmcnt(1)
	v_add_f32_e32 v2, v5, v6
	s_nop 0
	v_readlane_b32 s1, v2, 0
	v_readlane_b32 s0, v2, 4
	v_readlane_b32 s8, v2, 32
	v_readlane_b32 s9, v2, 36
	v_pk_mul_f32 v[6:7], v[8:9], s[0:1] op_sel_hi:[0,1]
	v_readlane_b32 s0, v2, 8
	v_cmp_gt_f32_e32 vcc, v6, v7
	v_readlane_b32 s10, v2, 40
	v_mul_f32_e32 v3, s0, v8
	v_readlane_b32 s0, v2, 12
	v_readlane_b32 s11, v2, 44
	v_readlane_b32 s12, v2, 48
	v_mul_f32_e32 v4, s0, v8
	v_readlane_b32 s0, v2, 16
	v_readlane_b32 s13, v2, 52
	v_readlane_b32 s14, v2, 56
	v_mul_f32_e32 v9, s0, v8
	v_readlane_b32 s0, v2, 20
	v_readlane_b32 s15, v2, 60
	v_cndmask_b32_e64 v12, 0, 1, vcc
	v_mul_f32_e32 v10, s0, v8
	v_readlane_b32 s0, v2, 24
	v_cmp_lt_f32_e64 s[52:53], s33, v7
	s_nop 0
	v_mul_f32_e32 v11, s0, v8
	v_readlane_b32 s0, v2, 28
	v_cndmask_b32_e32 v2, v7, v6, vcc
	v_cmp_gt_f32_e32 vcc, v3, v2
	v_mul_f32_e32 v5, s0, v8
	s_nop 0
	v_cndmask_b32_e32 v2, v2, v3, vcc
	v_cndmask_b32_e64 v12, v12, 2, vcc
	v_cmp_gt_f32_e32 vcc, v4, v2
	s_nop 1
	v_cndmask_b32_e32 v2, v2, v4, vcc
	v_cndmask_b32_e64 v12, v12, 3, vcc
	v_cmp_gt_f32_e32 vcc, v9, v2
	s_nop 1
	v_cndmask_b32_e32 v2, v2, v9, vcc
	v_cndmask_b32_e64 v12, v12, 4, vcc
	v_cmp_gt_f32_e32 vcc, v10, v2
	s_nop 1
	v_cndmask_b32_e32 v2, v2, v10, vcc
	v_cndmask_b32_e64 v12, v12, 5, vcc
	v_cmp_ngt_f32_e32 vcc, v11, v2
	s_nop 1
	v_cndmask_b32_e32 v2, v11, v2, vcc
	v_cndmask_b32_e32 v12, 6, v12, vcc
	v_cmp_gt_f32_e64 s[48:49], v5, v2
	s_or_b64 s[0:1], vcc, s[48:49]
	v_cmp_ngt_f32_e64 s[46:47], v5, v2
	v_cndmask_b32_e64 v172, v12, 7, s[48:49]
	v_cmp_ne_u32_e64 s[50:51], 0, v172
	s_and_b64 s[50:51], s[50:51], s[52:53]
	s_nop 0
	v_cndmask_b32_e64 v7, v196, v7, s[50:51]
	v_cmp_ne_u32_e64 s[50:51], 1, v172
	v_cmp_gt_f32_e64 s[52:53], v6, v7
	s_and_b64 s[50:51], s[50:51], s[52:53]
	v_cndmask_b32_e64 v6, v7, v6, s[50:51]
	v_cndmask_b32_e64 v7, 0, 1, s[50:51]
	v_cmp_ne_u32_e64 s[50:51], 2, v172
	v_cmp_gt_f32_e64 s[52:53], v3, v6
	s_and_b64 s[50:51], s[50:51], s[52:53]
	v_cndmask_b32_e64 v3, v6, v3, s[50:51]
	v_cndmask_b32_e64 v6, v7, 2, s[50:51]
	v_cmp_ne_u32_e64 s[50:51], 3, v172
	v_cmp_gt_f32_e64 s[52:53], v4, v3
	s_and_b64 s[50:51], s[50:51], s[52:53]
	v_cndmask_b32_e64 v3, v3, v4, s[50:51]
	v_cndmask_b32_e64 v4, v6, 3, s[50:51]
	v_cmp_ne_u32_e64 s[50:51], 4, v172
	v_cmp_gt_f32_e64 s[52:53], v9, v3
	s_and_b64 s[50:51], s[50:51], s[52:53]
	v_cndmask_b32_e64 v3, v3, v9, s[50:51]
	v_cndmask_b32_e64 v4, v4, 4, s[50:51]
	v_cmp_ne_u32_e64 s[50:51], 5, v172
	v_cmp_gt_f32_e64 s[52:53], v10, v3
	s_and_b64 s[50:51], s[50:51], s[52:53]
	v_cndmask_b32_e64 v3, v3, v10, s[50:51]
	v_cmp_gt_f32_e32 vcc, v11, v3
	v_cndmask_b32_e64 v4, v4, 5, s[50:51]
	s_and_b64 vcc, s[0:1], vcc
	v_cndmask_b32_e32 v43, v3, v11, vcc
	v_cndmask_b32_e64 v9, v4, 6, vcc
	s_and_saveexec_b64 s[0:1], s[46:47]
	s_cbranch_execz .LBB0_1340
	v_cmp_gt_f32_e32 vcc, v5, v43
	s_and_saveexec_b64 s[2:3], vcc
	v_mov_b32_e32 v9, 7
	v_mov_b32_e32 v43, v5
	s_or_b64 exec, exec, s[2:3]
	v_mov_b32_e32 v5, v2

.LBB0_1348:
	s_or_b64 exec, exec, s[0:1]
	s_waitcnt lgkmcnt(1)
	v_readfirstlane_b32 s19, v0
	s_waitcnt lgkmcnt(0)
	v_readfirstlane_b32 s54, v1
	s_or_b32 s26, s18, 2
	s_max_i32 s12, s26, 4
	s_add_i32 s12, s12, -4
	s_mov_b32 s13, s60
	s_lshl_b64 s[96:97], s[12:13], 12
	s_max_i32 s12, s26, 3
	s_add_i32 s12, s12, -3
	s_lshl_b64 s[52:53], s[12:13], 12
	s_max_i32 s12, s26, 2
	s_add_i32 s12, s12, -2
	s_lshl_b64 s[50:51], s[12:13], 12
	s_max_i32 s12, s26, 1
	s_add_i32 s12, s12, -1
	s_lshl_b64 s[48:49], s[12:13], 12
	s_max_i32 s12, s26, 0
	s_lshl_b64 s[46:47], s[12:13], 12
	s_max_i32 s12, s26, -1
	s_and_b32 s14, s26, 0x7fe
	s_add_i32 s12, s12, 1
	s_lshl_b64 s[92:93], s[12:13], 12
	s_min_u32 s12, s14, 15
	s_add_i32 s12, s12, 1
	s_min_u32 s13, s14, 14
	v_cvt_f32_ubyte0_e32 v0, s12
	s_add_i32 s15, s13, 2
	v_div_scale_f32 v1, s[12:13], v0, v0, 1.0
	v_rcp_f32_e32 v2, v1
	s_max_i32 s0, s26, 15
	s_add_i32 s0, s0, -15
	s_mov_b32 s1, s60
	v_fma_f32 v3, -v1, v2, 1.0
	v_fmac_f32_e32 v2, v3, v2
	v_div_scale_f32 v3, vcc, 1.0, v0, 1.0
	v_mul_f32_e32 v10, v3, v2
	v_fma_f32 v11, -v1, v10, v3
	v_fmac_f32_e32 v10, v11, v2
	v_fma_f32 v1, -v1, v10, v3
	v_div_fmas_f32 v1, v1, v2, v10
	v_div_fixup_f32 v90, v1, v0, 1.0
	v_cvt_f32_ubyte0_e32 v0, s15
	v_div_scale_f32 v1, s[12:13], v0, v0, 1.0
	v_rcp_f32_e32 v2, v1
	s_min_u32 s12, s14, 7
	s_add_i32 s12, s12, 1
	s_min_u32 s13, s14, 6
	v_fma_f32 v3, -v1, v2, 1.0
	v_fmac_f32_e32 v2, v3, v2
	v_div_scale_f32 v3, vcc, 1.0, v0, 1.0
	v_mul_f32_e32 v10, v3, v2
	v_fma_f32 v11, -v1, v10, v3
	v_fmac_f32_e32 v10, v11, v2
	v_fma_f32 v1, -v1, v10, v3
	v_div_fmas_f32 v1, v1, v2, v10
	v_div_fixup_f32 v92, v1, v0, 1.0
	v_cvt_f32_ubyte0_e32 v0, s12
	s_add_i32 s15, s13, 2
	v_div_scale_f32 v1, s[12:13], v0, v0, 1.0
	v_rcp_f32_e32 v2, v1
	s_lshl_b64 s[42:43], s[0:1], 12
	s_max_i32 s0, s26, 14
	s_add_i32 s0, s0, -14
	v_fma_f32 v3, -v1, v2, 1.0
	v_fmac_f32_e32 v2, v3, v2
	v_div_scale_f32 v3, vcc, 1.0, v0, 1.0
	v_mul_f32_e32 v10, v3, v2
	v_fma_f32 v11, -v1, v10, v3
	v_fmac_f32_e32 v10, v11, v2
	v_fma_f32 v1, -v1, v10, v3
	v_div_fmas_f32 v1, v1, v2, v10
	v_div_fixup_f32 v118, v1, v0, 1.0
	v_cvt_f32_ubyte0_e32 v0, s15
	v_div_scale_f32 v1, s[12:13], v0, v0, 1.0
	v_rcp_f32_e32 v2, v1
	s_lshl_b64 s[88:89], s[0:1], 12
	s_max_i32 s0, s26, 13
	s_add_i32 s0, s0, -13
	s_lshl_b64 s[36:37], s[0:1], 12
	s_max_i32 s0, s26, 12
	v_fma_f32 v3, -v1, v2, 1.0
	s_add_i32 s0, s0, -12
	v_fmac_f32_e32 v2, v3, v2
	v_div_scale_f32 v3, vcc, 1.0, v0, 1.0
	s_lshl_b64 s[78:79], s[0:1], 12
	s_max_i32 s0, s26, 11
	v_mul_f32_e32 v10, v3, v2
	s_add_i32 s0, s0, -11
	v_fma_f32 v11, -v1, v10, v3
	s_lshl_b64 s[76:77], s[0:1], 12
	s_max_i32 s0, s26, 10
	v_fmac_f32_e32 v10, v11, v2
	s_add_i32 s0, s0, -10
	v_fma_f32 v1, -v1, v10, v3
	s_min_u32 s12, s14, 3
	s_lshl_b64 s[10:11], s[0:1], 12
	s_max_i32 s0, s26, 9
	v_div_fmas_f32 v1, v1, v2, v10
	s_add_i32 s12, s12, 1
	s_add_i32 s0, s0, -9
	v_div_fixup_f32 v120, v1, v0, 1.0
	v_cvt_f32_ubyte0_e32 v0, s12
	s_lshl_b64 s[8:9], s[0:1], 12
	s_max_i32 s0, s26, 8
	v_div_scale_f32 v1, s[12:13], v0, v0, 1.0
	s_add_i32 s0, s0, -8
	v_rcp_f32_e32 v2, v1
	s_lshl_b64 s[44:45], s[0:1], 12
	s_max_i32 s0, s26, 7
	s_add_i32 s0, s0, -7
	s_lshl_b64 s[86:87], s[0:1], 12
	s_max_i32 s0, s26, 6
	s_max_i32 s2, s26, 5
	s_add_i32 s0, s0, -6
	s_add_i32 s2, s2, -5
	s_mov_b32 s3, s60
	v_fma_f32 v3, -v1, v2, 1.0
	s_ashr_i32 s27, s26, 31
	s_lshl_b64 s[0:1], s[0:1], 12
	s_lshl_b64 s[2:3], s[2:3], 12
	v_fmac_f32_e32 v2, v3, v2
	v_div_scale_f32 v3, vcc, 1.0, v0, 1.0
	s_lshl_b64 s[12:13], s[26:27], 12
	v_mul_f32_e32 v10, v3, v2
	s_add_u32 s30, s4, s12
	v_fma_f32 v11, -v1, v10, v3
	s_addc_u32 s31, s5, s13
	s_or_b32 s24, s18, 3
	v_fmac_f32_e32 v10, v11, v2
	s_ashr_i32 s25, s24, 31
	v_fma_f32 v1, -v1, v10, v3
	s_lshl_b64 s[12:13], s[24:25], 12
	v_mov_b32_e32 v55, v21
	v_div_fmas_f32 v1, v1, v2, v10
	s_add_u32 s28, s4, s12
	s_addc_u32 s29, s5, s13
	v_lshlrev_b32_e32 v10, 2, v55
	v_ashrrev_i32_e32 v11, 31, v10
	v_readlane_b32 s12, v253, 40
	v_lshlrev_b64 v[82:83], 1, v[10:11]
	v_readlane_b32 s13, v253, 41
	v_mov_b32_e32 v53, s7
	v_div_fixup_f32 v102, v1, v0, 1.0
	v_lshl_add_u64 v[10:11], s[12:13], 0, v[82:83]
	v_lshl_add_u64 v[236:237], v[10:11], 0, s[92:93]
	global_load_dwordx2 v[236:237], v[236:237], off
	v_lshl_add_u64 v[238:239], v[10:11], 0, s[48:49]
	global_load_dwordx2 v[238:239], v[238:239], off
	v_lshl_add_u64 v[240:241], v[10:11], 0, s[46:47]
	global_load_dwordx2 v[240:241], v[240:241], off
	v_lshl_add_u64 v[242:243], s[30:31], 0, v[82:83]
	global_load_dwordx2 v[242:243], v[242:243], off
	s_nop 0
	s_nop 0
	s_nop 0
	s_nop 0
	s_nop 0
	ds_read_b96 v[0:2], v53 offset:64
	s_nop 0
	s_add_u32 vcc_lo, s12, s92
	s_addc_u32 vcc_hi, s13, s93
	s_mov_b64 s[92:93], s[12:13]
	s_add_u32 s48, s92, s48
	s_addc_u32 s49, s93, s49
	s_add_u32 s46, s92, s46
	s_addc_u32 s47, s93, s47
	s_add_u32 s52, s92, s52
	s_addc_u32 s53, s93, s53
	s_add_u32 s50, s92, s50
	s_addc_u32 s51, s93, s51
	s_mov_b32 s12, 0x3e800000
	s_nop 0
	s_waitcnt vmcnt(3)
	v_lshlrev_b32_e32 v14, 16, v236
	v_and_b32_e32 v15, 0xffff0000, v236
	s_nop 0
	s_waitcnt vmcnt(2)
	v_lshlrev_b32_e32 v88, 16, v238
	v_and_b32_e32 v89, 0xffff0000, v238
	v_lshlrev_b32_e32 v86, 16, v239
	v_and_b32_e32 v87, 0xffff0000, v239
	s_waitcnt lgkmcnt(0)
	v_pk_fma_f32 v[94:95], v[0:1], v[88:89], 0 op_sel_hi:[0,1,0]
	v_pk_fma_f32 v[96:97], v[0:1], v[86:87], 0 op_sel_hi:[0,1,0]
	s_nop 0
	s_waitcnt vmcnt(1)
	v_lshlrev_b32_e32 v98, 16, v240
	v_and_b32_e32 v99, 0xffff0000, v240
	v_lshlrev_b32_e32 v10, 16, v241
	v_and_b32_e32 v11, 0xffff0000, v241
	v_pk_mul_f32 v[100:101], v[0:1], v[10:11] op_sel:[1,0]
	v_pk_fma_f32 v[10:11], v[0:1], v[10:11], v[96:97] op_sel:[1,0,0]
	v_pk_fma_f32 v[94:95], v[0:1], v[98:99], v[94:95] op_sel:[1,0,0]
	v_lshlrev_b32_e32 v12, 16, v237
	v_and_b32_e32 v13, 0xffff0000, v237
	v_pk_mul_f32 v[104:105], v[0:1], v[98:99] op_sel:[1,0]
	v_pk_fma_f32 v[88:89], v[0:1], v[88:89], v[94:95] op_sel_hi:[0,1,1] neg_lo:[1,0,0] neg_hi:[1,0,0]
	v_pk_fma_f32 v[0:1], v[0:1], v[86:87], v[10:11] op_sel_hi:[0,1,1] neg_lo:[1,0,0] neg_hi:[1,0,0]
	v_pk_mul_f32 v[84:85], v[2:3], v[12:13] op_sel_hi:[0,1]
	v_pk_fma_f32 v[0:1], v[2:3], v[12:13], v[0:1] op_sel_hi:[0,1,1]
	v_pk_mul_f32 v[80:81], v[2:3], v[14:15] op_sel_hi:[0,1]
	v_pk_fma_f32 v[2:3], v[2:3], v[14:15], v[88:89] op_sel_hi:[0,1,1]
	v_pk_fma_f32 v[14:15], v[0:1], 0.5, v[84:85] op_sel_hi:[1,0,1] neg_lo:[0,0,1] neg_hi:[0,0,1]
	v_lshl_add_u64 v[84:85], s[30:31], 0, v[82:83]
	s_nop 0
	v_lshl_add_u32 v0, v55, 4, s17
	v_pk_fma_f32 v[80:81], v[2:3], 0.5, v[80:81] op_sel_hi:[1,0,1] neg_lo:[0,0,1] neg_hi:[0,0,1]
	ds_read_b128 v[0:3], v0
	v_pk_fma_f32 v[10:11], v[10:11], 0.5, v[100:101] op_sel_hi:[1,0,1] neg_lo:[0,0,1] neg_hi:[0,0,1]
	v_lshl_add_u64 v[82:83], s[28:29], 0, v[82:83]
	v_pk_fma_f32 v[12:13], v[94:95], 0.5, v[104:105] op_sel_hi:[1,0,1] neg_lo:[0,0,1] neg_hi:[0,0,1]
	s_nop 0
	s_waitcnt vmcnt(0)
	v_lshlrev_b32_e32 v88, 16, v242
	v_and_b32_e32 v89, 0xffff0000, v242
	v_lshlrev_b32_e32 v86, 16, v243
	v_and_b32_e32 v87, 0xffff0000, v243
	s_waitcnt lgkmcnt(0)
	v_pk_fma_f32 v[10:11], v[2:3], v[10:11], v[86:87]
	global_load_dwordx2 v[86:87], v[82:83], off
	v_pk_fma_f32 v[12:13], v[0:1], v[12:13], v[88:89]
	s_nop 0
	s_waitcnt vmcnt(0)
	v_lshlrev_b32_e32 v88, 16, v86
	v_and_b32_e32 v89, 0xffff0000, v86
	v_lshlrev_b32_e32 v86, 16, v87
	v_and_b32_e32 v87, 0xffff0000, v87
	v_pk_fma_f32 v[80:81], v[0:1], v[80:81], v[88:89]
	v_cvt_pk_bf16_f32 v0, v12, v13
	v_cvt_pk_bf16_f32 v1, v10, v11
	v_pk_fma_f32 v[14:15], v[2:3], v[14:15], v[86:87]
	v_cvt_pk_bf16_f32 v2, v80, v81
	s_nop 0
	v_cvt_pk_bf16_f32 v3, v14, v15
	global_store_dwordx2 v[84:85], v[0:1], off
	global_store_dwordx2 v[82:83], v[2:3], off
	v_mov_b32_e32 v0, v21
	s_nop 0
	v_lshlrev_b32_e32 v82, 2, v0
	v_add_u32_e32 v84, 0x100, v82
	v_ashrrev_i32_e32 v85, 31, v84
	v_lshlrev_b64 v[86:87], 1, v[84:85]
	v_lshl_add_u64 v[236:237], vcc, 0, v[86:87]
	global_load_dwordx2 v[236:237], v[236:237], off
	v_lshl_add_u64 v[238:239], s[48:49], 0, v[86:87]
	global_load_dwordx2 v[238:239], v[238:239], off
	v_lshl_add_u64 v[240:241], s[46:47], 0, v[86:87]
	global_load_dwordx2 v[240:241], v[240:241], off
	s_nop 0
	s_nop 0
	s_nop 0
	s_nop 0
	s_nop 0
	ds_read_b96 v[0:2], v53 offset:64
	s_nop 0
	v_ashrrev_i32_e32 v83, 31, v82
	s_nop 0
	s_waitcnt vmcnt(2)
	v_lshlrev_b32_e32 v94, 16, v236
	v_and_b32_e32 v95, 0xffff0000, v236
	s_nop 0
	s_waitcnt vmcnt(1)
	v_lshlrev_b32_e32 v104, 16, v238
	v_and_b32_e32 v105, 0xffff0000, v238
	v_lshlrev_b32_e32 v100, 16, v239
	v_and_b32_e32 v101, 0xffff0000, v239
	s_waitcnt lgkmcnt(0)
	v_pk_fma_f32 v[106:107], v[0:1], v[104:105], 0 op_sel_hi:[0,1,0]
	v_pk_fma_f32 v[108:109], v[0:1], v[100:101], 0 op_sel_hi:[0,1,0]
	s_nop 0
	s_waitcnt vmcnt(0)
	v_lshlrev_b32_e32 v110, 16, v240
	v_and_b32_e32 v111, 0xffff0000, v240
	v_lshlrev_b32_e32 v86, 16, v241
	v_and_b32_e32 v87, 0xffff0000, v241
	v_pk_fma_f32 v[108:109], v[0:1], v[86:87], v[108:109] op_sel:[1,0,0]
	v_pk_fma_f32 v[106:107], v[0:1], v[110:111], v[106:107] op_sel:[1,0,0]
	v_lshlrev_b32_e32 v88, 16, v237
	v_and_b32_e32 v89, 0xffff0000, v237
	v_pk_mul_f32 v[112:113], v[0:1], v[86:87] op_sel:[1,0]
	v_pk_mul_f32 v[114:115], v[0:1], v[110:111] op_sel:[1,0]
	v_pk_fma_f32 v[86:87], v[0:1], v[104:105], v[106:107] op_sel_hi:[0,1,1] neg_lo:[1,0,0] neg_hi:[1,0,0]
	v_pk_fma_f32 v[0:1], v[0:1], v[100:101], v[108:109] op_sel_hi:[0,1,1] neg_lo:[1,0,0] neg_hi:[1,0,0]
	v_lshlrev_b64 v[100:101], 1, v[82:83]
	v_pk_mul_f32 v[96:97], v[2:3], v[88:89] op_sel_hi:[0,1]
	v_pk_mul_f32 v[98:99], v[2:3], v[94:95] op_sel_hi:[0,1]
	v_pk_fma_f32 v[0:1], v[2:3], v[88:89], v[0:1] op_sel_hi:[0,1,1]
	v_pk_fma_f32 v[2:3], v[2:3], v[94:95], v[86:87] op_sel_hi:[0,1,1]
	v_lshl_add_u64 v[236:237], s[30:31], 0, v[100:101]
	global_load_dwordx2 v[236:237], v[236:237], off offset:512
	v_lshl_add_u64 v[238:239], s[28:29], 0, v[100:101]
	global_load_dwordx2 v[238:239], v[238:239], off offset:512
	v_lshl_add_u64 v[94:95], s[30:31], 0, v[100:101]
	s_nop 0
	v_pk_fma_f32 v[86:87], v[0:1], 0.5, v[96:97] op_sel_hi:[1,0,1] neg_lo:[0,0,1] neg_hi:[0,0,1]
	v_lshl_add_u32 v0, v84, 2, s17
	v_pk_fma_f32 v[88:89], v[2:3], 0.5, v[98:99] op_sel_hi:[1,0,1] neg_lo:[0,0,1] neg_hi:[0,0,1]
	ds_read_b128 v[0:3], v0
	v_pk_fma_f32 v[96:97], v[106:107], 0.5, v[114:115] op_sel_hi:[1,0,1] neg_lo:[0,0,1] neg_hi:[0,0,1]
	v_pk_fma_f32 v[98:99], v[108:109], 0.5, v[112:113] op_sel_hi:[1,0,1] neg_lo:[0,0,1] neg_hi:[0,0,1]
	s_nop 0
	s_waitcnt vmcnt(1)
	v_lshlrev_b32_e32 v84, 16, v236
	v_and_b32_e32 v85, 0xffff0000, v236
	v_lshlrev_b32_e32 v82, 16, v237
	v_and_b32_e32 v83, 0xffff0000, v237
	s_waitcnt lgkmcnt(0)
	v_pk_fma_f32 v[84:85], v[0:1], v[96:97], v[84:85]
	v_lshl_add_u64 v[96:97], s[28:29], 0, v[100:101]
	v_pk_fma_f32 v[82:83], v[2:3], v[98:99], v[82:83]
	s_nop 0
	s_nop 0
	s_waitcnt vmcnt(0)
	v_lshlrev_b32_e32 v100, 16, v238
	v_and_b32_e32 v101, 0xffff0000, v238
	v_lshlrev_b32_e32 v98, 16, v239
	v_and_b32_e32 v99, 0xffff0000, v239
	v_pk_fma_f32 v[88:89], v[0:1], v[88:89], v[100:101]
	v_cvt_pk_bf16_f32 v0, v84, v85
	v_cvt_pk_bf16_f32 v1, v82, v83
	v_pk_fma_f32 v[86:87], v[2:3], v[86:87], v[98:99]
	v_cvt_pk_bf16_f32 v2, v88, v89
	s_nop 0
	v_cvt_pk_bf16_f32 v3, v86, v87
	global_store_dwordx2 v[94:95], v[0:1], off offset:512
	global_store_dwordx2 v[96:97], v[2:3], off offset:512
	v_mov_b32_e32 v0, v21
	ds_read_b32 v98, v53 offset:72
	v_lshlrev_b32_e32 v94, 2, v0
	v_add_u32_e32 v96, 0x200, v94
	v_ashrrev_i32_e32 v97, 31, v96
	v_lshlrev_b64 v[100:101], 1, v[96:97]
	v_lshl_add_u64 v[236:237], vcc, 0, v[100:101]
	global_load_dwordx2 v[236:237], v[236:237], off
	v_lshl_add_u64 v[238:239], s[52:53], 0, v[100:101]
	global_load_dwordx2 v[238:239], v[238:239], off
	v_lshl_add_u64 v[240:241], s[50:51], 0, v[100:101]
	global_load_dwordx2 v[240:241], v[240:241], off
	v_lshl_add_u64 v[242:243], s[48:49], 0, v[100:101]
	global_load_dwordx2 v[242:243], v[242:243], off
	v_lshl_add_u64 v[244:245], s[46:47], 0, v[100:101]
	global_load_dwordx2 v[244:245], v[244:245], off
	s_nop 0
	s_nop 0
	s_nop 0
	s_nop 0
	s_nop 0
	s_nop 0
	v_ashrrev_i32_e32 v95, 31, v94
	s_nop 0
	s_waitcnt vmcnt(4)
	v_lshlrev_b32_e32 v104, 16, v236
	v_and_b32_e32 v105, 0xffff0000, v236
	v_lshlrev_b32_e32 v106, 16, v237
	v_and_b32_e32 v107, 0xffff0000, v237
	ds_read2_b64 v[0:3], v53 offset0:7 offset1:8
	s_nop 0
	s_waitcnt vmcnt(3)
	v_lshlrev_b32_e32 v114, 16, v238
	v_and_b32_e32 v115, 0xffff0000, v238
	v_lshlrev_b32_e32 v112, 16, v239
	v_and_b32_e32 v113, 0xffff0000, v239
	s_waitcnt lgkmcnt(0)
	v_pk_fma_f32 v[122:123], v[0:1], v[112:113], 0 op_sel_hi:[0,1,0]
	s_nop 0
	s_waitcnt vmcnt(2)
	v_lshlrev_b32_e32 v126, 16, v240
	v_and_b32_e32 v127, 0xffff0000, v240
	v_lshlrev_b32_e32 v124, 16, v241
	v_and_b32_e32 v125, 0xffff0000, v241
	v_pk_fma_f32 v[122:123], v[0:1], v[124:125], v[122:123] op_sel:[1,0,0]
	s_nop 0
	s_nop 0
	s_nop 0
	s_nop 0
	v_pk_fma_f32 v[116:117], v[0:1], v[114:115], 0 op_sel_hi:[0,1,0]
	v_pk_fma_f32 v[116:117], v[0:1], v[126:127], v[116:117] op_sel:[1,0,0]
	v_pk_mul_f32 v[108:109], v[98:99], v[106:107] op_sel_hi:[0,1]
	v_pk_mul_f32 v[110:111], v[98:99], v[104:105] op_sel_hi:[0,1]
	s_nop 0
	s_waitcnt vmcnt(1)
	v_lshlrev_b32_e32 v126, 16, v242
	v_and_b32_e32 v127, 0xffff0000, v242
	v_lshlrev_b32_e32 v124, 16, v243
	v_and_b32_e32 v125, 0xffff0000, v243
	v_pk_fma_f32 v[116:117], v[2:3], v[126:127], v[116:117] op_sel_hi:[0,1,1]
	v_pk_fma_f32 v[122:123], v[2:3], v[124:125], v[122:123] op_sel_hi:[0,1,1]
	s_nop 0
	s_waitcnt vmcnt(0)
	v_lshlrev_b32_e32 v124, 16, v244
	v_and_b32_e32 v125, 0xffff0000, v244
	v_lshlrev_b32_e32 v100, 16, v245
	v_and_b32_e32 v101, 0xffff0000, v245
	v_mov_b32_e32 v2, v3
	v_pk_mul_f32 v[126:127], v[2:3], v[100:101] op_sel_hi:[0,1]
	v_pk_mul_f32 v[128:129], v[2:3], v[124:125] op_sel_hi:[0,1]
	v_pk_fma_f32 v[122:123], v[2:3], v[100:101], v[122:123] op_sel_hi:[0,1,1]
	v_pk_fma_f32 v[2:3], v[2:3], v[124:125], v[116:117] op_sel_hi:[0,1,1]
	v_pk_fma_f32 v[100:101], v[0:1], v[114:115], v[2:3] op_sel_hi:[0,1,1] neg_lo:[1,0,0] neg_hi:[1,0,0]
	v_pk_fma_f32 v[0:1], v[0:1], v[112:113], v[122:123] op_sel_hi:[0,1,1] neg_lo:[1,0,0] neg_hi:[1,0,0]
	v_pk_fma_f32 v[0:1], v[98:99], v[106:107], v[0:1] op_sel_hi:[0,1,1]
	v_pk_fma_f32 v[98:99], v[98:99], v[104:105], v[100:101] op_sel_hi:[0,1,1]
	v_pk_fma_f32 v[100:101], v[98:99], s[12:13], v[110:111] op_sel_hi:[1,0,1] neg_lo:[0,0,1] neg_hi:[0,0,1]
	v_lshlrev_b64 v[110:111], 1, v[94:95]
	v_lshl_add_u64 v[236:237], s[30:31], 0, v[110:111]
	global_load_dwordx2 v[236:237], v[236:237], off offset:1024
	v_lshl_add_u64 v[238:239], s[28:29], 0, v[110:111]
	global_load_dwordx2 v[238:239], v[238:239], off offset:1024
	v_lshl_add_u64 v[104:105], s[30:31], 0, v[110:111]
	s_nop 0
	v_pk_fma_f32 v[98:99], v[0:1], s[12:13], v[108:109] op_sel_hi:[1,0,1] neg_lo:[0,0,1] neg_hi:[0,0,1]
	v_lshl_add_u32 v0, v96, 2, s17
	v_pk_fma_f32 v[106:107], v[102:103], v[2:3], v[128:129] op_sel_hi:[0,1,1] neg_lo:[0,0,1] neg_hi:[0,0,1]
	ds_read_b128 v[0:3], v0
	v_pk_fma_f32 v[108:109], v[102:103], v[122:123], v[126:127] op_sel_hi:[0,1,1] neg_lo:[0,0,1] neg_hi:[0,0,1]
	s_nop 0
	s_waitcnt vmcnt(1)
	v_lshlrev_b32_e32 v96, 16, v236
	v_and_b32_e32 v97, 0xffff0000, v236
	v_lshlrev_b32_e32 v94, 16, v237
	v_and_b32_e32 v95, 0xffff0000, v237
	s_waitcnt lgkmcnt(0)
	v_pk_fma_f32 v[96:97], v[0:1], v[106:107], v[96:97]
	v_lshl_add_u64 v[106:107], s[28:29], 0, v[110:111]
	v_pk_fma_f32 v[94:95], v[2:3], v[108:109], v[94:95]
	s_nop 0
	s_nop 0
	s_waitcnt vmcnt(0)
	v_lshlrev_b32_e32 v110, 16, v238
	v_and_b32_e32 v111, 0xffff0000, v238
	v_lshlrev_b32_e32 v108, 16, v239
	v_and_b32_e32 v109, 0xffff0000, v239
	v_pk_fma_f32 v[100:101], v[0:1], v[100:101], v[110:111]
	v_cvt_pk_bf16_f32 v0, v96, v97
	v_cvt_pk_bf16_f32 v1, v94, v95
	v_pk_fma_f32 v[98:99], v[2:3], v[98:99], v[108:109]
	v_cvt_pk_bf16_f32 v2, v100, v101
	s_nop 0
	v_cvt_pk_bf16_f32 v3, v98, v99
	global_store_dwordx2 v[104:105], v[0:1], off offset:1024
	global_store_dwordx2 v[106:107], v[2:3], off offset:1024
	v_mov_b32_e32 v0, v21
	ds_read_b32 v106, v53 offset:72
	v_lshlrev_b32_e32 v104, 2, v0
	v_add_u32_e32 v110, 0x300, v104
	v_ashrrev_i32_e32 v111, 31, v110
	v_lshlrev_b64 v[108:109], 1, v[110:111]
	v_lshl_add_u64 v[236:237], vcc, 0, v[108:109]
	global_load_dwordx2 v[236:237], v[236:237], off
	v_lshl_add_u64 v[238:239], s[52:53], 0, v[108:109]
	global_load_dwordx2 v[238:239], v[238:239], off
	v_lshl_add_u64 v[240:241], s[50:51], 0, v[108:109]
	global_load_dwordx2 v[240:241], v[240:241], off
	v_lshl_add_u64 v[242:243], s[48:49], 0, v[108:109]
	global_load_dwordx2 v[242:243], v[242:243], off
	v_lshl_add_u64 v[244:245], s[46:47], 0, v[108:109]
	global_load_dwordx2 v[244:245], v[244:245], off
	s_nop 0
	s_nop 0
	s_nop 0
	s_nop 0
	s_nop 0
	s_nop 0
	v_ashrrev_i32_e32 v105, 31, v104
	s_nop 0
	s_waitcnt vmcnt(4)
	v_lshlrev_b32_e32 v112, 16, v236
	v_and_b32_e32 v113, 0xffff0000, v236
	v_lshlrev_b32_e32 v114, 16, v237
	v_and_b32_e32 v115, 0xffff0000, v237
	ds_read2_b64 v[0:3], v53 offset0:7 offset1:8
	s_nop 0
	s_waitcnt vmcnt(3)
	v_lshlrev_b32_e32 v126, 16, v238
	v_and_b32_e32 v127, 0xffff0000, v238
	v_lshlrev_b32_e32 v124, 16, v239
	v_and_b32_e32 v125, 0xffff0000, v239
	s_waitcnt lgkmcnt(0)
	v_pk_fma_f32 v[130:131], v[0:1], v[124:125], 0 op_sel_hi:[0,1,0]
	s_nop 0
	s_waitcnt vmcnt(2)
	v_lshlrev_b32_e32 v134, 16, v240
	v_and_b32_e32 v135, 0xffff0000, v240
	v_lshlrev_b32_e32 v132, 16, v241
	v_and_b32_e32 v133, 0xffff0000, v241
	v_pk_fma_f32 v[130:131], v[0:1], v[132:133], v[130:131] op_sel:[1,0,0]
	s_nop 0
	s_nop 0
	s_nop 0
	s_nop 0
	v_pk_fma_f32 v[128:129], v[0:1], v[126:127], 0 op_sel_hi:[0,1,0]
	v_pk_fma_f32 v[128:129], v[0:1], v[134:135], v[128:129] op_sel:[1,0,0]
	v_pk_mul_f32 v[116:117], v[106:107], v[114:115] op_sel_hi:[0,1]
	v_pk_mul_f32 v[122:123], v[106:107], v[112:113] op_sel_hi:[0,1]
	s_nop 0
	s_waitcnt vmcnt(1)
	v_lshlrev_b32_e32 v134, 16, v242
	v_and_b32_e32 v135, 0xffff0000, v242
	v_lshlrev_b32_e32 v132, 16, v243
	v_and_b32_e32 v133, 0xffff0000, v243
	v_pk_fma_f32 v[128:129], v[2:3], v[134:135], v[128:129] op_sel_hi:[0,1,1]
	v_pk_fma_f32 v[130:131], v[2:3], v[132:133], v[130:131] op_sel_hi:[0,1,1]
	s_nop 0
	s_waitcnt vmcnt(0)
	v_lshlrev_b32_e32 v132, 16, v244
	v_and_b32_e32 v133, 0xffff0000, v244
	v_lshlrev_b32_e32 v108, 16, v245
	v_and_b32_e32 v109, 0xffff0000, v245
	v_mov_b32_e32 v2, v3
	v_pk_mul_f32 v[134:135], v[2:3], v[108:109] op_sel_hi:[0,1]
	v_pk_mul_f32 v[136:137], v[2:3], v[132:133] op_sel_hi:[0,1]
	v_pk_fma_f32 v[130:131], v[2:3], v[108:109], v[130:131] op_sel_hi:[0,1,1]
	v_pk_fma_f32 v[2:3], v[2:3], v[132:133], v[128:129] op_sel_hi:[0,1,1]
	v_pk_fma_f32 v[108:109], v[0:1], v[126:127], v[2:3] op_sel_hi:[0,1,1] neg_lo:[1,0,0] neg_hi:[1,0,0]
	v_pk_fma_f32 v[0:1], v[0:1], v[124:125], v[130:131] op_sel_hi:[0,1,1] neg_lo:[1,0,0] neg_hi:[1,0,0]
	v_pk_fma_f32 v[0:1], v[106:107], v[114:115], v[0:1] op_sel_hi:[0,1,1]
	v_pk_fma_f32 v[106:107], v[106:107], v[112:113], v[108:109] op_sel_hi:[0,1,1]
	v_lshlrev_b64 v[114:115], 1, v[104:105]
	v_pk_fma_f32 v[108:109], v[106:107], s[12:13], v[122:123] op_sel_hi:[1,0,1] neg_lo:[0,0,1] neg_hi:[0,0,1]
	v_pk_fma_f32 v[106:107], v[0:1], s[12:13], v[116:117] op_sel_hi:[1,0,1] neg_lo:[0,0,1] neg_hi:[0,0,1]
	v_lshl_add_u32 v0, v110, 2, s17
	v_lshl_add_u64 v[236:237], s[30:31], 0, v[114:115]
	global_load_dwordx2 v[236:237], v[236:237], off offset:1536
	v_lshl_add_u64 v[238:239], s[28:29], 0, v[114:115]
	global_load_dwordx2 v[238:239], v[238:239], off offset:1536
	v_lshl_add_u64 v[110:111], s[30:31], 0, v[114:115]
	s_nop 0
	v_pk_fma_f32 v[112:113], v[102:103], v[2:3], v[136:137] op_sel_hi:[0,1,1] neg_lo:[0,0,1] neg_hi:[0,0,1]
	ds_read_b128 v[0:3], v0
	v_pk_fma_f32 v[102:103], v[102:103], v[130:131], v[134:135] op_sel_hi:[0,1,1] neg_lo:[0,0,1] neg_hi:[0,0,1]
	s_nop 0
	s_waitcnt vmcnt(1)
	v_lshlrev_b32_e32 v116, 16, v236
	v_and_b32_e32 v117, 0xffff0000, v236
	v_lshlrev_b32_e32 v104, 16, v237
	v_and_b32_e32 v105, 0xffff0000, v237
	s_waitcnt lgkmcnt(0)
	v_pk_fma_f32 v[102:103], v[2:3], v[102:103], v[104:105]
	v_pk_fma_f32 v[104:105], v[0:1], v[112:113], v[116:117]
	v_lshl_add_u64 v[112:113], s[28:29], 0, v[114:115]
	s_nop 0
	s_nop 0
	s_waitcnt vmcnt(0)
	v_lshlrev_b32_e32 v116, 16, v238
	v_and_b32_e32 v117, 0xffff0000, v238
	v_lshlrev_b32_e32 v114, 16, v239
	v_and_b32_e32 v115, 0xffff0000, v239
	v_pk_fma_f32 v[108:109], v[0:1], v[108:109], v[116:117]
	v_cvt_pk_bf16_f32 v0, v104, v105
	v_cvt_pk_bf16_f32 v1, v102, v103
	v_pk_fma_f32 v[106:107], v[2:3], v[106:107], v[114:115]
	v_cvt_pk_bf16_f32 v2, v108, v109
	s_nop 0
	v_cvt_pk_bf16_f32 v3, v106, v107
	global_store_dwordx2 v[110:111], v[0:1], off offset:1536
	global_store_dwordx2 v[112:113], v[2:3], off offset:1536
	v_mov_b32_e32 v0, v21
	s_add_u32 s86, s92, s86
	v_lshlrev_b32_e32 v110, 2, v0
	v_add_u32_e32 v112, 0x400, v110
	v_ashrrev_i32_e32 v113, 31, v112
	v_lshlrev_b64 v[128:129], 1, v[112:113]
	v_lshl_add_u64 v[0:1], vcc, 0, v[128:129]
	global_load_dwordx2 v[0:1], v[0:1], off
	s_addc_u32 s87, s93, s87
	s_add_u32 s0, s92, s0
	v_lshl_add_u64 v[130:131], s[86:87], 0, v[128:129]
	s_addc_u32 s1, s93, s1
	global_load_dwordx2 v[132:133], v[130:131], off
	v_lshl_add_u64 v[138:139], s[0:1], 0, v[128:129]
	global_load_dwordx2 v[138:139], v[138:139], off
	ds_read_b32 v114, v53 offset:72
	s_add_u32 s2, s92, s2
	s_addc_u32 s3, s93, s3
	s_add_u32 s96, s92, s96
	s_addc_u32 s97, s93, s97
	v_ashrrev_i32_e32 v111, 31, v110
	s_add_u32 s42, s92, s42
	s_addc_u32 s43, s93, s43
	s_add_u32 s88, s92, s88
	s_addc_u32 s89, s93, s89
	s_add_u32 s36, s92, s36
	s_addc_u32 s37, s93, s37
	s_add_u32 s78, s92, s78
	s_addc_u32 s79, s93, s79
	s_add_u32 s76, s92, s76
	s_addc_u32 s77, s93, s77
	s_add_u32 s10, s92, s10
	s_addc_u32 s11, s93, s11
	s_add_u32 s8, s92, s8
	s_addc_u32 s9, s93, s9
	s_add_u32 s44, s92, s44
	s_addc_u32 s45, s93, s45
	s_nop 0
	s_waitcnt vmcnt(2)
	v_lshlrev_b32_e32 v116, 16, v0
	v_and_b32_e32 v117, 0xffff0000, v0
	v_lshlrev_b32_e32 v124, 16, v1
	v_and_b32_e32 v125, 0xffff0000, v1
	ds_read2_b64 v[0:3], v53 offset0:5 offset1:6
	s_nop 0
	s_waitcnt vmcnt(1)
	v_lshlrev_b32_e32 v130, 16, v132
	v_and_b32_e32 v131, 0xffff0000, v132
	v_lshlrev_b32_e32 v132, 16, v133
	v_and_b32_e32 v133, 0xffff0000, v133
	s_waitcnt lgkmcnt(0)
	v_pk_fma_f32 v[136:137], v[0:1], v[132:133], 0 op_sel_hi:[0,1,0]
	s_nop 0
	s_waitcnt vmcnt(0)
	v_lshlrev_b32_e32 v140, 16, v138
	v_and_b32_e32 v141, 0xffff0000, v138
	v_lshlrev_b32_e32 v138, 16, v139
	v_and_b32_e32 v139, 0xffff0000, v139
	v_pk_fma_f32 v[136:137], v[0:1], v[138:139], v[136:137] op_sel:[1,0,0]
	v_lshl_add_u64 v[236:237], s[2:3], 0, v[128:129]
	global_load_dwordx2 v[236:237], v[236:237], off
	v_lshl_add_u64 v[238:239], s[96:97], 0, v[128:129]
	global_load_dwordx2 v[238:239], v[238:239], off
	v_lshl_add_u64 v[240:241], s[52:53], 0, v[128:129]
	global_load_dwordx2 v[240:241], v[240:241], off
	v_lshl_add_u64 v[242:243], s[50:51], 0, v[128:129]
	global_load_dwordx2 v[242:243], v[242:243], off
	v_lshl_add_u64 v[244:245], s[48:49], 0, v[128:129]
	global_load_dwordx2 v[244:245], v[244:245], off
	v_lshl_add_u64 v[246:247], s[46:47], 0, v[128:129]
	global_load_dwordx2 v[246:247], v[246:247], off
	s_nop 0
	s_nop 0
	v_pk_fma_f32 v[134:135], v[0:1], v[130:131], 0 op_sel_hi:[0,1,0]
	v_pk_fma_f32 v[134:135], v[0:1], v[140:141], v[134:135] op_sel:[1,0,0]
	v_pk_mul_f32 v[122:123], v[114:115], v[124:125] op_sel_hi:[0,1]
	v_pk_mul_f32 v[126:127], v[114:115], v[116:117] op_sel_hi:[0,1]
	s_nop 0
	s_waitcnt vmcnt(5)
	v_lshlrev_b32_e32 v140, 16, v236
	v_and_b32_e32 v141, 0xffff0000, v236
	v_lshlrev_b32_e32 v138, 16, v237
	v_and_b32_e32 v139, 0xffff0000, v237
	v_pk_fma_f32 v[136:137], v[2:3], v[138:139], v[136:137] op_sel_hi:[0,1,1]
	s_nop 0
	s_nop 0
	v_pk_fma_f32 v[134:135], v[2:3], v[140:141], v[134:135] op_sel_hi:[0,1,1]
	v_mov_b32_e32 v2, v3
	s_nop 0
	s_waitcnt vmcnt(4)
	v_lshlrev_b32_e32 v140, 16, v238
	v_and_b32_e32 v141, 0xffff0000, v238
	v_lshlrev_b32_e32 v138, 16, v239
	v_and_b32_e32 v139, 0xffff0000, v239
	v_pk_fma_f32 v[138:139], v[2:3], v[138:139], v[136:137] op_sel_hi:[0,1,1]
	v_pk_fma_f32 v[2:3], v[2:3], v[140:141], v[134:135] op_sel_hi:[0,1,1]
	s_nop 0
	s_nop 0
	ds_read2_b64 v[134:137], v53 offset0:7 offset1:8
	s_nop 0
	s_waitcnt vmcnt(3)
	v_lshlrev_b32_e32 v142, 16, v240
	v_and_b32_e32 v143, 0xffff0000, v240
	v_lshlrev_b32_e32 v140, 16, v241
	v_and_b32_e32 v141, 0xffff0000, v241
	s_waitcnt lgkmcnt(0)
	v_pk_fma_f32 v[138:139], v[134:135], v[140:141], v[138:139] op_sel_hi:[0,1,1]
	s_nop 0
	s_nop 0
	v_pk_fma_f32 v[2:3], v[134:135], v[142:143], v[2:3] op_sel_hi:[0,1,1]
	s_nop 0
	s_waitcnt vmcnt(2)
	v_lshlrev_b32_e32 v142, 16, v242
	v_and_b32_e32 v143, 0xffff0000, v242
	v_lshlrev_b32_e32 v140, 16, v243
	v_and_b32_e32 v141, 0xffff0000, v243
	v_pk_fma_f32 v[138:139], v[134:135], v[140:141], v[138:139] op_sel:[1,0,0]
	v_pk_fma_f32 v[2:3], v[134:135], v[142:143], v[2:3] op_sel:[1,0,0]
	s_nop 0
	s_nop 0
	s_nop 0
	s_nop 0
	s_nop 0
	s_waitcnt vmcnt(1)
	v_lshlrev_b32_e32 v140, 16, v244
	v_and_b32_e32 v141, 0xffff0000, v244
	v_lshlrev_b32_e32 v134, 16, v245
	v_and_b32_e32 v135, 0xffff0000, v245
	v_pk_fma_f32 v[2:3], v[136:137], v[140:141], v[2:3] op_sel_hi:[0,1,1]
	v_pk_fma_f32 v[134:135], v[136:137], v[134:135], v[138:139] op_sel_hi:[0,1,1]
	s_nop 0
	s_waitcnt vmcnt(0)
	v_lshlrev_b32_e32 v138, 16, v246
	v_and_b32_e32 v139, 0xffff0000, v246
	v_lshlrev_b32_e32 v128, 16, v247
	v_and_b32_e32 v129, 0xffff0000, v247
	v_mov_b32_e32 v136, v137
	v_pk_mul_f32 v[140:141], v[136:137], v[128:129] op_sel_hi:[0,1]
	v_pk_fma_f32 v[128:129], v[136:137], v[128:129], v[134:135] op_sel_hi:[0,1,1]
	v_pk_fma_f32 v[2:3], v[136:137], v[138:139], v[2:3] op_sel_hi:[0,1,1]
	v_pk_fma_f32 v[130:131], v[0:1], v[130:131], v[2:3] op_sel_hi:[0,1,1] neg_lo:[1,0,0] neg_hi:[1,0,0]
	v_pk_fma_f32 v[0:1], v[0:1], v[132:133], v[128:129] op_sel_hi:[0,1,1] neg_lo:[1,0,0] neg_hi:[1,0,0]
	v_pk_fma_f32 v[0:1], v[114:115], v[124:125], v[0:1] op_sel_hi:[0,1,1]
	v_pk_fma_f32 v[114:115], v[114:115], v[116:117], v[130:131] op_sel_hi:[0,1,1]
	v_pk_fma_f32 v[116:117], v[120:121], v[114:115], v[126:127] op_sel_hi:[0,1,1] neg_lo:[0,0,1] neg_hi:[0,0,1]
	v_pk_fma_f32 v[126:127], v[118:119], v[128:129], v[140:141] op_sel_hi:[0,1,1] neg_lo:[0,0,1] neg_hi:[0,0,1]
	v_lshlrev_b64 v[128:129], 1, v[110:111]
	v_pk_fma_f32 v[114:115], v[120:121], v[0:1], v[122:123] op_sel_hi:[0,1,1] neg_lo:[0,0,1] neg_hi:[0,0,1]
	v_lshl_add_u64 v[236:237], s[30:31], 0, v[128:129]
	global_load_dwordx2 v[236:237], v[236:237], off offset:2048
	v_lshl_add_u64 v[238:239], s[28:29], 0, v[128:129]
	global_load_dwordx2 v[238:239], v[238:239], off offset:2048
	v_lshl_add_u64 v[122:123], s[30:31], 0, v[128:129]
	s_nop 0
	v_pk_mul_f32 v[142:143], v[136:137], v[138:139] op_sel_hi:[0,1]
	v_lshl_add_u32 v0, v112, 2, s17
	v_pk_fma_f32 v[124:125], v[118:119], v[2:3], v[142:143] op_sel_hi:[0,1,1] neg_lo:[0,0,1] neg_hi:[0,0,1]
	ds_read_b128 v[0:3], v0
	s_nop 0
	s_waitcnt vmcnt(1)
	v_lshlrev_b32_e32 v112, 16, v236
	v_and_b32_e32 v113, 0xffff0000, v236
	v_lshlrev_b32_e32 v110, 16, v237
	v_and_b32_e32 v111, 0xffff0000, v237
	s_waitcnt lgkmcnt(0)
	v_pk_fma_f32 v[112:113], v[0:1], v[124:125], v[112:113]
	v_lshl_add_u64 v[124:125], s[28:29], 0, v[128:129]
	v_pk_fma_f32 v[110:111], v[2:3], v[126:127], v[110:111]
	s_nop 0
	s_nop 0
	s_waitcnt vmcnt(0)
	v_lshlrev_b32_e32 v128, 16, v238
	v_and_b32_e32 v129, 0xffff0000, v238
	v_lshlrev_b32_e32 v126, 16, v239
	v_and_b32_e32 v127, 0xffff0000, v239
	v_pk_fma_f32 v[116:117], v[0:1], v[116:117], v[128:129]
	v_cvt_pk_bf16_f32 v0, v112, v113
	v_cvt_pk_bf16_f32 v1, v110, v111
	v_pk_fma_f32 v[114:115], v[2:3], v[114:115], v[126:127]
	v_cvt_pk_bf16_f32 v2, v116, v117
	s_nop 0
	v_cvt_pk_bf16_f32 v3, v114, v115
	global_store_dwordx2 v[122:123], v[0:1], off offset:2048
	global_store_dwordx2 v[124:125], v[2:3], off offset:2048
	v_mov_b32_e32 v0, v21
	ds_read_b32 v122, v53 offset:72
	v_lshlrev_b32_e32 v126, 2, v0
	v_add_u32_e32 v128, 0x500, v126
	v_ashrrev_i32_e32 v129, 31, v128
	v_lshlrev_b64 v[136:137], 1, v[128:129]
	v_lshl_add_u64 v[236:237], vcc, 0, v[136:137]
	global_load_dwordx2 v[236:237], v[236:237], off
	v_lshl_add_u64 v[238:239], s[86:87], 0, v[136:137]
	global_load_dwordx2 v[238:239], v[238:239], off
	v_lshl_add_u64 v[240:241], s[0:1], 0, v[136:137]
	global_load_dwordx2 v[240:241], v[240:241], off
	v_lshl_add_u64 v[242:243], s[2:3], 0, v[136:137]
	global_load_dwordx2 v[242:243], v[242:243], off
	v_lshl_add_u64 v[244:245], s[96:97], 0, v[136:137]
	global_load_dwordx2 v[244:245], v[244:245], off
	v_lshl_add_u64 v[246:247], s[52:53], 0, v[136:137]
	global_load_dwordx2 v[246:247], v[246:247], off
	s_nop 0
	s_nop 0
	v_lshl_add_u64 v[138:139], s[86:87], 0, v[136:137]
	s_nop 0
	s_nop 0
	s_nop 0
	v_ashrrev_i32_e32 v127, 31, v126
	s_nop 0
	s_waitcnt vmcnt(5)
	v_lshlrev_b32_e32 v124, 16, v236
	v_and_b32_e32 v125, 0xffff0000, v236
	v_lshlrev_b32_e32 v132, 16, v237
	v_and_b32_e32 v133, 0xffff0000, v237
	ds_read2_b64 v[0:3], v53 offset0:5 offset1:6
	s_nop 0
	s_waitcnt vmcnt(4)
	v_lshlrev_b32_e32 v138, 16, v238
	v_and_b32_e32 v139, 0xffff0000, v238
	v_lshlrev_b32_e32 v140, 16, v239
	v_and_b32_e32 v141, 0xffff0000, v239
	s_waitcnt lgkmcnt(0)
	v_pk_fma_f32 v[144:145], v[0:1], v[140:141], 0 op_sel_hi:[0,1,0]
	s_nop 0
	s_waitcnt vmcnt(3)
	v_lshlrev_b32_e32 v148, 16, v240
	v_and_b32_e32 v149, 0xffff0000, v240
	v_lshlrev_b32_e32 v146, 16, v241
	v_and_b32_e32 v147, 0xffff0000, v241
	v_pk_fma_f32 v[144:145], v[0:1], v[146:147], v[144:145] op_sel:[1,0,0]
	s_nop 0
	s_nop 0
	v_pk_fma_f32 v[142:143], v[0:1], v[138:139], 0 op_sel_hi:[0,1,0]
	v_pk_fma_f32 v[142:143], v[0:1], v[148:149], v[142:143] op_sel:[1,0,0]
	v_pk_mul_f32 v[130:131], v[122:123], v[132:133] op_sel_hi:[0,1]
	v_pk_mul_f32 v[134:135], v[122:123], v[124:125] op_sel_hi:[0,1]
	s_nop 0
	s_waitcnt vmcnt(2)
	v_lshlrev_b32_e32 v148, 16, v242
	v_and_b32_e32 v149, 0xffff0000, v242
	v_lshlrev_b32_e32 v146, 16, v243
	v_and_b32_e32 v147, 0xffff0000, v243
	v_pk_fma_f32 v[144:145], v[2:3], v[146:147], v[144:145] op_sel_hi:[0,1,1]
	s_nop 0
	s_nop 0
	v_pk_fma_f32 v[142:143], v[2:3], v[148:149], v[142:143] op_sel_hi:[0,1,1]
	v_mov_b32_e32 v2, v3
	s_nop 0
	s_waitcnt vmcnt(1)
	v_lshlrev_b32_e32 v148, 16, v244
	v_and_b32_e32 v149, 0xffff0000, v244
	v_lshlrev_b32_e32 v146, 16, v245
	v_and_b32_e32 v147, 0xffff0000, v245
	v_pk_fma_f32 v[146:147], v[2:3], v[146:147], v[144:145] op_sel_hi:[0,1,1]
	v_pk_fma_f32 v[2:3], v[2:3], v[148:149], v[142:143] op_sel_hi:[0,1,1]
	s_nop 0
	s_nop 0
	ds_read2_b64 v[142:145], v53 offset0:7 offset1:8
	s_nop 0
	s_waitcnt vmcnt(0)
	v_lshlrev_b32_e32 v150, 16, v246
	v_and_b32_e32 v151, 0xffff0000, v246
	v_lshlrev_b32_e32 v148, 16, v247
	v_and_b32_e32 v149, 0xffff0000, v247
	s_waitcnt lgkmcnt(0)
	v_pk_fma_f32 v[146:147], v[142:143], v[148:149], v[146:147] op_sel_hi:[0,1,1]
	v_lshl_add_u64 v[236:237], s[50:51], 0, v[136:137]
	global_load_dwordx2 v[236:237], v[236:237], off
	v_lshl_add_u64 v[238:239], s[48:49], 0, v[136:137]
	global_load_dwordx2 v[238:239], v[238:239], off
	v_lshl_add_u64 v[240:241], s[46:47], 0, v[136:137]
	global_load_dwordx2 v[240:241], v[240:241], off
	s_nop 0
	s_nop 0
	v_pk_fma_f32 v[2:3], v[142:143], v[150:151], v[2:3] op_sel_hi:[0,1,1]
	s_nop 0
	s_waitcnt vmcnt(2)
	v_lshlrev_b32_e32 v150, 16, v236
	v_and_b32_e32 v151, 0xffff0000, v236
	v_lshlrev_b32_e32 v148, 16, v237
	v_and_b32_e32 v149, 0xffff0000, v237
	v_pk_fma_f32 v[146:147], v[142:143], v[148:149], v[146:147] op_sel:[1,0,0]
	v_pk_fma_f32 v[2:3], v[142:143], v[150:151], v[2:3] op_sel:[1,0,0]
	s_nop 0
	s_nop 0
	s_nop 0
	s_nop 0
	s_nop 0
	s_waitcnt vmcnt(1)
	v_lshlrev_b32_e32 v148, 16, v238
	v_and_b32_e32 v149, 0xffff0000, v238
	v_lshlrev_b32_e32 v142, 16, v239
	v_and_b32_e32 v143, 0xffff0000, v239
	v_pk_fma_f32 v[2:3], v[144:145], v[148:149], v[2:3] op_sel_hi:[0,1,1]
	v_pk_fma_f32 v[142:143], v[144:145], v[142:143], v[146:147] op_sel_hi:[0,1,1]
	s_nop 0
	s_waitcnt vmcnt(0)
	v_lshlrev_b32_e32 v146, 16, v240
	v_and_b32_e32 v147, 0xffff0000, v240
	v_lshlrev_b32_e32 v136, 16, v241
	v_and_b32_e32 v137, 0xffff0000, v241
	v_mov_b32_e32 v144, v145
	v_pk_mul_f32 v[148:149], v[144:145], v[136:137] op_sel_hi:[0,1]
	v_pk_fma_f32 v[136:137], v[144:145], v[136:137], v[142:143] op_sel_hi:[0,1,1]
	v_pk_fma_f32 v[2:3], v[144:145], v[146:147], v[2:3] op_sel_hi:[0,1,1]
	v_pk_fma_f32 v[138:139], v[0:1], v[138:139], v[2:3] op_sel_hi:[0,1,1] neg_lo:[1,0,0] neg_hi:[1,0,0]
	v_pk_fma_f32 v[0:1], v[0:1], v[140:141], v[136:137] op_sel_hi:[0,1,1] neg_lo:[1,0,0] neg_hi:[1,0,0]
	v_pk_fma_f32 v[0:1], v[122:123], v[132:133], v[0:1] op_sel_hi:[0,1,1]
	v_pk_fma_f32 v[122:123], v[122:123], v[124:125], v[138:139] op_sel_hi:[0,1,1]
	v_pk_fma_f32 v[124:125], v[120:121], v[122:123], v[134:135] op_sel_hi:[0,1,1] neg_lo:[0,0,1] neg_hi:[0,0,1]
	v_pk_fma_f32 v[122:123], v[120:121], v[0:1], v[130:131] op_sel_hi:[0,1,1] neg_lo:[0,0,1] neg_hi:[0,0,1]
	v_lshl_add_u32 v0, v128, 2, s17
	v_lshlrev_b64 v[128:129], 1, v[126:127]
	v_lshl_add_u64 v[126:127], s[30:31], 0, v[128:129]
	global_load_dwordx2 v[130:131], v[126:127], off offset:2560
	v_pk_mul_f32 v[150:151], v[144:145], v[146:147] op_sel_hi:[0,1]
	v_pk_fma_f32 v[120:121], v[118:119], v[2:3], v[150:151] op_sel_hi:[0,1,1] neg_lo:[0,0,1] neg_hi:[0,0,1]
	ds_read_b128 v[0:3], v0
	v_pk_fma_f32 v[118:119], v[118:119], v[136:137], v[148:149] op_sel_hi:[0,1,1] neg_lo:[0,0,1] neg_hi:[0,0,1]
	v_lshl_add_u64 v[128:129], s[28:29], 0, v[128:129]
	s_nop 0
	s_waitcnt vmcnt(0)
	v_lshlrev_b32_e32 v132, 16, v130
	v_and_b32_e32 v133, 0xffff0000, v130
	v_lshlrev_b32_e32 v130, 16, v131
	v_and_b32_e32 v131, 0xffff0000, v131
	s_waitcnt lgkmcnt(0)
	v_pk_fma_f32 v[118:119], v[2:3], v[118:119], v[130:131]
	global_load_dwordx2 v[130:131], v[128:129], off offset:2560
	v_pk_fma_f32 v[120:121], v[0:1], v[120:121], v[132:133]
	s_nop 0
	s_waitcnt vmcnt(0)
	v_lshlrev_b32_e32 v132, 16, v130
	v_and_b32_e32 v133, 0xffff0000, v130
	v_lshlrev_b32_e32 v130, 16, v131
	v_and_b32_e32 v131, 0xffff0000, v131
	v_pk_fma_f32 v[124:125], v[0:1], v[124:125], v[132:133]
	v_cvt_pk_bf16_f32 v0, v120, v121
	v_cvt_pk_bf16_f32 v1, v118, v119
	v_pk_fma_f32 v[122:123], v[2:3], v[122:123], v[130:131]
	v_cvt_pk_bf16_f32 v2, v124, v125
	s_nop 0
	v_cvt_pk_bf16_f32 v3, v122, v123
	global_store_dwordx2 v[126:127], v[0:1], off offset:2560
	global_store_dwordx2 v[128:129], v[2:3], off offset:2560
	v_mov_b32_e32 v0, v21
	ds_read_b32 v130, v53 offset:72
	v_lshlrev_b32_e32 v126, 2, v0
	v_add_u32_e32 v128, 0x600, v126
	v_ashrrev_i32_e32 v129, 31, v128
	v_lshlrev_b64 v[140:141], 1, v[128:129]
	v_lshl_add_u64 v[236:237], vcc, 0, v[140:141]
	global_load_dwordx2 v[236:237], v[236:237], off
	v_lshl_add_u64 v[238:239], s[42:43], 0, v[140:141]
	global_load_dwordx2 v[238:239], v[238:239], off
	v_lshl_add_u64 v[240:241], s[88:89], 0, v[140:141]
	global_load_dwordx2 v[240:241], v[240:241], off
	v_lshl_add_u64 v[242:243], s[36:37], 0, v[140:141]
	global_load_dwordx2 v[242:243], v[242:243], off
	v_lshl_add_u64 v[244:245], s[78:79], 0, v[140:141]
	global_load_dwordx2 v[244:245], v[244:245], off
	v_lshl_add_u64 v[246:247], s[76:77], 0, v[140:141]
	global_load_dwordx2 v[246:247], v[246:247], off
	s_nop 0
	s_nop 0
	v_lshl_add_u64 v[142:143], s[42:43], 0, v[140:141]
	s_nop 0
	s_nop 0
	s_nop 0
	v_ashrrev_i32_e32 v127, 31, v126
	s_nop 0
	s_waitcnt vmcnt(5)
	v_lshlrev_b32_e32 v132, 16, v236
	v_and_b32_e32 v133, 0xffff0000, v236
	v_lshlrev_b32_e32 v136, 16, v237
	v_and_b32_e32 v137, 0xffff0000, v237
	ds_read2_b64 v[0:3], v53 offset0:1 offset1:2
	s_nop 0
	s_waitcnt vmcnt(4)
	v_lshlrev_b32_e32 v142, 16, v238
	v_and_b32_e32 v143, 0xffff0000, v238
	v_lshlrev_b32_e32 v144, 16, v239
	v_and_b32_e32 v145, 0xffff0000, v239
	s_waitcnt lgkmcnt(0)
	v_pk_fma_f32 v[148:149], v[0:1], v[144:145], 0 op_sel_hi:[0,1,0]
	s_nop 0
	s_waitcnt vmcnt(3)
	v_lshlrev_b32_e32 v152, 16, v240
	v_and_b32_e32 v153, 0xffff0000, v240
	v_lshlrev_b32_e32 v150, 16, v241
	v_and_b32_e32 v151, 0xffff0000, v241
	v_pk_fma_f32 v[148:149], v[0:1], v[150:151], v[148:149] op_sel:[1,0,0]
	s_nop 0
	s_nop 0
	v_pk_fma_f32 v[146:147], v[0:1], v[142:143], 0 op_sel_hi:[0,1,0]
	v_pk_fma_f32 v[146:147], v[0:1], v[152:153], v[146:147] op_sel:[1,0,0]
	v_pk_mul_f32 v[134:135], v[130:131], v[136:137] op_sel_hi:[0,1]
	v_pk_mul_f32 v[138:139], v[130:131], v[132:133] op_sel_hi:[0,1]
	s_nop 0
	s_waitcnt vmcnt(2)
	v_lshlrev_b32_e32 v152, 16, v242
	v_and_b32_e32 v153, 0xffff0000, v242
	v_lshlrev_b32_e32 v150, 16, v243
	v_and_b32_e32 v151, 0xffff0000, v243
	v_pk_fma_f32 v[148:149], v[2:3], v[150:151], v[148:149] op_sel_hi:[0,1,1]
	s_nop 0
	s_nop 0
	v_pk_fma_f32 v[146:147], v[2:3], v[152:153], v[146:147] op_sel_hi:[0,1,1]
	v_mov_b32_e32 v2, v3
	s_nop 0
	s_waitcnt vmcnt(1)
	v_lshlrev_b32_e32 v152, 16, v244
	v_and_b32_e32 v153, 0xffff0000, v244
	v_lshlrev_b32_e32 v150, 16, v245
	v_and_b32_e32 v151, 0xffff0000, v245
	v_pk_fma_f32 v[150:151], v[2:3], v[150:151], v[148:149] op_sel_hi:[0,1,1]
	v_pk_fma_f32 v[2:3], v[2:3], v[152:153], v[146:147] op_sel_hi:[0,1,1]
	s_nop 0
	s_nop 0
	ds_read2_b64 v[146:149], v53 offset0:3 offset1:4
	s_nop 0
	s_waitcnt vmcnt(0)
	v_lshlrev_b32_e32 v154, 16, v246
	v_and_b32_e32 v155, 0xffff0000, v246
	v_lshlrev_b32_e32 v152, 16, v247
	v_and_b32_e32 v153, 0xffff0000, v247
	s_waitcnt lgkmcnt(0)
	v_pk_fma_f32 v[150:151], v[146:147], v[152:153], v[150:151] op_sel_hi:[0,1,1]
	v_lshl_add_u64 v[236:237], s[10:11], 0, v[140:141]
	global_load_dwordx2 v[236:237], v[236:237], off
	v_lshl_add_u64 v[238:239], s[8:9], 0, v[140:141]
	global_load_dwordx2 v[238:239], v[238:239], off
	v_lshl_add_u64 v[240:241], s[44:45], 0, v[140:141]
	global_load_dwordx2 v[240:241], v[240:241], off
	v_lshl_add_u64 v[242:243], s[86:87], 0, v[140:141]
	global_load_dwordx2 v[242:243], v[242:243], off
	v_lshl_add_u64 v[244:245], s[0:1], 0, v[140:141]
	global_load_dwordx2 v[244:245], v[244:245], off
	v_lshl_add_u64 v[246:247], s[2:3], 0, v[140:141]
	global_load_dwordx2 v[246:247], v[246:247], off
	s_nop 0
	s_nop 0
	v_pk_fma_f32 v[2:3], v[146:147], v[154:155], v[2:3] op_sel_hi:[0,1,1]
	s_nop 0
	s_waitcnt vmcnt(5)
	v_lshlrev_b32_e32 v154, 16, v236
	v_and_b32_e32 v155, 0xffff0000, v236
	v_lshlrev_b32_e32 v152, 16, v237
	v_and_b32_e32 v153, 0xffff0000, v237
	v_pk_fma_f32 v[150:151], v[146:147], v[152:153], v[150:151] op_sel:[1,0,0]
	v_pk_fma_f32 v[2:3], v[146:147], v[154:155], v[2:3] op_sel:[1,0,0]
	s_nop 0
	s_nop 0
	s_nop 0
	s_waitcnt vmcnt(4)
	v_lshlrev_b32_e32 v152, 16, v238
	v_and_b32_e32 v153, 0xffff0000, v238
	v_lshlrev_b32_e32 v146, 16, v239
	v_and_b32_e32 v147, 0xffff0000, v239
	v_pk_fma_f32 v[146:147], v[148:149], v[146:147], v[150:151] op_sel_hi:[0,1,1]
	s_nop 0
	s_nop 0
	v_pk_fma_f32 v[2:3], v[148:149], v[152:153], v[2:3] op_sel_hi:[0,1,1]
	v_mov_b32_e32 v148, v149
	s_nop 0
	s_waitcnt vmcnt(3)
	v_lshlrev_b32_e32 v152, 16, v240
	v_and_b32_e32 v153, 0xffff0000, v240
	v_pk_fma_f32 v[2:3], v[148:149], v[152:153], v[2:3] op_sel_hi:[0,1,1]
	s_nop 0
	s_nop 0
	v_lshlrev_b32_e32 v150, 16, v241
	v_and_b32_e32 v151, 0xffff0000, v241
	v_pk_fma_f32 v[150:151], v[148:149], v[150:151], v[146:147] op_sel_hi:[0,1,1]
	ds_read2_b64 v[146:149], v53 offset0:5 offset1:6
	s_nop 0
	s_waitcnt vmcnt(2)
	v_lshlrev_b32_e32 v154, 16, v242
	v_and_b32_e32 v155, 0xffff0000, v242
	v_lshlrev_b32_e32 v152, 16, v243
	v_and_b32_e32 v153, 0xffff0000, v243
	s_waitcnt lgkmcnt(0)
	v_pk_fma_f32 v[150:151], v[146:147], v[152:153], v[150:151] op_sel_hi:[0,1,1]
	s_nop 0
	s_nop 0
	v_pk_fma_f32 v[2:3], v[146:147], v[154:155], v[2:3] op_sel_hi:[0,1,1]
	s_nop 0
	s_waitcnt vmcnt(1)
	v_lshlrev_b32_e32 v154, 16, v244
	v_and_b32_e32 v155, 0xffff0000, v244
	v_lshlrev_b32_e32 v152, 16, v245
	v_and_b32_e32 v153, 0xffff0000, v245
	v_pk_fma_f32 v[150:151], v[146:147], v[152:153], v[150:151] op_sel:[1,0,0]
	v_pk_fma_f32 v[2:3], v[146:147], v[154:155], v[2:3] op_sel:[1,0,0]
	s_nop 0
	s_nop 0
	s_nop 0
	s_waitcnt vmcnt(0)
	v_lshlrev_b32_e32 v152, 16, v246
	v_and_b32_e32 v153, 0xffff0000, v246
	v_lshlrev_b32_e32 v146, 16, v247
	v_and_b32_e32 v147, 0xffff0000, v247
	v_pk_fma_f32 v[146:147], v[148:149], v[146:147], v[150:151] op_sel_hi:[0,1,1]
	v_lshl_add_u64 v[236:237], s[96:97], 0, v[140:141]
	global_load_dwordx2 v[236:237], v[236:237], off
	v_lshl_add_u64 v[238:239], s[52:53], 0, v[140:141]
	global_load_dwordx2 v[238:239], v[238:239], off
	v_lshl_add_u64 v[240:241], s[50:51], 0, v[140:141]
	global_load_dwordx2 v[240:241], v[240:241], off
	v_lshl_add_u64 v[242:243], s[48:49], 0, v[140:141]
	global_load_dwordx2 v[242:243], v[242:243], off
	v_lshl_add_u64 v[244:245], s[46:47], 0, v[140:141]
	global_load_dwordx2 v[244:245], v[244:245], off
	s_nop 0
	s_nop 0
	v_pk_fma_f32 v[2:3], v[148:149], v[152:153], v[2:3] op_sel_hi:[0,1,1]
	v_mov_b32_e32 v148, v149
	s_nop 0
	s_waitcnt vmcnt(4)
	v_lshlrev_b32_e32 v152, 16, v236
	v_and_b32_e32 v153, 0xffff0000, v236
	v_pk_fma_f32 v[2:3], v[148:149], v[152:153], v[2:3] op_sel_hi:[0,1,1]
	s_nop 0
	s_nop 0
	v_lshlrev_b32_e32 v150, 16, v237
	v_and_b32_e32 v151, 0xffff0000, v237
	v_pk_fma_f32 v[150:151], v[148:149], v[150:151], v[146:147] op_sel_hi:[0,1,1]
	ds_read2_b64 v[146:149], v53 offset0:7 offset1:8
	s_nop 0
	s_waitcnt vmcnt(3)
	v_lshlrev_b32_e32 v154, 16, v238
	v_and_b32_e32 v155, 0xffff0000, v238
	v_lshlrev_b32_e32 v152, 16, v239
	v_and_b32_e32 v153, 0xffff0000, v239
	s_waitcnt lgkmcnt(0)
	v_pk_fma_f32 v[150:151], v[146:147], v[152:153], v[150:151] op_sel_hi:[0,1,1]
	s_nop 0
	s_nop 0
	v_pk_fma_f32 v[2:3], v[146:147], v[154:155], v[2:3] op_sel_hi:[0,1,1]
	s_nop 0
	s_waitcnt vmcnt(2)
	v_lshlrev_b32_e32 v154, 16, v240
	v_and_b32_e32 v155, 0xffff0000, v240
	v_lshlrev_b32_e32 v152, 16, v241
	v_and_b32_e32 v153, 0xffff0000, v241
	v_pk_fma_f32 v[150:151], v[146:147], v[152:153], v[150:151] op_sel:[1,0,0]
	v_pk_fma_f32 v[2:3], v[146:147], v[154:155], v[2:3] op_sel:[1,0,0]
	s_nop 0
	s_nop 0
	s_nop 0
	s_nop 0
	s_nop 0
	s_waitcnt vmcnt(1)
	v_lshlrev_b32_e32 v152, 16, v242
	v_and_b32_e32 v153, 0xffff0000, v242
	v_lshlrev_b32_e32 v146, 16, v243
	v_and_b32_e32 v147, 0xffff0000, v243
	v_pk_fma_f32 v[2:3], v[148:149], v[152:153], v[2:3] op_sel_hi:[0,1,1]
	v_pk_fma_f32 v[146:147], v[148:149], v[146:147], v[150:151] op_sel_hi:[0,1,1]
	s_nop 0
	s_waitcnt vmcnt(0)
	v_lshlrev_b32_e32 v150, 16, v244
	v_and_b32_e32 v151, 0xffff0000, v244
	v_lshlrev_b32_e32 v140, 16, v245
	v_and_b32_e32 v141, 0xffff0000, v245
	v_mov_b32_e32 v148, v149
	v_pk_mul_f32 v[152:153], v[148:149], v[140:141] op_sel_hi:[0,1]
	v_pk_fma_f32 v[140:141], v[148:149], v[140:141], v[146:147] op_sel_hi:[0,1,1]
	v_pk_fma_f32 v[2:3], v[148:149], v[150:151], v[2:3] op_sel_hi:[0,1,1]
	v_pk_fma_f32 v[142:143], v[0:1], v[142:143], v[2:3] op_sel_hi:[0,1,1] neg_lo:[1,0,0] neg_hi:[1,0,0]
	v_pk_fma_f32 v[0:1], v[0:1], v[144:145], v[140:141] op_sel_hi:[0,1,1] neg_lo:[1,0,0] neg_hi:[1,0,0]
	v_pk_fma_f32 v[0:1], v[130:131], v[136:137], v[0:1] op_sel_hi:[0,1,1]
	v_pk_fma_f32 v[130:131], v[130:131], v[132:133], v[142:143] op_sel_hi:[0,1,1]
	v_pk_fma_f32 v[132:133], v[92:93], v[130:131], v[138:139] op_sel_hi:[0,1,1] neg_lo:[0,0,1] neg_hi:[0,0,1]
	v_pk_fma_f32 v[138:139], v[90:91], v[140:141], v[152:153] op_sel_hi:[0,1,1] neg_lo:[0,0,1] neg_hi:[0,0,1]
	v_lshlrev_b64 v[140:141], 1, v[126:127]
	v_pk_fma_f32 v[130:131], v[92:93], v[0:1], v[134:135] op_sel_hi:[0,1,1] neg_lo:[0,0,1] neg_hi:[0,0,1]
	v_lshl_add_u64 v[236:237], s[30:31], 0, v[140:141]
	global_load_dwordx2 v[236:237], v[236:237], off offset:3072
	v_lshl_add_u64 v[238:239], s[28:29], 0, v[140:141]
	global_load_dwordx2 v[238:239], v[238:239], off offset:3072
	v_lshl_add_u64 v[134:135], s[30:31], 0, v[140:141]
	s_nop 0
	v_pk_mul_f32 v[154:155], v[148:149], v[150:151] op_sel_hi:[0,1]
	v_lshl_add_u32 v0, v128, 2, s17
	v_pk_fma_f32 v[136:137], v[90:91], v[2:3], v[154:155] op_sel_hi:[0,1,1] neg_lo:[0,0,1] neg_hi:[0,0,1]
	ds_read_b128 v[0:3], v0
	s_nop 0
	s_waitcnt vmcnt(1)
	v_lshlrev_b32_e32 v128, 16, v236
	v_and_b32_e32 v129, 0xffff0000, v236
	v_lshlrev_b32_e32 v126, 16, v237
	v_and_b32_e32 v127, 0xffff0000, v237
	s_waitcnt lgkmcnt(0)
	v_pk_fma_f32 v[128:129], v[0:1], v[136:137], v[128:129]
	v_lshl_add_u64 v[136:137], s[28:29], 0, v[140:141]
	v_pk_fma_f32 v[126:127], v[2:3], v[138:139], v[126:127]
	s_nop 0
	s_nop 0
	s_waitcnt vmcnt(0)
	v_lshlrev_b32_e32 v140, 16, v238
	v_and_b32_e32 v141, 0xffff0000, v238
	v_lshlrev_b32_e32 v138, 16, v239
	v_and_b32_e32 v139, 0xffff0000, v239
	v_pk_fma_f32 v[132:133], v[0:1], v[132:133], v[140:141]
	v_cvt_pk_bf16_f32 v0, v128, v129
	v_cvt_pk_bf16_f32 v1, v126, v127
	v_pk_fma_f32 v[130:131], v[2:3], v[130:131], v[138:139]
	v_cvt_pk_bf16_f32 v2, v132, v133
	s_nop 0
	v_cvt_pk_bf16_f32 v3, v130, v131
	global_store_dwordx2 v[134:135], v[0:1], off offset:3072
	global_store_dwordx2 v[136:137], v[2:3], off offset:3072
	v_mov_b32_e32 v0, v21
	ds_read_b32 v138, v53 offset:72
	v_lshlrev_b32_e32 v134, 2, v0
	v_add_u32_e32 v136, 0x700, v134
	v_ashrrev_i32_e32 v137, 31, v136
	v_lshlrev_b64 v[148:149], 1, v[136:137]
	v_lshl_add_u64 v[236:237], vcc, 0, v[148:149]
	global_load_dwordx2 v[236:237], v[236:237], off
	v_lshl_add_u64 v[238:239], s[42:43], 0, v[148:149]
	global_load_dwordx2 v[238:239], v[238:239], off
	v_lshl_add_u64 v[240:241], s[88:89], 0, v[148:149]
	global_load_dwordx2 v[240:241], v[240:241], off
	v_lshl_add_u64 v[242:243], s[36:37], 0, v[148:149]
	global_load_dwordx2 v[242:243], v[242:243], off
	v_lshl_add_u64 v[244:245], s[78:79], 0, v[148:149]
	global_load_dwordx2 v[244:245], v[244:245], off
	v_lshl_add_u64 v[246:247], s[76:77], 0, v[148:149]
	global_load_dwordx2 v[246:247], v[246:247], off
	s_nop 0
	s_nop 0
	v_lshl_add_u64 v[150:151], s[42:43], 0, v[148:149]
	s_nop 0
	s_nop 0
	s_nop 0
	v_ashrrev_i32_e32 v135, 31, v134
	s_nop 0
	s_waitcnt vmcnt(5)
	v_lshlrev_b32_e32 v140, 16, v236
	v_and_b32_e32 v141, 0xffff0000, v236
	v_lshlrev_b32_e32 v144, 16, v237
	v_and_b32_e32 v145, 0xffff0000, v237
	ds_read2_b64 v[0:3], v53 offset0:1 offset1:2
	s_nop 0
	s_waitcnt vmcnt(4)
	v_lshlrev_b32_e32 v150, 16, v238
	v_and_b32_e32 v151, 0xffff0000, v238
	v_lshlrev_b32_e32 v152, 16, v239
	v_and_b32_e32 v153, 0xffff0000, v239
	s_waitcnt lgkmcnt(0)
	v_pk_fma_f32 v[156:157], v[0:1], v[152:153], 0 op_sel_hi:[0,1,0]
	s_nop 0
	s_waitcnt vmcnt(3)
	v_lshlrev_b32_e32 v160, 16, v240
	v_and_b32_e32 v161, 0xffff0000, v240
	v_lshlrev_b32_e32 v158, 16, v241
	v_and_b32_e32 v159, 0xffff0000, v241
	v_pk_fma_f32 v[156:157], v[0:1], v[158:159], v[156:157] op_sel:[1,0,0]
	s_nop 0
	s_nop 0
	v_pk_fma_f32 v[154:155], v[0:1], v[150:151], 0 op_sel_hi:[0,1,0]
	v_pk_fma_f32 v[154:155], v[0:1], v[160:161], v[154:155] op_sel:[1,0,0]
	v_pk_mul_f32 v[142:143], v[138:139], v[144:145] op_sel_hi:[0,1]
	v_pk_mul_f32 v[146:147], v[138:139], v[140:141] op_sel_hi:[0,1]
	s_nop 0
	s_waitcnt vmcnt(2)
	v_lshlrev_b32_e32 v160, 16, v242
	v_and_b32_e32 v161, 0xffff0000, v242
	v_lshlrev_b32_e32 v158, 16, v243
	v_and_b32_e32 v159, 0xffff0000, v243
	v_pk_fma_f32 v[156:157], v[2:3], v[158:159], v[156:157] op_sel_hi:[0,1,1]
	s_nop 0
	s_nop 0
	v_pk_fma_f32 v[154:155], v[2:3], v[160:161], v[154:155] op_sel_hi:[0,1,1]
	v_mov_b32_e32 v2, v3
	s_nop 0
	s_waitcnt vmcnt(1)
	v_lshlrev_b32_e32 v160, 16, v244
	v_and_b32_e32 v161, 0xffff0000, v244
	v_lshlrev_b32_e32 v158, 16, v245
	v_and_b32_e32 v159, 0xffff0000, v245
	v_pk_fma_f32 v[158:159], v[2:3], v[158:159], v[156:157] op_sel_hi:[0,1,1]
	v_pk_fma_f32 v[2:3], v[2:3], v[160:161], v[154:155] op_sel_hi:[0,1,1]
	s_nop 0
	s_nop 0
	ds_read2_b64 v[154:157], v53 offset0:3 offset1:4
	s_nop 0
	s_waitcnt vmcnt(0)
	v_lshlrev_b32_e32 v162, 16, v246
	v_and_b32_e32 v163, 0xffff0000, v246
	v_lshlrev_b32_e32 v160, 16, v247
	v_and_b32_e32 v161, 0xffff0000, v247
	s_waitcnt lgkmcnt(0)
	v_pk_fma_f32 v[158:159], v[154:155], v[160:161], v[158:159] op_sel_hi:[0,1,1]
	v_lshl_add_u64 v[236:237], s[10:11], 0, v[148:149]
	global_load_dwordx2 v[236:237], v[236:237], off
	v_lshl_add_u64 v[238:239], s[8:9], 0, v[148:149]
	global_load_dwordx2 v[238:239], v[238:239], off
	v_lshl_add_u64 v[240:241], s[44:45], 0, v[148:149]
	global_load_dwordx2 v[240:241], v[240:241], off
	v_lshl_add_u64 v[242:243], s[86:87], 0, v[148:149]
	global_load_dwordx2 v[242:243], v[242:243], off
	v_lshl_add_u64 v[244:245], s[0:1], 0, v[148:149]
	global_load_dwordx2 v[244:245], v[244:245], off
	v_lshl_add_u64 v[246:247], s[2:3], 0, v[148:149]
	global_load_dwordx2 v[246:247], v[246:247], off
	s_nop 0
	s_nop 0
	v_pk_fma_f32 v[2:3], v[154:155], v[162:163], v[2:3] op_sel_hi:[0,1,1]
	s_nop 0
	s_waitcnt vmcnt(5)
	v_lshlrev_b32_e32 v162, 16, v236
	v_and_b32_e32 v163, 0xffff0000, v236
	v_lshlrev_b32_e32 v160, 16, v237
	v_and_b32_e32 v161, 0xffff0000, v237
	v_pk_fma_f32 v[158:159], v[154:155], v[160:161], v[158:159] op_sel:[1,0,0]
	v_pk_fma_f32 v[2:3], v[154:155], v[162:163], v[2:3] op_sel:[1,0,0]
	s_nop 0
	s_nop 0
	s_nop 0
	s_waitcnt vmcnt(4)
	v_lshlrev_b32_e32 v160, 16, v238
	v_and_b32_e32 v161, 0xffff0000, v238
	v_lshlrev_b32_e32 v154, 16, v239
	v_and_b32_e32 v155, 0xffff0000, v239
	v_pk_fma_f32 v[154:155], v[156:157], v[154:155], v[158:159] op_sel_hi:[0,1,1]
	s_nop 0
	s_nop 0
	v_pk_fma_f32 v[2:3], v[156:157], v[160:161], v[2:3] op_sel_hi:[0,1,1]
	v_mov_b32_e32 v156, v157
	s_nop 0
	s_waitcnt vmcnt(3)
	v_lshlrev_b32_e32 v160, 16, v240
	v_and_b32_e32 v161, 0xffff0000, v240
	v_pk_fma_f32 v[2:3], v[156:157], v[160:161], v[2:3] op_sel_hi:[0,1,1]
	s_nop 0
	s_nop 0
	v_lshlrev_b32_e32 v158, 16, v241
	v_and_b32_e32 v159, 0xffff0000, v241
	v_pk_fma_f32 v[158:159], v[156:157], v[158:159], v[154:155] op_sel_hi:[0,1,1]
	ds_read2_b64 v[154:157], v53 offset0:5 offset1:6
	s_nop 0
	s_waitcnt vmcnt(2)
	v_lshlrev_b32_e32 v162, 16, v242
	v_and_b32_e32 v163, 0xffff0000, v242
	v_lshlrev_b32_e32 v160, 16, v243
	v_and_b32_e32 v161, 0xffff0000, v243
	s_waitcnt lgkmcnt(0)
	v_pk_fma_f32 v[158:159], v[154:155], v[160:161], v[158:159] op_sel_hi:[0,1,1]
	s_nop 0
	s_nop 0
	v_pk_fma_f32 v[2:3], v[154:155], v[162:163], v[2:3] op_sel_hi:[0,1,1]
	s_nop 0
	s_waitcnt vmcnt(1)
	v_lshlrev_b32_e32 v162, 16, v244
	v_and_b32_e32 v163, 0xffff0000, v244
	v_lshlrev_b32_e32 v160, 16, v245
	v_and_b32_e32 v161, 0xffff0000, v245
	v_pk_fma_f32 v[158:159], v[154:155], v[160:161], v[158:159] op_sel:[1,0,0]
	v_pk_fma_f32 v[2:3], v[154:155], v[162:163], v[2:3] op_sel:[1,0,0]
	s_nop 0
	s_nop 0
	s_nop 0
	s_waitcnt vmcnt(0)
	v_lshlrev_b32_e32 v160, 16, v246
	v_and_b32_e32 v161, 0xffff0000, v246
	v_lshlrev_b32_e32 v154, 16, v247
	v_and_b32_e32 v155, 0xffff0000, v247
	v_pk_fma_f32 v[154:155], v[156:157], v[154:155], v[158:159] op_sel_hi:[0,1,1]
	v_lshl_add_u64 v[236:237], s[96:97], 0, v[148:149]
	global_load_dwordx2 v[236:237], v[236:237], off
	v_lshl_add_u64 v[238:239], s[52:53], 0, v[148:149]
	global_load_dwordx2 v[238:239], v[238:239], off
	v_lshl_add_u64 v[240:241], s[50:51], 0, v[148:149]
	global_load_dwordx2 v[240:241], v[240:241], off
	v_lshl_add_u64 v[242:243], s[48:49], 0, v[148:149]
	global_load_dwordx2 v[242:243], v[242:243], off
	v_lshl_add_u64 v[244:245], s[46:47], 0, v[148:149]
	global_load_dwordx2 v[244:245], v[244:245], off
	s_nop 0
	s_nop 0
	v_pk_fma_f32 v[2:3], v[156:157], v[160:161], v[2:3] op_sel_hi:[0,1,1]
	v_mov_b32_e32 v156, v157
	s_nop 0
	s_waitcnt vmcnt(4)
	v_lshlrev_b32_e32 v160, 16, v236
	v_and_b32_e32 v161, 0xffff0000, v236
	v_pk_fma_f32 v[2:3], v[156:157], v[160:161], v[2:3] op_sel_hi:[0,1,1]
	s_nop 0
	s_nop 0
	v_lshlrev_b32_e32 v158, 16, v237
	v_and_b32_e32 v159, 0xffff0000, v237
	v_pk_fma_f32 v[158:159], v[156:157], v[158:159], v[154:155] op_sel_hi:[0,1,1]
	ds_read2_b64 v[154:157], v53 offset0:7 offset1:8
	s_nop 0
	s_waitcnt vmcnt(3)
	v_lshlrev_b32_e32 v162, 16, v238
	v_and_b32_e32 v163, 0xffff0000, v238
	v_lshlrev_b32_e32 v160, 16, v239
	v_and_b32_e32 v161, 0xffff0000, v239
	s_waitcnt lgkmcnt(0)
	v_pk_fma_f32 v[158:159], v[154:155], v[160:161], v[158:159] op_sel_hi:[0,1,1]
	s_nop 0
	s_nop 0
	v_pk_fma_f32 v[2:3], v[154:155], v[162:163], v[2:3] op_sel_hi:[0,1,1]
	s_nop 0
	s_waitcnt vmcnt(2)
	v_lshlrev_b32_e32 v162, 16, v240
	v_and_b32_e32 v163, 0xffff0000, v240
	v_lshlrev_b32_e32 v160, 16, v241
	v_and_b32_e32 v161, 0xffff0000, v241
	v_pk_fma_f32 v[158:159], v[154:155], v[160:161], v[158:159] op_sel:[1,0,0]
	v_pk_fma_f32 v[2:3], v[154:155], v[162:163], v[2:3] op_sel:[1,0,0]
	s_nop 0
	s_nop 0
	s_nop 0
	s_nop 0
	s_nop 0
	s_waitcnt vmcnt(1)
	v_lshlrev_b32_e32 v160, 16, v242
	v_and_b32_e32 v161, 0xffff0000, v242
	v_lshlrev_b32_e32 v154, 16, v243
	v_and_b32_e32 v155, 0xffff0000, v243
	v_pk_fma_f32 v[2:3], v[156:157], v[160:161], v[2:3] op_sel_hi:[0,1,1]
	v_pk_fma_f32 v[154:155], v[156:157], v[154:155], v[158:159] op_sel_hi:[0,1,1]
	s_nop 0
	s_waitcnt vmcnt(0)
	v_lshlrev_b32_e32 v158, 16, v244
	v_and_b32_e32 v159, 0xffff0000, v244
	v_lshlrev_b32_e32 v148, 16, v245
	v_and_b32_e32 v149, 0xffff0000, v245
	v_mov_b32_e32 v156, v157
	v_pk_mul_f32 v[160:161], v[156:157], v[148:149] op_sel_hi:[0,1]
	v_pk_fma_f32 v[148:149], v[156:157], v[148:149], v[154:155] op_sel_hi:[0,1,1]
	v_pk_fma_f32 v[2:3], v[156:157], v[158:159], v[2:3] op_sel_hi:[0,1,1]
	v_pk_fma_f32 v[150:151], v[0:1], v[150:151], v[2:3] op_sel_hi:[0,1,1] neg_lo:[1,0,0] neg_hi:[1,0,0]
	v_pk_fma_f32 v[0:1], v[0:1], v[152:153], v[148:149] op_sel_hi:[0,1,1] neg_lo:[1,0,0] neg_hi:[1,0,0]
	v_pk_fma_f32 v[0:1], v[138:139], v[144:145], v[0:1] op_sel_hi:[0,1,1]
	v_pk_fma_f32 v[138:139], v[138:139], v[140:141], v[150:151] op_sel_hi:[0,1,1]
	v_pk_fma_f32 v[140:141], v[92:93], v[0:1], v[142:143] op_sel_hi:[0,1,1] neg_lo:[0,0,1] neg_hi:[0,0,1]
	v_lshl_add_u32 v0, v136, 2, s17
	v_lshlrev_b64 v[136:137], 1, v[134:135]
	v_lshl_add_u64 v[236:237], s[30:31], 0, v[136:137]
	global_load_dwordx2 v[236:237], v[236:237], off offset:3584
	v_lshl_add_u64 v[238:239], s[28:29], 0, v[136:137]
	global_load_dwordx2 v[238:239], v[238:239], off offset:3584
	v_lshl_add_u64 v[134:135], s[30:31], 0, v[136:137]
	s_nop 0
	v_pk_mul_f32 v[162:163], v[156:157], v[158:159] op_sel_hi:[0,1]
	v_pk_fma_f32 v[138:139], v[92:93], v[138:139], v[146:147] op_sel_hi:[0,1,1] neg_lo:[0,0,1] neg_hi:[0,0,1]
	v_pk_fma_f32 v[92:93], v[90:91], v[2:3], v[162:163] op_sel_hi:[0,1,1] neg_lo:[0,0,1] neg_hi:[0,0,1]
	ds_read_b128 v[0:3], v0
	v_pk_fma_f32 v[90:91], v[90:91], v[148:149], v[160:161] op_sel_hi:[0,1,1] neg_lo:[0,0,1] neg_hi:[0,0,1]
	s_nop 0
	s_waitcnt vmcnt(1)
	v_lshlrev_b32_e32 v144, 16, v236
	v_and_b32_e32 v145, 0xffff0000, v236
	v_lshlrev_b32_e32 v142, 16, v237
	v_and_b32_e32 v143, 0xffff0000, v237
	s_waitcnt lgkmcnt(0)
	v_pk_fma_f32 v[90:91], v[2:3], v[90:91], v[142:143]
	v_lshl_add_u64 v[142:143], s[28:29], 0, v[136:137]
	s_nop 0
	v_pk_fma_f32 v[92:93], v[0:1], v[92:93], v[144:145]
	s_nop 0
	s_waitcnt vmcnt(0)
	v_lshlrev_b32_e32 v144, 16, v238
	v_and_b32_e32 v145, 0xffff0000, v238
	v_lshlrev_b32_e32 v136, 16, v239
	v_and_b32_e32 v137, 0xffff0000, v239
	v_pk_fma_f32 v[138:139], v[0:1], v[138:139], v[144:145]
	v_cvt_pk_bf16_f32 v0, v92, v93
	v_cvt_pk_bf16_f32 v1, v90, v91
	v_pk_fma_f32 v[136:137], v[2:3], v[140:141], v[136:137]
	v_cvt_pk_bf16_f32 v2, v138, v139
	s_nop 0
	v_cvt_pk_bf16_f32 v3, v136, v137
	global_store_dwordx2 v[134:135], v[0:1], off offset:3584
	global_store_dwordx2 v[142:143], v[2:3], off offset:3584
	v_mul_f32_e32 v0, v81, v81
	v_mul_f32_e32 v1, v15, v15
	v_fmac_f32_e32 v0, v80, v80
	v_fmac_f32_e32 v1, v14, v14
	v_mov_b32_e32 v2, v13
	v_mov_b32_e32 v3, v85
	v_add_f32_e32 v53, v0, v1
	v_mov_b32_e32 v0, v12
	v_mov_b32_e32 v1, v84
	v_pk_mul_f32 v[2:3], v[2:3], v[2:3]
	v_mov_b32_e32 v134, v11
	v_mov_b32_e32 v135, v83
	v_pk_fma_f32 v[0:1], v[0:1], v[0:1], v[2:3]
	v_mov_b32_e32 v2, v10
	v_mov_b32_e32 v3, v82
	v_pk_mul_f32 v[134:135], v[134:135], v[134:135]
	v_mul_f32_e32 v59, v112, v112
	v_pk_fma_f32 v[2:3], v[2:3], v[2:3], v[134:135]
	v_pk_mul_f32 v[134:135], v[96:97], v[96:97]
	v_pk_add_f32 v[0:1], v[0:1], v[2:3]
	v_mul_f32_e32 v2, v89, v89
	v_mul_f32_e32 v3, v87, v87
	v_fmac_f32_e32 v2, v88, v88
	v_fmac_f32_e32 v3, v86, v86
	v_add_f32_e32 v2, v2, v3
	v_add_f32_e32 v53, v53, v2
	v_pk_mul_f32 v[2:3], v[94:95], v[94:95]
	v_mul_f32_e32 v61, v113, v113
	v_pk_mov_b32 v[140:141], v[134:135], v[2:3] op_sel:[1,0]
	v_mov_b32_e32 v135, v3
	v_pk_add_f32 v[2:3], v[140:141], v[134:135]
	v_pk_add_f32 v[0:1], v[0:1], v[0:1] op_sel:[0,1] op_sel_hi:[1,0]
	v_pk_add_f32 v[2:3], v[2:3], v[2:3] op_sel:[0,1] op_sel_hi:[1,0]
	v_mov_b32_e32 v1, v59
	v_mov_b32_e32 v3, v61
	v_pk_add_f32 v[0:1], v[0:1], v[2:3]
	v_mul_f32_e32 v2, v105, v105
	v_mul_f32_e32 v134, v103, v103
	v_mul_f32_e32 v63, v110, v110
	v_mul_f32_e32 v65, v111, v111
	v_pk_fma_f32 v[2:3], v[104:105], v[104:105], v[2:3] op_sel_hi:[1,1,0]
	v_pk_fma_f32 v[134:135], v[102:103], v[102:103], v[134:135] op_sel_hi:[1,1,0]
	v_mov_b32_e32 v3, v63
	v_mov_b32_e32 v135, v65
	v_pk_add_f32 v[2:3], v[2:3], v[134:135]
	v_pk_mul_f32 v[134:135], v[120:121], v[120:121]
	v_pk_add_f32 v[0:1], v[0:1], v[2:3]
	v_pk_mul_f32 v[2:3], v[118:119], v[118:119]
	v_mul_f32_e32 v59, v92, v92
	v_pk_mov_b32 v[140:141], v[134:135], v[2:3] op_sel:[1,0]
	v_mov_b32_e32 v135, v3
	v_pk_add_f32 v[2:3], v[140:141], v[134:135]
	v_mul_f32_e32 v61, v93, v93
	v_pk_add_f32 v[0:1], v[0:1], v[0:1] op_sel:[0,1] op_sel_hi:[1,0]
	v_pk_add_f32 v[2:3], v[2:3], v[2:3] op_sel:[0,1] op_sel_hi:[1,0]
	v_mov_b32_e32 v1, v59
	v_mov_b32_e32 v3, v61
	v_pk_add_f32 v[0:1], v[0:1], v[2:3]
	v_mul_f32_e32 v2, v129, v129
	v_mul_f32_e32 v134, v127, v127
	v_mul_f32_e32 v63, v90, v90
	v_mul_f32_e32 v65, v91, v91
	v_pk_fma_f32 v[2:3], v[128:129], v[128:129], v[2:3] op_sel_hi:[1,1,0]
	v_pk_fma_f32 v[134:135], v[126:127], v[126:127], v[134:135] op_sel_hi:[1,1,0]
	v_mov_b32_e32 v3, v63
	v_mov_b32_e32 v135, v65
	v_pk_add_f32 v[2:3], v[2:3], v[134:135]
	v_mul_f32_e32 v55, v101, v101
	v_pk_add_f32 v[0:1], v[0:1], v[2:3]
	v_mul_f32_e32 v57, v99, v99
	v_add_f32_e32 v0, v0, v1
	ds_bpermute_b32 v1, v31, v0
	v_fmac_f32_e32 v55, v100, v100
	v_fmac_f32_e32 v57, v98, v98
	v_add_f32_e32 v55, v55, v57
	v_add_f32_e32 v53, v53, v55
	s_waitcnt lgkmcnt(0)
	v_add_f32_e32 v0, v0, v1
	ds_bpermute_b32 v1, v33, v0
	v_mul_f32_e32 v55, v109, v109
	v_mul_f32_e32 v57, v107, v107
	v_fmac_f32_e32 v55, v108, v108
	v_fmac_f32_e32 v57, v106, v106
	s_waitcnt lgkmcnt(0)
	v_add_f32_e32 v0, v0, v1
	ds_bpermute_b32 v1, v35, v0
	v_add_f32_e32 v2, v55, v57
	v_add_f32_e32 v2, v53, v2
	v_mul_f32_e32 v3, v117, v117
	v_mul_f32_e32 v53, v115, v115
	s_waitcnt lgkmcnt(0)
	v_add_f32_e32 v0, v0, v1
	ds_bpermute_b32 v1, v41, v0
	v_fmac_f32_e32 v3, v116, v116
	v_fmac_f32_e32 v53, v114, v114
	v_add_f32_e32 v3, v3, v53
	v_add_f32_e32 v2, v2, v3
	s_waitcnt lgkmcnt(0)
	v_add_f32_e32 v0, v0, v1
	ds_bpermute_b32 v1, v37, v0
	v_mul_f32_e32 v3, v125, v125
	v_mul_f32_e32 v53, v123, v123
	v_fmac_f32_e32 v3, v124, v124
	v_fmac_f32_e32 v53, v122, v122
	s_waitcnt lgkmcnt(0)
	v_add_f32_e32 v0, v0, v1
	ds_bpermute_b32 v1, v39, v0
	v_add_f32_e32 v3, v3, v53
	v_add_f32_e32 v2, v2, v3
	v_mul_f32_e32 v3, v133, v133
	v_mul_f32_e32 v53, v131, v131
	s_waitcnt lgkmcnt(0)
	v_add_f32_e32 v0, v0, v1
	v_fmamk_f32 v0, v0, 0x3a000000, v189
	v_mul_f32_e32 v1, 0x4f800000, v0
	v_cmp_gt_f32_e32 vcc, s84, v0
	v_fmac_f32_e32 v3, v132, v132
	v_fmac_f32_e32 v53, v130, v130
	v_cndmask_b32_e32 v0, v0, v1, vcc
	v_add_f32_e32 v3, v3, v53
	v_sqrt_f32_e32 v1, v0
	v_add_f32_e32 v2, v2, v3
	v_mul_f32_e32 v3, v139, v139
	v_mul_f32_e32 v53, v137, v137
	v_fmac_f32_e32 v3, v138, v138
	v_fmac_f32_e32 v53, v136, v136
	v_add_f32_e32 v3, v3, v53
	v_add_f32_e32 v2, v2, v3
	v_add_u32_e32 v3, -1, v1
	v_fma_f32 v53, -v3, v1, v0
	v_cmp_ge_f32_e64 s[46:47], 0, v53
	v_add_u32_e32 v53, 1, v1
	s_mov_b32 s33, 0xff61b1e6
	v_cndmask_b32_e64 v3, v1, v3, s[46:47]
	v_fma_f32 v1, -v53, v1, v0
	v_cmp_lt_f32_e64 s[46:47], 0, v1
	s_nop 1
	v_cndmask_b32_e64 v1, v3, v53, s[46:47]
	v_mul_f32_e32 v3, 0x37800000, v1
	v_cndmask_b32_e32 v1, v1, v3, vcc
	ds_bpermute_b32 v3, v31, v2
	v_cmp_class_f32_e32 vcc, v0, v190
	v_cndmask_b32_e32 v53, v1, v0, vcc
	s_waitcnt lgkmcnt(0)
	v_add_f32_e32 v0, v2, v3
	ds_bpermute_b32 v1, v33, v0
	v_div_scale_f32 v57, s[0:1], v53, v53, 1.0
	v_rcp_f32_e32 v55, v57
	v_div_scale_f32 v61, vcc, 1.0, v53, 1.0
	s_waitcnt lgkmcnt(0)
	v_add_f32_e32 v0, v0, v1
	ds_bpermute_b32 v1, v35, v0
	v_fma_f32 v2, -v57, v55, 1.0
	v_fmac_f32_e32 v55, v2, v55
	v_mul_f32_e32 v59, v61, v55
	v_fma_f32 v65, -v57, v59, v61
	s_waitcnt lgkmcnt(0)
	v_add_f32_e32 v63, v0, v1
	ds_read_b128 v[0:3], v25
	ds_read_b128 v[142:145], v25 offset:1024
	ds_read_b128 v[146:149], v25 offset:2048
	ds_read_b128 v[150:153], v25 offset:3072
	ds_read_b128 v[154:157], v25 offset:4096
	ds_read_b128 v[158:161], v25 offset:5120
	ds_read_b128 v[162:165], v25 offset:6144
	ds_read_b128 v[174:177], v25 offset:7168
	ds_read_b128 v[178:181], v25 offset:8192
	ds_read_b128 v[182:185], v25 offset:9216
	ds_read_b128 v[198:201], v25 offset:10240
	ds_read_b128 v[202:205], v25 offset:11264
	ds_read_b128 v[206:209], v25 offset:12288
	ds_read_b128 v[210:213], v25 offset:13312
	ds_read_b128 v[214:217], v25 offset:14336
	ds_read_b128 v[224:227], v25 offset:15360
	s_waitcnt lgkmcnt(7)
	v_mov_b32_e32 v134, v178
	v_mov_b32_e32 v135, v1
	v_mov_b32_e32 v166, v180
	v_mov_b32_e32 v167, v3
	v_pk_mul_f32 v[140:141], v[12:13], v[134:135]
	v_mov_b32_e32 v1, v179
	v_pk_mul_f32 v[178:179], v[10:11], v[166:167]
	v_mov_b32_e32 v3, v181
	v_pk_fma_f32 v[140:141], v[12:13], v[0:1], v[140:141] op_sel:[0,0,1] op_sel_hi:[1,1,0]
	v_pk_fma_f32 v[178:179], v[10:11], v[2:3], v[178:179] op_sel:[0,0,1] op_sel_hi:[1,1,0]
	v_pk_mul_f32 v[134:135], v[80:81], v[134:135]
	v_pk_add_f32 v[140:141], v[140:141], v[178:179]
	s_waitcnt lgkmcnt(6)
	v_mov_b32_e32 v178, v182
	v_mov_b32_e32 v179, v143
	v_mov_b32_e32 v143, v183
	v_mov_b32_e32 v182, v184
	v_mov_b32_e32 v183, v145
	v_pk_mul_f32 v[180:181], v[84:85], v[178:179]
	v_pk_mul_f32 v[218:219], v[82:83], v[182:183]
	v_mov_b32_e32 v145, v185
	v_pk_fma_f32 v[180:181], v[84:85], v[142:143], v[180:181] op_sel:[0,0,1] op_sel_hi:[1,1,0]
	v_pk_fma_f32 v[184:185], v[82:83], v[144:145], v[218:219] op_sel:[0,0,1] op_sel_hi:[1,1,0]
	v_pk_add_f32 v[140:141], v[140:141], 0 op_sel_hi:[1,0]
	v_pk_add_f32 v[180:181], v[180:181], v[184:185]
	v_pk_fma_f32 v[0:1], v[80:81], v[0:1], v[134:135] op_sel:[0,0,1] op_sel_hi:[1,1,0]
	v_pk_add_f32 v[140:141], v[140:141], v[180:181]
	s_waitcnt lgkmcnt(5)
	v_mov_b32_e32 v180, v198
	v_mov_b32_e32 v181, v147
	v_mov_b32_e32 v147, v199
	v_mov_b32_e32 v198, v200
	v_mov_b32_e32 v199, v149
	v_pk_mul_f32 v[184:185], v[96:97], v[180:181]
	v_pk_mul_f32 v[218:219], v[94:95], v[198:199]
	v_mov_b32_e32 v149, v201
	v_pk_fma_f32 v[184:185], v[96:97], v[146:147], v[184:185] op_sel:[0,0,1] op_sel_hi:[1,1,0]
	v_pk_fma_f32 v[200:201], v[94:95], v[148:149], v[218:219] op_sel:[0,0,1] op_sel_hi:[1,1,0]
	v_pk_mul_f32 v[134:135], v[14:15], v[166:167]
	v_pk_add_f32 v[184:185], v[184:185], v[200:201]
	v_pk_fma_f32 v[2:3], v[14:15], v[2:3], v[134:135] op_sel:[0,0,1] op_sel_hi:[1,1,0]
	v_pk_add_f32 v[140:141], v[140:141], v[184:185]
	s_waitcnt lgkmcnt(4)
	v_mov_b32_e32 v184, v202
	v_mov_b32_e32 v185, v151
	v_mov_b32_e32 v151, v203
	v_mov_b32_e32 v202, v204
	v_mov_b32_e32 v203, v153
	v_pk_add_f32 v[0:1], v[0:1], v[2:3]
	v_pk_mul_f32 v[2:3], v[88:89], v[178:179]
	v_pk_mul_f32 v[134:135], v[86:87], v[182:183]
	v_pk_mul_f32 v[200:201], v[104:105], v[184:185]
	v_pk_mul_f32 v[218:219], v[102:103], v[202:203]
	v_mov_b32_e32 v153, v205
	v_pk_fma_f32 v[2:3], v[88:89], v[142:143], v[2:3] op_sel:[0,0,1] op_sel_hi:[1,1,0]
	v_pk_fma_f32 v[134:135], v[86:87], v[144:145], v[134:135] op_sel:[0,0,1] op_sel_hi:[1,1,0]
	v_pk_fma_f32 v[200:201], v[104:105], v[150:151], v[200:201] op_sel:[0,0,1] op_sel_hi:[1,1,0]
	v_pk_fma_f32 v[204:205], v[102:103], v[152:153], v[218:219] op_sel:[0,0,1] op_sel_hi:[1,1,0]
	v_pk_add_f32 v[0:1], v[0:1], 0 op_sel_hi:[1,0]
	v_pk_add_f32 v[2:3], v[2:3], v[134:135]
	v_pk_add_f32 v[200:201], v[200:201], v[204:205]
	v_pk_add_f32 v[0:1], v[0:1], v[2:3]
	v_pk_mul_f32 v[2:3], v[100:101], v[180:181]
	v_pk_mul_f32 v[134:135], v[98:99], v[198:199]
	v_pk_add_f32 v[140:141], v[140:141], v[200:201]
	s_waitcnt lgkmcnt(3)
	v_mov_b32_e32 v200, v206
	v_mov_b32_e32 v201, v155
	v_mov_b32_e32 v155, v207
	v_mov_b32_e32 v206, v208
	v_mov_b32_e32 v207, v157
	v_pk_fma_f32 v[2:3], v[100:101], v[146:147], v[2:3] op_sel:[0,0,1] op_sel_hi:[1,1,0]
	v_pk_fma_f32 v[134:135], v[98:99], v[148:149], v[134:135] op_sel:[0,0,1] op_sel_hi:[1,1,0]
	v_pk_mul_f32 v[204:205], v[112:113], v[200:201]
	v_pk_mul_f32 v[218:219], v[110:111], v[206:207]
	v_mov_b32_e32 v157, v209
	v_pk_add_f32 v[2:3], v[2:3], v[134:135]
	v_pk_fma_f32 v[204:205], v[112:113], v[154:155], v[204:205] op_sel:[0,0,1] op_sel_hi:[1,1,0]
	v_pk_fma_f32 v[208:209], v[110:111], v[156:157], v[218:219] op_sel:[0,0,1] op_sel_hi:[1,1,0]
	v_pk_add_f32 v[0:1], v[0:1], v[2:3]
	v_pk_mul_f32 v[2:3], v[108:109], v[184:185]
	v_pk_mul_f32 v[134:135], v[106:107], v[202:203]
	v_pk_add_f32 v[204:205], v[204:205], v[208:209]
	v_pk_fma_f32 v[2:3], v[108:109], v[150:151], v[2:3] op_sel:[0,0,1] op_sel_hi:[1,1,0]
	v_pk_fma_f32 v[134:135], v[106:107], v[152:153], v[134:135] op_sel:[0,0,1] op_sel_hi:[1,1,0]
	v_pk_add_f32 v[140:141], v[140:141], v[204:205]
	s_waitcnt lgkmcnt(2)
	v_mov_b32_e32 v204, v210
	v_mov_b32_e32 v205, v159
	v_mov_b32_e32 v159, v211
	v_mov_b32_e32 v210, v212
	v_mov_b32_e32 v211, v161
	v_pk_add_f32 v[2:3], v[2:3], v[134:135]
	v_pk_mul_f32 v[208:209], v[120:121], v[204:205]
	v_pk_mul_f32 v[218:219], v[118:119], v[210:211]
	v_mov_b32_e32 v161, v213
	v_pk_add_f32 v[0:1], v[0:1], v[2:3]
	v_pk_mul_f32 v[2:3], v[116:117], v[200:201]
	v_pk_mul_f32 v[134:135], v[114:115], v[206:207]
	v_pk_fma_f32 v[208:209], v[120:121], v[158:159], v[208:209] op_sel:[0,0,1] op_sel_hi:[1,1,0]
	v_pk_fma_f32 v[212:213], v[118:119], v[160:161], v[218:219] op_sel:[0,0,1] op_sel_hi:[1,1,0]
	v_pk_fma_f32 v[2:3], v[116:117], v[154:155], v[2:3] op_sel:[0,0,1] op_sel_hi:[1,1,0]
	v_pk_fma_f32 v[134:135], v[114:115], v[156:157], v[134:135] op_sel:[0,0,1] op_sel_hi:[1,1,0]
	v_pk_add_f32 v[208:209], v[208:209], v[212:213]
	v_pk_add_f32 v[2:3], v[2:3], v[134:135]
	v_pk_add_f32 v[140:141], v[140:141], v[208:209]
	s_waitcnt lgkmcnt(1)
	v_mov_b32_e32 v208, v214
	v_mov_b32_e32 v209, v163
	v_mov_b32_e32 v163, v215
	v_mov_b32_e32 v214, v216
	v_mov_b32_e32 v215, v165
	v_pk_add_f32 v[0:1], v[0:1], v[2:3]
	v_pk_mul_f32 v[2:3], v[124:125], v[204:205]
	v_pk_mul_f32 v[134:135], v[122:123], v[210:211]
	v_pk_mul_f32 v[212:213], v[128:129], v[208:209]
	v_pk_mul_f32 v[218:219], v[126:127], v[214:215]
	v_mov_b32_e32 v165, v217
	v_pk_fma_f32 v[2:3], v[124:125], v[158:159], v[2:3] op_sel:[0,0,1] op_sel_hi:[1,1,0]
	v_pk_fma_f32 v[134:135], v[122:123], v[160:161], v[134:135] op_sel:[0,0,1] op_sel_hi:[1,1,0]
	v_pk_fma_f32 v[212:213], v[128:129], v[162:163], v[212:213] op_sel:[0,0,1] op_sel_hi:[1,1,0]
	v_pk_fma_f32 v[216:217], v[126:127], v[164:165], v[218:219] op_sel:[0,0,1] op_sel_hi:[1,1,0]
	v_pk_add_f32 v[2:3], v[2:3], v[134:135]
	v_pk_add_f32 v[212:213], v[212:213], v[216:217]
	v_pk_add_f32 v[0:1], v[0:1], v[2:3]
	v_pk_mul_f32 v[2:3], v[132:133], v[208:209]
	v_pk_mul_f32 v[134:135], v[130:131], v[214:215]
	v_pk_add_f32 v[140:141], v[140:141], v[212:213]
	s_waitcnt lgkmcnt(0)
	v_mov_b32_e32 v212, v224
	v_mov_b32_e32 v213, v175
	v_mov_b32_e32 v218, v226
	v_mov_b32_e32 v219, v177
	v_pk_fma_f32 v[2:3], v[132:133], v[162:163], v[2:3] op_sel:[0,0,1] op_sel_hi:[1,1,0]
	v_pk_fma_f32 v[134:135], v[130:131], v[164:165], v[134:135] op_sel:[0,0,1] op_sel_hi:[1,1,0]
	v_pk_mul_f32 v[216:217], v[92:93], v[212:213]
	v_mov_b32_e32 v175, v225
	v_pk_mul_f32 v[224:225], v[90:91], v[218:219]
	v_mov_b32_e32 v177, v227
	v_pk_add_f32 v[2:3], v[2:3], v[134:135]
	v_pk_fma_f32 v[216:217], v[92:93], v[174:175], v[216:217] op_sel:[0,0,1] op_sel_hi:[1,1,0]
	v_pk_fma_f32 v[224:225], v[90:91], v[176:177], v[224:225] op_sel:[0,0,1] op_sel_hi:[1,1,0]
	v_pk_add_f32 v[0:1], v[0:1], v[2:3]
	v_pk_mul_f32 v[2:3], v[138:139], v[212:213]
	v_pk_mul_f32 v[134:135], v[136:137], v[218:219]
	v_pk_add_f32 v[216:217], v[216:217], v[224:225]
	v_pk_fma_f32 v[2:3], v[138:139], v[174:175], v[2:3] op_sel:[0,0,1] op_sel_hi:[1,1,0]
	v_pk_fma_f32 v[134:135], v[136:137], v[176:177], v[134:135] op_sel:[0,0,1] op_sel_hi:[1,1,0]
	v_pk_add_f32 v[140:141], v[140:141], v[216:217]
	v_pk_add_f32 v[2:3], v[2:3], v[134:135]
	ds_read_b128 v[144:147], v25 offset:16384
	ds_read_b128 v[148:151], v25 offset:17408
	ds_read_b128 v[152:155], v25 offset:18432
	ds_read_b128 v[156:159], v25 offset:19456
	ds_read_b128 v[160:163], v25 offset:20480
	ds_read_b128 v[164:167], v25 offset:21504
	ds_read_b128 v[174:177], v25 offset:22528
	ds_read_b128 v[178:181], v25 offset:23552
	ds_read_b128 v[182:185], v25 offset:24576
	ds_read_b128 v[198:201], v25 offset:25600
	ds_read_b128 v[202:205], v25 offset:26624
	ds_read_b128 v[206:209], v25 offset:27648
	ds_read_b128 v[210:213], v25 offset:28672
	ds_read_b128 v[214:217], v25 offset:29696
	ds_read_b128 v[224:227], v25 offset:30720
	ds_read_b128 v[228:231], v25 offset:31744
	v_pk_add_f32 v[0:1], v[0:1], v[2:3]
	s_waitcnt lgkmcnt(7)
	v_mov_b32_e32 v2, v182
	v_mov_b32_e32 v3, v145
	v_mov_b32_e32 v145, v183
	v_mov_b32_e32 v182, v184
	v_mov_b32_e32 v183, v147
	v_pk_mul_f32 v[134:135], v[12:13], v[2:3]
	v_pk_mul_f32 v[142:143], v[10:11], v[182:183]
	v_mov_b32_e32 v147, v185
	v_pk_fma_f32 v[134:135], v[12:13], v[144:145], v[134:135] op_sel:[0,0,1] op_sel_hi:[1,1,0]
	v_pk_fma_f32 v[142:143], v[10:11], v[146:147], v[142:143] op_sel:[0,0,1] op_sel_hi:[1,1,0]
	s_waitcnt lgkmcnt(6)
	v_mov_b32_e32 v184, v198
	v_mov_b32_e32 v185, v149
	v_mov_b32_e32 v149, v199
	v_mov_b32_e32 v198, v200
	v_mov_b32_e32 v199, v151
	v_pk_add_f32 v[134:135], v[134:135], v[142:143]
	v_pk_mul_f32 v[142:143], v[84:85], v[184:185]
	v_pk_mul_f32 v[218:219], v[82:83], v[198:199]
	v_mov_b32_e32 v151, v201
	v_pk_fma_f32 v[142:143], v[84:85], v[148:149], v[142:143] op_sel:[0,0,1] op_sel_hi:[1,1,0]
	v_pk_fma_f32 v[200:201], v[82:83], v[150:151], v[218:219] op_sel:[0,0,1] op_sel_hi:[1,1,0]
	v_pk_add_f32 v[134:135], v[134:135], 0 op_sel_hi:[1,0]
	v_pk_add_f32 v[142:143], v[142:143], v[200:201]
	s_waitcnt lgkmcnt(5)
	v_mov_b32_e32 v200, v202
	v_mov_b32_e32 v201, v153
	v_mov_b32_e32 v153, v203
	v_mov_b32_e32 v202, v204
	v_mov_b32_e32 v203, v155
	v_pk_add_f32 v[134:135], v[134:135], v[142:143]
	v_pk_mul_f32 v[142:143], v[96:97], v[200:201]
	v_pk_mul_f32 v[218:219], v[94:95], v[202:203]
	v_mov_b32_e32 v155, v205
	v_pk_fma_f32 v[142:143], v[96:97], v[152:153], v[142:143] op_sel:[0,0,1] op_sel_hi:[1,1,0]
	v_pk_fma_f32 v[204:205], v[94:95], v[154:155], v[218:219] op_sel:[0,0,1] op_sel_hi:[1,1,0]
	v_pk_mul_f32 v[2:3], v[80:81], v[2:3]
	v_pk_add_f32 v[142:143], v[142:143], v[204:205]
	s_waitcnt lgkmcnt(4)
	v_mov_b32_e32 v204, v206
	v_mov_b32_e32 v205, v157
	v_mov_b32_e32 v157, v207
	v_mov_b32_e32 v206, v208
	v_mov_b32_e32 v207, v159
	v_pk_add_f32 v[134:135], v[134:135], v[142:143]
	v_pk_mul_f32 v[142:143], v[104:105], v[204:205]
	v_pk_mul_f32 v[218:219], v[102:103], v[206:207]
	v_mov_b32_e32 v159, v209
	v_pk_fma_f32 v[142:143], v[104:105], v[156:157], v[142:143] op_sel:[0,0,1] op_sel_hi:[1,1,0]
	v_pk_fma_f32 v[208:209], v[102:103], v[158:159], v[218:219] op_sel:[0,0,1] op_sel_hi:[1,1,0]
	v_pk_fma_f32 v[2:3], v[80:81], v[144:145], v[2:3] op_sel:[0,0,1] op_sel_hi:[1,1,0]
	v_pk_add_f32 v[142:143], v[142:143], v[208:209]
	s_waitcnt lgkmcnt(3)
	v_mov_b32_e32 v208, v210
	v_mov_b32_e32 v209, v161
	v_mov_b32_e32 v161, v211
	v_mov_b32_e32 v210, v212
	v_mov_b32_e32 v211, v163
	v_pk_add_f32 v[134:135], v[134:135], v[142:143]
	v_pk_mul_f32 v[142:143], v[112:113], v[208:209]
	v_pk_mul_f32 v[218:219], v[110:111], v[210:211]
	v_mov_b32_e32 v163, v213
	v_pk_fma_f32 v[142:143], v[112:113], v[160:161], v[142:143] op_sel:[0,0,1] op_sel_hi:[1,1,0]
	v_pk_fma_f32 v[212:213], v[110:111], v[162:163], v[218:219] op_sel:[0,0,1] op_sel_hi:[1,1,0]
	v_pk_mul_f32 v[144:145], v[86:87], v[198:199]
	v_pk_add_f32 v[142:143], v[142:143], v[212:213]
	s_waitcnt lgkmcnt(2)
	v_mov_b32_e32 v212, v214
	v_mov_b32_e32 v213, v165
	v_mov_b32_e32 v165, v215
	v_mov_b32_e32 v214, v216
	v_mov_b32_e32 v215, v167
	v_pk_add_f32 v[134:135], v[134:135], v[142:143]
	v_pk_mul_f32 v[142:143], v[120:121], v[212:213]
	v_pk_mul_f32 v[218:219], v[118:119], v[214:215]
	v_mov_b32_e32 v167, v217
	v_pk_fma_f32 v[142:143], v[120:121], v[164:165], v[142:143] op_sel:[0,0,1] op_sel_hi:[1,1,0]
	v_pk_fma_f32 v[216:217], v[118:119], v[166:167], v[218:219] op_sel:[0,0,1] op_sel_hi:[1,1,0]
	s_waitcnt lgkmcnt(1)
	v_mov_b32_e32 v218, v226
	v_pk_add_f32 v[142:143], v[142:143], v[216:217]
	v_mov_b32_e32 v216, v224
	v_mov_b32_e32 v217, v175
	v_mov_b32_e32 v219, v177
	v_pk_add_f32 v[134:135], v[134:135], v[142:143]
	v_pk_mul_f32 v[142:143], v[128:129], v[216:217]
	v_mov_b32_e32 v175, v225
	v_pk_mul_f32 v[224:225], v[126:127], v[218:219]
	v_mov_b32_e32 v177, v227
	v_pk_fma_f32 v[142:143], v[128:129], v[174:175], v[142:143] op_sel:[0,0,1] op_sel_hi:[1,1,0]
	v_pk_fma_f32 v[224:225], v[126:127], v[176:177], v[224:225] op_sel:[0,0,1] op_sel_hi:[1,1,0]
	s_waitcnt lgkmcnt(0)
	v_mov_b32_e32 v226, v230
	v_pk_add_f32 v[142:143], v[142:143], v[224:225]
	v_mov_b32_e32 v224, v228
	v_mov_b32_e32 v225, v179
	v_mov_b32_e32 v227, v181
	v_pk_add_f32 v[134:135], v[134:135], v[142:143]
	v_pk_mul_f32 v[142:143], v[92:93], v[224:225]
	v_mov_b32_e32 v179, v229
	v_pk_mul_f32 v[228:229], v[90:91], v[226:227]
	v_mov_b32_e32 v181, v231
	v_pk_fma_f32 v[142:143], v[92:93], v[178:179], v[142:143] op_sel:[0,0,1] op_sel_hi:[1,1,0]
	v_pk_fma_f32 v[228:229], v[90:91], v[180:181], v[228:229] op_sel:[0,0,1] op_sel_hi:[1,1,0]
	v_pk_fma_f32 v[144:145], v[86:87], v[150:151], v[144:145] op_sel:[0,0,1] op_sel_hi:[1,1,0]
	v_pk_add_f32 v[142:143], v[142:143], v[228:229]
	ds_bpermute_b32 v67, v41, v63
	v_pk_add_f32 v[142:143], v[134:135], v[142:143]
	v_pk_mul_f32 v[134:135], v[14:15], v[182:183]
	v_fmac_f32_e32 v59, v65, v55
	v_pk_fma_f32 v[134:135], v[14:15], v[146:147], v[134:135] op_sel:[0,0,1] op_sel_hi:[1,1,0]
	v_pk_add_f32 v[2:3], v[2:3], v[134:135]
	v_pk_mul_f32 v[134:135], v[88:89], v[184:185]
	v_pk_add_f32 v[2:3], v[2:3], 0 op_sel_hi:[1,0]
	v_pk_fma_f32 v[134:135], v[88:89], v[148:149], v[134:135] op_sel:[0,0,1] op_sel_hi:[1,1,0]
	v_pk_add_f32 v[134:135], v[134:135], v[144:145]
	v_pk_mul_f32 v[144:145], v[98:99], v[202:203]
	v_pk_add_f32 v[2:3], v[2:3], v[134:135]
	v_pk_mul_f32 v[134:135], v[100:101], v[200:201]
	v_pk_fma_f32 v[144:145], v[98:99], v[154:155], v[144:145] op_sel:[0,0,1] op_sel_hi:[1,1,0]
	v_pk_fma_f32 v[134:135], v[100:101], v[152:153], v[134:135] op_sel:[0,0,1] op_sel_hi:[1,1,0]
	v_pk_add_f32 v[134:135], v[134:135], v[144:145]
	v_pk_mul_f32 v[144:145], v[106:107], v[206:207]
	v_pk_add_f32 v[2:3], v[2:3], v[134:135]
	v_pk_mul_f32 v[134:135], v[108:109], v[204:205]
	v_pk_fma_f32 v[144:145], v[106:107], v[158:159], v[144:145] op_sel:[0,0,1] op_sel_hi:[1,1,0]
	v_pk_fma_f32 v[134:135], v[108:109], v[156:157], v[134:135] op_sel:[0,0,1] op_sel_hi:[1,1,0]
	v_pk_add_f32 v[134:135], v[134:135], v[144:145]
	v_pk_mul_f32 v[144:145], v[114:115], v[210:211]
	v_pk_add_f32 v[2:3], v[2:3], v[134:135]
	v_pk_mul_f32 v[134:135], v[116:117], v[208:209]
	v_pk_fma_f32 v[144:145], v[114:115], v[162:163], v[144:145] op_sel:[0,0,1] op_sel_hi:[1,1,0]
	v_pk_fma_f32 v[134:135], v[116:117], v[160:161], v[134:135] op_sel:[0,0,1] op_sel_hi:[1,1,0]
	v_pk_add_f32 v[134:135], v[134:135], v[144:145]
	v_pk_mul_f32 v[144:145], v[122:123], v[214:215]
	v_pk_add_f32 v[2:3], v[2:3], v[134:135]
	v_pk_mul_f32 v[134:135], v[124:125], v[212:213]
	v_pk_fma_f32 v[144:145], v[122:123], v[166:167], v[144:145] op_sel:[0,0,1] op_sel_hi:[1,1,0]
	v_pk_fma_f32 v[134:135], v[124:125], v[164:165], v[134:135] op_sel:[0,0,1] op_sel_hi:[1,1,0]
	v_pk_add_f32 v[134:135], v[134:135], v[144:145]
	v_pk_mul_f32 v[144:145], v[130:131], v[218:219]
	v_pk_add_f32 v[2:3], v[2:3], v[134:135]
	v_pk_mul_f32 v[134:135], v[132:133], v[216:217]
	v_pk_fma_f32 v[144:145], v[130:131], v[176:177], v[144:145] op_sel:[0,0,1] op_sel_hi:[1,1,0]
	v_pk_fma_f32 v[134:135], v[132:133], v[174:175], v[134:135] op_sel:[0,0,1] op_sel_hi:[1,1,0]
	v_pk_add_f32 v[134:135], v[134:135], v[144:145]
	v_pk_mul_f32 v[144:145], v[136:137], v[226:227]
	v_pk_add_f32 v[2:3], v[2:3], v[134:135]
	v_pk_mul_f32 v[134:135], v[138:139], v[224:225]
	v_pk_fma_f32 v[144:145], v[136:137], v[180:181], v[144:145] op_sel:[0,0,1] op_sel_hi:[1,1,0]
	v_pk_fma_f32 v[134:135], v[138:139], v[178:179], v[134:135] op_sel:[0,0,1] op_sel_hi:[1,1,0]
	ds_read_b128 v[146:149], v25 offset:32768
	ds_read_b128 v[150:153], v25 offset:33792
	ds_read_b128 v[154:157], v25 offset:34816
	ds_read_b128 v[158:161], v25 offset:35840
	ds_read_b128 v[162:165], v25 offset:36864
	ds_read_b128 v[174:177], v25 offset:37888
	ds_read_b128 v[178:181], v25 offset:38912
	ds_read_b128 v[182:185], v25 offset:39936
	ds_read_b128 v[198:201], v25 offset:40960
	ds_read_b128 v[202:205], v25 offset:41984
	ds_read_b128 v[206:209], v25 offset:43008
	ds_read_b128 v[210:213], v25 offset:44032
	ds_read_b128 v[214:217], v25 offset:45056
	ds_read_b128 v[224:227], v25 offset:46080
	ds_read_b128 v[228:231], v25 offset:47104
	ds_read_b128 v[232:235], v25 offset:48128
	v_pk_add_f32 v[134:135], v[134:135], v[144:145]
	s_waitcnt lgkmcnt(7)
	v_mov_b32_e32 v166, v200
	v_pk_add_f32 v[2:3], v[2:3], v[134:135]
	v_mov_b32_e32 v134, v198
	v_mov_b32_e32 v135, v147
	v_mov_b32_e32 v167, v149
	v_pk_mul_f32 v[144:145], v[12:13], v[134:135]
	v_mov_b32_e32 v147, v199
	v_pk_mul_f32 v[198:199], v[10:11], v[166:167]
	v_mov_b32_e32 v149, v201
	v_pk_fma_f32 v[144:145], v[12:13], v[146:147], v[144:145] op_sel:[0,0,1] op_sel_hi:[1,1,0]
	v_pk_fma_f32 v[198:199], v[10:11], v[148:149], v[198:199] op_sel:[0,0,1] op_sel_hi:[1,1,0]
	v_pk_mul_f32 v[134:135], v[80:81], v[134:135]
	v_pk_add_f32 v[144:145], v[144:145], v[198:199]
	s_waitcnt lgkmcnt(6)
	v_mov_b32_e32 v198, v202
	v_mov_b32_e32 v199, v151
	v_mov_b32_e32 v151, v203
	v_mov_b32_e32 v202, v204
	v_mov_b32_e32 v203, v153
	v_pk_mul_f32 v[200:201], v[84:85], v[198:199]
	v_pk_mul_f32 v[218:219], v[82:83], v[202:203]
	v_mov_b32_e32 v153, v205
	v_pk_fma_f32 v[200:201], v[84:85], v[150:151], v[200:201] op_sel:[0,0,1] op_sel_hi:[1,1,0]
	v_pk_fma_f32 v[204:205], v[82:83], v[152:153], v[218:219] op_sel:[0,0,1] op_sel_hi:[1,1,0]
	v_pk_add_f32 v[144:145], v[144:145], 0 op_sel_hi:[1,0]
	v_pk_add_f32 v[200:201], v[200:201], v[204:205]
	v_pk_fma_f32 v[134:135], v[80:81], v[146:147], v[134:135] op_sel:[0,0,1] op_sel_hi:[1,1,0]
	v_pk_add_f32 v[144:145], v[144:145], v[200:201]
	s_waitcnt lgkmcnt(5)
	v_mov_b32_e32 v200, v206
	v_mov_b32_e32 v201, v155
	v_mov_b32_e32 v155, v207
	v_mov_b32_e32 v206, v208
	v_mov_b32_e32 v207, v157
	v_pk_mul_f32 v[204:205], v[96:97], v[200:201]
	v_pk_mul_f32 v[218:219], v[94:95], v[206:207]
	v_mov_b32_e32 v157, v209
	v_pk_mul_f32 v[146:147], v[14:15], v[166:167]
	v_pk_fma_f32 v[204:205], v[96:97], v[154:155], v[204:205] op_sel:[0,0,1] op_sel_hi:[1,1,0]
	v_pk_fma_f32 v[208:209], v[94:95], v[156:157], v[218:219] op_sel:[0,0,1] op_sel_hi:[1,1,0]
	v_pk_fma_f32 v[146:147], v[14:15], v[148:149], v[146:147] op_sel:[0,0,1] op_sel_hi:[1,1,0]
	v_pk_add_f32 v[204:205], v[204:205], v[208:209]
	v_pk_add_f32 v[134:135], v[134:135], v[146:147]
	v_pk_mul_f32 v[146:147], v[88:89], v[198:199]
	v_pk_mul_f32 v[148:149], v[86:87], v[202:203]
	v_pk_add_f32 v[144:145], v[144:145], v[204:205]
	s_waitcnt lgkmcnt(4)
	v_mov_b32_e32 v204, v210
	v_mov_b32_e32 v205, v159
	v_mov_b32_e32 v159, v211
	v_mov_b32_e32 v210, v212
	v_mov_b32_e32 v211, v161
	v_pk_fma_f32 v[146:147], v[88:89], v[150:151], v[146:147] op_sel:[0,0,1] op_sel_hi:[1,1,0]
	v_pk_fma_f32 v[148:149], v[86:87], v[152:153], v[148:149] op_sel:[0,0,1] op_sel_hi:[1,1,0]
	v_pk_mul_f32 v[208:209], v[104:105], v[204:205]
	v_pk_mul_f32 v[218:219], v[102:103], v[210:211]
	v_mov_b32_e32 v161, v213
	v_pk_add_f32 v[134:135], v[134:135], 0 op_sel_hi:[1,0]
	v_pk_add_f32 v[146:147], v[146:147], v[148:149]
	v_pk_fma_f32 v[208:209], v[104:105], v[158:159], v[208:209] op_sel:[0,0,1] op_sel_hi:[1,1,0]
	v_pk_fma_f32 v[212:213], v[102:103], v[160:161], v[218:219] op_sel:[0,0,1] op_sel_hi:[1,1,0]
	v_pk_add_f32 v[134:135], v[134:135], v[146:147]
	v_pk_mul_f32 v[146:147], v[100:101], v[200:201]
	v_pk_mul_f32 v[148:149], v[98:99], v[206:207]
	v_pk_add_f32 v[208:209], v[208:209], v[212:213]
	v_pk_fma_f32 v[146:147], v[100:101], v[154:155], v[146:147] op_sel:[0,0,1] op_sel_hi:[1,1,0]
	v_pk_fma_f32 v[148:149], v[98:99], v[156:157], v[148:149] op_sel:[0,0,1] op_sel_hi:[1,1,0]
	v_pk_add_f32 v[144:145], v[144:145], v[208:209]
	s_waitcnt lgkmcnt(3)
	v_mov_b32_e32 v208, v214
	v_mov_b32_e32 v209, v163
	v_mov_b32_e32 v163, v215
	v_mov_b32_e32 v214, v216
	v_mov_b32_e32 v215, v165
	v_pk_add_f32 v[146:147], v[146:147], v[148:149]
	v_pk_mul_f32 v[212:213], v[112:113], v[208:209]
	v_pk_mul_f32 v[218:219], v[110:111], v[214:215]
	v_mov_b32_e32 v165, v217
	v_pk_add_f32 v[134:135], v[134:135], v[146:147]
	v_pk_mul_f32 v[146:147], v[108:109], v[204:205]
	v_pk_mul_f32 v[148:149], v[106:107], v[210:211]
	v_pk_fma_f32 v[212:213], v[112:113], v[162:163], v[212:213] op_sel:[0,0,1] op_sel_hi:[1,1,0]
	v_pk_fma_f32 v[216:217], v[110:111], v[164:165], v[218:219] op_sel:[0,0,1] op_sel_hi:[1,1,0]
	v_pk_fma_f32 v[146:147], v[108:109], v[158:159], v[146:147] op_sel:[0,0,1] op_sel_hi:[1,1,0]
	v_pk_fma_f32 v[148:149], v[106:107], v[160:161], v[148:149] op_sel:[0,0,1] op_sel_hi:[1,1,0]
	v_pk_add_f32 v[212:213], v[212:213], v[216:217]
	v_pk_add_f32 v[146:147], v[146:147], v[148:149]
	v_pk_add_f32 v[144:145], v[144:145], v[212:213]
	s_waitcnt lgkmcnt(2)
	v_mov_b32_e32 v212, v224
	v_mov_b32_e32 v213, v175
	v_mov_b32_e32 v218, v226
	v_mov_b32_e32 v219, v177
	v_pk_add_f32 v[134:135], v[134:135], v[146:147]
	v_pk_mul_f32 v[146:147], v[116:117], v[208:209]
	v_pk_mul_f32 v[148:149], v[114:115], v[214:215]
	v_pk_mul_f32 v[216:217], v[120:121], v[212:213]
	v_mov_b32_e32 v175, v225
	v_pk_mul_f32 v[224:225], v[118:119], v[218:219]
	v_mov_b32_e32 v177, v227
	v_pk_fma_f32 v[146:147], v[116:117], v[162:163], v[146:147] op_sel:[0,0,1] op_sel_hi:[1,1,0]
	v_pk_fma_f32 v[148:149], v[114:115], v[164:165], v[148:149] op_sel:[0,0,1] op_sel_hi:[1,1,0]
	v_pk_fma_f32 v[216:217], v[120:121], v[174:175], v[216:217] op_sel:[0,0,1] op_sel_hi:[1,1,0]
	v_pk_fma_f32 v[224:225], v[118:119], v[176:177], v[224:225] op_sel:[0,0,1] op_sel_hi:[1,1,0]
	v_pk_add_f32 v[146:147], v[146:147], v[148:149]
	v_pk_add_f32 v[216:217], v[216:217], v[224:225]
	v_pk_add_f32 v[134:135], v[134:135], v[146:147]
	v_pk_mul_f32 v[146:147], v[124:125], v[212:213]
	v_pk_mul_f32 v[148:149], v[122:123], v[218:219]
	v_pk_add_f32 v[144:145], v[144:145], v[216:217]
	s_waitcnt lgkmcnt(1)
	v_mov_b32_e32 v216, v228
	v_mov_b32_e32 v217, v179
	v_mov_b32_e32 v226, v230
	v_mov_b32_e32 v227, v181
	v_pk_fma_f32 v[146:147], v[124:125], v[174:175], v[146:147] op_sel:[0,0,1] op_sel_hi:[1,1,0]
	v_pk_fma_f32 v[148:149], v[122:123], v[176:177], v[148:149] op_sel:[0,0,1] op_sel_hi:[1,1,0]
	v_pk_mul_f32 v[224:225], v[128:129], v[216:217]
	v_mov_b32_e32 v179, v229
	v_pk_mul_f32 v[228:229], v[126:127], v[226:227]
	v_mov_b32_e32 v181, v231
	v_pk_add_f32 v[146:147], v[146:147], v[148:149]
	v_pk_fma_f32 v[224:225], v[128:129], v[178:179], v[224:225] op_sel:[0,0,1] op_sel_hi:[1,1,0]
	v_pk_fma_f32 v[228:229], v[126:127], v[180:181], v[228:229] op_sel:[0,0,1] op_sel_hi:[1,1,0]
	v_pk_add_f32 v[134:135], v[134:135], v[146:147]
	v_pk_mul_f32 v[146:147], v[132:133], v[216:217]
	v_pk_mul_f32 v[148:149], v[130:131], v[226:227]
	v_pk_add_f32 v[224:225], v[224:225], v[228:229]
	v_pk_fma_f32 v[146:147], v[132:133], v[178:179], v[146:147] op_sel:[0,0,1] op_sel_hi:[1,1,0]
	v_pk_fma_f32 v[148:149], v[130:131], v[180:181], v[148:149] op_sel:[0,0,1] op_sel_hi:[1,1,0]
	v_pk_add_f32 v[144:145], v[144:145], v[224:225]
	s_waitcnt lgkmcnt(0)
	v_mov_b32_e32 v224, v232
	v_mov_b32_e32 v225, v183
	v_mov_b32_e32 v230, v234
	v_mov_b32_e32 v231, v185
	v_pk_add_f32 v[146:147], v[146:147], v[148:149]
	v_pk_mul_f32 v[228:229], v[92:93], v[224:225]
	v_mov_b32_e32 v183, v233
	v_pk_mul_f32 v[232:233], v[90:91], v[230:231]
	v_mov_b32_e32 v185, v235
	v_pk_add_f32 v[134:135], v[134:135], v[146:147]
	v_pk_mul_f32 v[146:147], v[138:139], v[224:225]
	v_pk_mul_f32 v[148:149], v[136:137], v[230:231]
	v_pk_fma_f32 v[228:229], v[92:93], v[182:183], v[228:229] op_sel:[0,0,1] op_sel_hi:[1,1,0]
	v_pk_fma_f32 v[232:233], v[90:91], v[184:185], v[232:233] op_sel:[0,0,1] op_sel_hi:[1,1,0]
	v_pk_fma_f32 v[146:147], v[138:139], v[182:183], v[146:147] op_sel:[0,0,1] op_sel_hi:[1,1,0]
	v_pk_fma_f32 v[148:149], v[136:137], v[184:185], v[148:149] op_sel:[0,0,1] op_sel_hi:[1,1,0]
	v_pk_add_f32 v[228:229], v[228:229], v[232:233]
	v_pk_add_f32 v[146:147], v[146:147], v[148:149]
	v_pk_add_f32 v[144:145], v[144:145], v[228:229]
	v_pk_add_f32 v[134:135], v[134:135], v[146:147]
	ds_read_b128 v[146:149], v25 offset:49152
	ds_read_b128 v[150:153], v25 offset:50176
	ds_read_b128 v[154:157], v25 offset:51200
	ds_read_b128 v[158:161], v25 offset:52224
	ds_read_b128 v[162:165], v25 offset:53248
	ds_read_b128 v[174:177], v25 offset:54272
	ds_read_b128 v[178:181], v25 offset:55296
	ds_read_b128 v[182:185], v25 offset:56320
	ds_read_b128 v[198:201], v25 offset:57344
	ds_read_b128 v[202:205], v25 offset:58368
	ds_read_b128 v[206:209], v25 offset:59392
	ds_read_b128 v[210:213], v25 offset:60416
	ds_read_b128 v[214:217], v25 offset:61440
	ds_read_b128 v[224:227], v25 offset:62464
	ds_read_b128 v[228:231], v25 offset:63488
	ds_read_b128 v[232:235], v25 offset:64512
	s_waitcnt lgkmcnt(7)
	v_mov_b32_e32 v166, v198
	v_mov_b32_e32 v167, v147
	v_pk_mul_f32 v[218:219], v[12:13], v[166:167]
	v_mov_b32_e32 v147, v199
	v_mov_b32_e32 v198, v200
	v_mov_b32_e32 v199, v149
	v_pk_fma_f32 v[12:13], v[12:13], v[146:147], v[218:219] op_sel:[0,0,1] op_sel_hi:[1,1,0]
	v_pk_mul_f32 v[218:219], v[10:11], v[198:199]
	v_mov_b32_e32 v149, v201
	v_pk_fma_f32 v[10:11], v[10:11], v[148:149], v[218:219] op_sel:[0,0,1] op_sel_hi:[1,1,0]
	s_waitcnt lgkmcnt(6)
	v_mov_b32_e32 v200, v202
	v_mov_b32_e32 v201, v151
	v_pk_add_f32 v[10:11], v[12:13], v[10:11]
	v_pk_mul_f32 v[12:13], v[84:85], v[200:201]
	v_mov_b32_e32 v151, v203
	v_pk_fma_f32 v[12:13], v[84:85], v[150:151], v[12:13] op_sel:[0,0,1] op_sel_hi:[1,1,0]
	v_mov_b32_e32 v84, v204
	v_mov_b32_e32 v85, v153
	v_pk_mul_f32 v[202:203], v[82:83], v[84:85]
	v_mov_b32_e32 v153, v205
	v_pk_fma_f32 v[82:83], v[82:83], v[152:153], v[202:203] op_sel:[0,0,1] op_sel_hi:[1,1,0]
	v_pk_add_f32 v[10:11], v[10:11], 0 op_sel_hi:[1,0]
	v_pk_add_f32 v[12:13], v[12:13], v[82:83]
	s_waitcnt lgkmcnt(5)
	v_mov_b32_e32 v82, v206
	v_mov_b32_e32 v83, v155
	v_pk_add_f32 v[10:11], v[10:11], v[12:13]
	v_pk_mul_f32 v[12:13], v[96:97], v[82:83]
	v_mov_b32_e32 v155, v207
	v_pk_fma_f32 v[12:13], v[96:97], v[154:155], v[12:13] op_sel:[0,0,1] op_sel_hi:[1,1,0]
	v_mov_b32_e32 v96, v208
	v_mov_b32_e32 v97, v157
	v_pk_mul_f32 v[202:203], v[94:95], v[96:97]
	v_mov_b32_e32 v157, v209
	v_pk_fma_f32 v[94:95], v[94:95], v[156:157], v[202:203] op_sel:[0,0,1] op_sel_hi:[1,1,0]
	v_pk_add_f32 v[12:13], v[12:13], v[94:95]
	s_waitcnt lgkmcnt(4)
	v_mov_b32_e32 v94, v210
	v_mov_b32_e32 v95, v159
	v_pk_add_f32 v[10:11], v[10:11], v[12:13]
	v_pk_mul_f32 v[12:13], v[104:105], v[94:95]
	v_mov_b32_e32 v159, v211
	v_pk_fma_f32 v[12:13], v[104:105], v[158:159], v[12:13] op_sel:[0,0,1] op_sel_hi:[1,1,0]
	v_mov_b32_e32 v104, v212
	v_mov_b32_e32 v105, v161
	v_pk_mul_f32 v[202:203], v[102:103], v[104:105]
	v_mov_b32_e32 v161, v213
	v_pk_fma_f32 v[102:103], v[102:103], v[160:161], v[202:203] op_sel:[0,0,1] op_sel_hi:[1,1,0]
	v_pk_add_f32 v[12:13], v[12:13], v[102:103]
	s_waitcnt lgkmcnt(3)
	v_mov_b32_e32 v102, v214
	v_mov_b32_e32 v103, v163
	v_pk_add_f32 v[10:11], v[10:11], v[12:13]
	v_pk_mul_f32 v[12:13], v[112:113], v[102:103]
	v_mov_b32_e32 v163, v215
	v_pk_fma_f32 v[12:13], v[112:113], v[162:163], v[12:13] op_sel:[0,0,1] op_sel_hi:[1,1,0]
	v_mov_b32_e32 v112, v216
	v_mov_b32_e32 v113, v165
	v_pk_mul_f32 v[202:203], v[110:111], v[112:113]
	v_mov_b32_e32 v165, v217
	v_pk_fma_f32 v[110:111], v[110:111], v[164:165], v[202:203] op_sel:[0,0,1] op_sel_hi:[1,1,0]
	v_pk_add_f32 v[12:13], v[12:13], v[110:111]
	s_waitcnt lgkmcnt(2)
	v_mov_b32_e32 v110, v224
	v_mov_b32_e32 v111, v175
	v_pk_add_f32 v[10:11], v[10:11], v[12:13]
	v_pk_mul_f32 v[12:13], v[120:121], v[110:111]
	v_mov_b32_e32 v175, v225
	v_pk_fma_f32 v[12:13], v[120:121], v[174:175], v[12:13] op_sel:[0,0,1] op_sel_hi:[1,1,0]
	v_mov_b32_e32 v120, v226
	v_mov_b32_e32 v121, v177
	v_pk_mul_f32 v[202:203], v[118:119], v[120:121]
	v_mov_b32_e32 v177, v227
	v_pk_fma_f32 v[118:119], v[118:119], v[176:177], v[202:203] op_sel:[0,0,1] op_sel_hi:[1,1,0]
	v_pk_add_f32 v[12:13], v[12:13], v[118:119]
	s_waitcnt lgkmcnt(1)
	v_mov_b32_e32 v118, v228
	v_mov_b32_e32 v119, v179
	v_pk_add_f32 v[10:11], v[10:11], v[12:13]
	v_pk_mul_f32 v[12:13], v[128:129], v[118:119]
	v_mov_b32_e32 v179, v229
	v_pk_fma_f32 v[12:13], v[128:129], v[178:179], v[12:13] op_sel:[0,0,1] op_sel_hi:[1,1,0]
	v_mov_b32_e32 v128, v230
	v_mov_b32_e32 v129, v181
	v_pk_mul_f32 v[202:203], v[126:127], v[128:129]
	v_mov_b32_e32 v181, v231
	v_pk_fma_f32 v[126:127], v[126:127], v[180:181], v[202:203] op_sel:[0,0,1] op_sel_hi:[1,1,0]
	v_pk_add_f32 v[12:13], v[12:13], v[126:127]
	s_waitcnt lgkmcnt(0)
	v_mov_b32_e32 v126, v232
	v_mov_b32_e32 v127, v183
	v_pk_add_f32 v[10:11], v[10:11], v[12:13]
	v_pk_mul_f32 v[12:13], v[92:93], v[126:127]
	v_mov_b32_e32 v183, v233
	v_pk_fma_f32 v[12:13], v[92:93], v[182:183], v[12:13] op_sel:[0,0,1] op_sel_hi:[1,1,0]
	v_mov_b32_e32 v92, v234
	v_mov_b32_e32 v93, v185
	v_pk_mul_f32 v[202:203], v[90:91], v[92:93]
	v_mov_b32_e32 v185, v235
	v_pk_fma_f32 v[90:91], v[90:91], v[184:185], v[202:203] op_sel:[0,0,1] op_sel_hi:[1,1,0]
	v_pk_add_f32 v[12:13], v[12:13], v[90:91]
	v_pk_add_f32 v[12:13], v[10:11], v[12:13]
	v_pk_mul_f32 v[10:11], v[80:81], v[166:167]
	v_pk_fma_f32 v[10:11], v[80:81], v[146:147], v[10:11] op_sel:[0,0,1] op_sel_hi:[1,1,0]
	v_pk_mul_f32 v[80:81], v[14:15], v[198:199]
	v_pk_fma_f32 v[14:15], v[14:15], v[148:149], v[80:81] op_sel:[0,0,1] op_sel_hi:[1,1,0]
	v_pk_mul_f32 v[80:81], v[86:87], v[84:85]
	v_pk_add_f32 v[10:11], v[10:11], v[14:15]
	v_pk_mul_f32 v[14:15], v[88:89], v[200:201]
	v_pk_fma_f32 v[80:81], v[86:87], v[152:153], v[80:81] op_sel:[0,0,1] op_sel_hi:[1,1,0]
	v_pk_fma_f32 v[14:15], v[88:89], v[150:151], v[14:15] op_sel:[0,0,1] op_sel_hi:[1,1,0]
	v_pk_add_f32 v[10:11], v[10:11], 0 op_sel_hi:[1,0]
	v_pk_add_f32 v[14:15], v[14:15], v[80:81]
	v_pk_mul_f32 v[80:81], v[98:99], v[96:97]
	v_pk_add_f32 v[10:11], v[10:11], v[14:15]
	v_pk_mul_f32 v[14:15], v[100:101], v[82:83]
	v_pk_fma_f32 v[80:81], v[98:99], v[156:157], v[80:81] op_sel:[0,0,1] op_sel_hi:[1,1,0]
	v_pk_fma_f32 v[14:15], v[100:101], v[154:155], v[14:15] op_sel:[0,0,1] op_sel_hi:[1,1,0]
	v_pk_add_f32 v[14:15], v[14:15], v[80:81]
	v_pk_mul_f32 v[80:81], v[106:107], v[104:105]
	v_pk_add_f32 v[10:11], v[10:11], v[14:15]
	v_pk_mul_f32 v[14:15], v[108:109], v[94:95]
	v_pk_fma_f32 v[80:81], v[106:107], v[160:161], v[80:81] op_sel:[0,0,1] op_sel_hi:[1,1,0]
	v_pk_fma_f32 v[14:15], v[108:109], v[158:159], v[14:15] op_sel:[0,0,1] op_sel_hi:[1,1,0]
	v_pk_add_f32 v[14:15], v[14:15], v[80:81]
	v_pk_mul_f32 v[80:81], v[114:115], v[112:113]
	v_pk_add_f32 v[10:11], v[10:11], v[14:15]
	v_pk_mul_f32 v[14:15], v[116:117], v[102:103]
	v_pk_fma_f32 v[80:81], v[114:115], v[164:165], v[80:81] op_sel:[0,0,1] op_sel_hi:[1,1,0]
	v_pk_fma_f32 v[14:15], v[116:117], v[162:163], v[14:15] op_sel:[0,0,1] op_sel_hi:[1,1,0]
	v_pk_add_f32 v[14:15], v[14:15], v[80:81]
	v_pk_mul_f32 v[80:81], v[122:123], v[120:121]
	v_pk_add_f32 v[10:11], v[10:11], v[14:15]
	v_pk_mul_f32 v[14:15], v[124:125], v[110:111]
	v_pk_fma_f32 v[80:81], v[122:123], v[176:177], v[80:81] op_sel:[0,0,1] op_sel_hi:[1,1,0]
	v_pk_fma_f32 v[14:15], v[124:125], v[174:175], v[14:15] op_sel:[0,0,1] op_sel_hi:[1,1,0]
	v_pk_add_f32 v[14:15], v[14:15], v[80:81]
	v_pk_mul_f32 v[80:81], v[130:131], v[128:129]
	v_pk_add_f32 v[10:11], v[10:11], v[14:15]
	v_pk_mul_f32 v[14:15], v[132:133], v[118:119]
	v_pk_fma_f32 v[80:81], v[130:131], v[180:181], v[80:81] op_sel:[0,0,1] op_sel_hi:[1,1,0]
	v_pk_fma_f32 v[14:15], v[132:133], v[178:179], v[14:15] op_sel:[0,0,1] op_sel_hi:[1,1,0]
	v_pk_add_f32 v[14:15], v[14:15], v[80:81]
	v_pk_mul_f32 v[80:81], v[136:137], v[92:93]
	v_pk_add_f32 v[10:11], v[10:11], v[14:15]
	v_pk_mul_f32 v[14:15], v[138:139], v[126:127]
	v_pk_fma_f32 v[80:81], v[136:137], v[184:185], v[80:81] op_sel:[0,0,1] op_sel_hi:[1,1,0]
	v_pk_fma_f32 v[14:15], v[138:139], v[182:183], v[14:15] op_sel:[0,0,1] op_sel_hi:[1,1,0]
	v_pk_add_f32 v[14:15], v[14:15], v[80:81]
	v_pk_add_f32 v[10:11], v[10:11], v[14:15]
	v_cmp_eq_u32_e64 s[46:47], 8, v20
	s_nop 1
	v_cndmask_b32_e64 v14, v140, v0, s[46:47]
	ds_bpermute_b32 v14, v39, v14
	v_cmp_eq_u32_e64 s[46:47], 8, v22
	s_nop 1
	v_cndmask_b32_e64 v15, v140, v0, s[46:47]
	s_waitcnt lgkmcnt(0)
	v_add_f32_e32 v69, v15, v14
	v_cmp_eq_u32_e64 s[46:47], 9, v24
	s_nop 1
	v_cndmask_b32_e64 v14, v141, v1, s[46:47]
	ds_bpermute_b32 v14, v39, v14
	v_cmp_eq_u32_e64 s[46:47], 9, v26
	s_nop 1
	v_cndmask_b32_e64 v15, v141, v1, s[46:47]
	s_waitcnt lgkmcnt(0)
	v_add_f32_e32 v71, v15, v14
	v_cmp_eq_u32_e64 s[46:47], 10, v28
	s_nop 1
	v_cndmask_b32_e64 v14, v142, v2, s[46:47]
	ds_bpermute_b32 v14, v39, v14
	v_cmp_eq_u32_e64 s[46:47], 10, v30
	s_nop 1
	v_cndmask_b32_e64 v15, v142, v2, s[46:47]
	s_waitcnt lgkmcnt(0)
	v_add_f32_e32 v73, v15, v14
	v_cmp_eq_u32_e64 s[46:47], 11, v32
	s_nop 1
	v_cndmask_b32_e64 v14, v143, v3, s[46:47]
	ds_bpermute_b32 v14, v39, v14
	v_cmp_eq_u32_e64 s[46:47], 11, v34
	s_nop 1
	v_cndmask_b32_e64 v15, v143, v3, s[46:47]
	s_waitcnt lgkmcnt(0)
	v_add_f32_e32 v75, v15, v14
	v_cmp_eq_u32_e64 s[46:47], 12, v36
	s_nop 1
	v_cndmask_b32_e64 v14, v144, v134, s[46:47]
	ds_bpermute_b32 v14, v39, v14
	v_cmp_eq_u32_e64 s[46:47], 12, v38
	s_nop 1
	v_cndmask_b32_e64 v15, v144, v134, s[46:47]
	s_waitcnt lgkmcnt(0)
	v_add_f32_e32 v14, v15, v14
	v_cmp_eq_u32_e64 s[46:47], 13, v40
	s_nop 1
	v_cndmask_b32_e64 v15, v145, v135, s[46:47]
	ds_bpermute_b32 v15, v39, v15
	v_cmp_eq_u32_e64 s[46:47], 13, v42
	s_nop 1
	v_cndmask_b32_e64 v80, v145, v135, s[46:47]
	s_waitcnt lgkmcnt(0)
	v_add_f32_e32 v15, v80, v15
	v_cmp_eq_u32_e64 s[46:47], 14, v44
	s_nop 1
	v_cndmask_b32_e64 v80, v12, v10, s[46:47]
	ds_bpermute_b32 v80, v39, v80
	v_cmp_eq_u32_e64 s[46:47], 14, v46
	s_nop 1
	v_cndmask_b32_e64 v12, v12, v10, s[46:47]
	s_waitcnt lgkmcnt(0)
	v_add_f32_e32 v12, v12, v80
	v_cmp_eq_u32_e64 s[46:47], 15, v48
	s_nop 1
	v_cndmask_b32_e64 v80, v13, v11, s[46:47]
	ds_bpermute_b32 v80, v39, v80
	v_cmp_eq_u32_e64 s[46:47], 15, v50
	s_nop 1
	v_cndmask_b32_e64 v13, v13, v11, s[46:47]
	s_waitcnt lgkmcnt(0)
	v_add_f32_e32 v13, v13, v80
	v_cmp_eq_u32_e64 s[46:47], 4, v52
	s_nop 1
	v_cndmask_b32_e64 v80, v69, v14, s[46:47]
	ds_bpermute_b32 v80, v37, v80
	v_cmp_eq_u32_e64 s[46:47], 4, v54
	s_nop 1
	v_cndmask_b32_e64 v69, v69, v14, s[46:47]
	s_waitcnt lgkmcnt(0)
	v_add_f32_e32 v69, v69, v80
	v_cmp_eq_u32_e64 s[46:47], 5, v56
	s_nop 1
	v_cndmask_b32_e64 v80, v71, v15, s[46:47]
	ds_bpermute_b32 v80, v37, v80
	v_cmp_eq_u32_e64 s[46:47], 5, v58
	s_nop 1
	v_cndmask_b32_e64 v71, v71, v15, s[46:47]
	s_waitcnt lgkmcnt(0)
	v_add_f32_e32 v71, v71, v80
	v_cmp_eq_u32_e64 s[46:47], 6, v60
	s_nop 1
	v_cndmask_b32_e64 v80, v73, v12, s[46:47]
	ds_bpermute_b32 v80, v37, v80
	v_cmp_eq_u32_e64 s[46:47], 6, v62
	s_nop 1
	v_cndmask_b32_e64 v73, v73, v12, s[46:47]
	s_waitcnt lgkmcnt(0)
	v_add_f32_e32 v73, v73, v80
	v_cmp_eq_u32_e64 s[46:47], 7, v64
	s_nop 1
	v_cndmask_b32_e64 v80, v75, v13, s[46:47]
	ds_bpermute_b32 v80, v37, v80
	v_cmp_eq_u32_e64 s[46:47], 7, v66
	s_nop 1
	v_cndmask_b32_e64 v75, v75, v13, s[46:47]
	s_waitcnt lgkmcnt(0)
	v_add_f32_e32 v75, v75, v80
	v_cmp_eq_u32_e64 s[46:47], 2, v68
	s_nop 1
	v_cndmask_b32_e64 v80, v69, v73, s[46:47]
	ds_bpermute_b32 v80, v41, v80
	v_cmp_eq_u32_e64 s[46:47], 2, v70
	s_nop 1
	v_cndmask_b32_e64 v69, v69, v73, s[46:47]
	s_waitcnt lgkmcnt(0)
	v_add_f32_e32 v69, v69, v80
	v_cmp_eq_u32_e64 s[46:47], 3, v72
	s_nop 1
	v_cndmask_b32_e64 v80, v71, v75, s[46:47]
	ds_bpermute_b32 v41, v41, v80
	v_cmp_eq_u32_e64 s[46:47], 3, v74
	s_nop 1
	v_cndmask_b32_e64 v71, v71, v75, s[46:47]
	s_waitcnt lgkmcnt(0)
	v_add_f32_e32 v41, v71, v41
	v_cmp_ne_u64_e64 s[46:47], 0, v[76:77]
	s_nop 1
	v_cndmask_b32_e64 v71, v69, v41, s[46:47]
	v_cmp_eq_u32_e64 s[46:47], 2, v76
	s_nop 1
	v_cndmask_b32_e64 v71, v71, v73, s[46:47]
	v_cmp_eq_u32_e64 s[46:47], 3, v76
	s_nop 1
	v_cndmask_b32_e64 v71, v71, v75, s[46:47]
	v_cmp_eq_u32_e64 s[46:47], 4, v76
	s_nop 1
	v_cndmask_b32_e64 v71, v71, v14, s[46:47]
	v_cmp_eq_u32_e64 s[46:47], 5, v76
	s_nop 1
	v_cndmask_b32_e64 v71, v71, v15, s[46:47]
	v_cmp_eq_u32_e64 s[46:47], 6, v76
	s_nop 1
	v_cndmask_b32_e64 v71, v71, v12, s[46:47]
	v_cmp_eq_u32_e64 s[46:47], 7, v76
	s_nop 1
	v_cndmask_b32_e64 v71, v71, v13, s[46:47]
	v_cmp_eq_u32_e64 s[46:47], 8, v76
	s_nop 1
	v_cndmask_b32_e64 v71, v71, v0, s[46:47]
	v_cmp_eq_u32_e64 s[46:47], 9, v76
	s_nop 1
	v_cndmask_b32_e64 v71, v71, v1, s[46:47]
	v_cmp_eq_u32_e64 s[46:47], 10, v76
	s_nop 1
	v_cndmask_b32_e64 v71, v71, v2, s[46:47]
	v_cmp_eq_u32_e64 s[46:47], 11, v76
	s_nop 1
	v_cndmask_b32_e64 v71, v71, v3, s[46:47]
	v_cmp_eq_u32_e64 s[46:47], 12, v76
	s_nop 1
	v_cndmask_b32_e64 v71, v71, v134, s[46:47]
	v_cmp_eq_u32_e64 s[46:47], 13, v76
	s_nop 1
	v_cndmask_b32_e64 v71, v71, v135, s[46:47]
	v_cmp_ne_u64_e64 s[46:47], 0, v[78:79]
	s_nop 1
	v_cndmask_b32_e64 v41, v69, v41, s[46:47]
	v_cmp_eq_u32_e64 s[46:47], 2, v78
	s_nop 1
	v_cndmask_b32_e64 v41, v41, v73, s[46:47]
	v_cmp_eq_u32_e64 s[46:47], 3, v78
	s_nop 1
	v_cndmask_b32_e64 v41, v41, v75, s[46:47]
	v_cmp_eq_u32_e64 s[46:47], 4, v78
	s_nop 1
	v_cndmask_b32_e64 v14, v41, v14, s[46:47]
	v_cmp_eq_u32_e64 s[46:47], 5, v78
	s_nop 1
	v_cndmask_b32_e64 v14, v14, v15, s[46:47]
	v_cmp_eq_u32_e64 s[46:47], 6, v78
	s_nop 1
	v_cndmask_b32_e64 v12, v14, v12, s[46:47]
	v_cmp_eq_u32_e64 s[46:47], 7, v78
	s_nop 1
	v_cndmask_b32_e64 v12, v12, v13, s[46:47]
	v_cmp_eq_u32_e64 s[46:47], 8, v78
	s_nop 1
	v_cndmask_b32_e64 v0, v12, v0, s[46:47]
	v_cmp_eq_u32_e64 s[46:47], 9, v78
	s_nop 1
	v_cndmask_b32_e64 v0, v0, v1, s[46:47]
	v_cmp_eq_u32_e64 s[46:47], 10, v78
	s_nop 1
	v_cndmask_b32_e64 v0, v0, v2, s[46:47]
	v_cmp_eq_u32_e64 s[46:47], 11, v78
	v_fma_f32 v2, -v57, v59, v61
	s_nop 0
	v_cndmask_b32_e64 v0, v0, v3, s[46:47]
	v_cmp_eq_u32_e64 s[46:47], 12, v78
	v_add_f32_e32 v3, v63, v67
	s_nop 0
	v_cndmask_b32_e64 v0, v0, v134, s[46:47]
	v_cmp_eq_u32_e64 s[46:47], 13, v78
	s_nop 1
	v_cndmask_b32_e64 v0, v0, v135, s[46:47]
	v_cmp_eq_u32_e64 s[46:47], 14, v78
	s_nop 1
	v_cndmask_b32_e64 v0, v0, v10, s[46:47]
	v_cmp_eq_u32_e64 s[46:47], 15, v78
	s_nop 1
	v_cndmask_b32_e64 v0, v0, v11, s[46:47]
	ds_bpermute_b32 v0, v35, v0
	v_cmp_eq_u32_e64 s[46:47], 14, v76
	s_nop 1
	v_cndmask_b32_e64 v1, v71, v10, s[46:47]
	v_cmp_eq_u32_e64 s[46:47], 15, v76
	ds_bpermute_b32 v10, v37, v3
	s_nop 0
	v_cndmask_b32_e64 v1, v1, v11, s[46:47]
	s_waitcnt lgkmcnt(1)
	v_add_f32_e32 v0, v1, v0
	ds_bpermute_b32 v1, v33, v0
	s_waitcnt lgkmcnt(0)
	v_add_f32_e32 v1, v0, v1
	ds_bpermute_b32 v11, v31, v1
	v_div_fmas_f32 v0, v2, v55, v59
	v_div_fixup_f32 v12, v0, v53, 1.0
	v_add_f32_e32 v0, v3, v10
	ds_bpermute_b32 v2, v39, v0
	s_waitcnt lgkmcnt(1)
	v_add_f32_e32 v3, v1, v11
	s_nop 0
	v_readlane_b32 s1, v3, 0
	v_readlane_b32 s0, v3, 4
	v_readlane_b32 s8, v3, 32
	v_readlane_b32 s9, v3, 36
	v_pk_mul_f32 v[14:15], v[12:13], s[0:1] op_sel_hi:[0,1]
	v_readlane_b32 s0, v3, 8
	v_cmp_gt_f32_e32 vcc, v14, v15
	v_readlane_b32 s10, v3, 40
	v_mul_f32_e32 v11, s0, v12
	v_readlane_b32 s0, v3, 12
	v_readlane_b32 s11, v3, 44
	v_readlane_b32 s12, v3, 48
	v_mul_f32_e32 v13, s0, v12
	v_readlane_b32 s0, v3, 16
	v_readlane_b32 s13, v3, 52
	v_readlane_b32 s14, v3, 56
	v_mul_f32_e32 v31, s0, v12
	v_readlane_b32 s0, v3, 20
	v_readlane_b32 s15, v3, 60
	v_cndmask_b32_e64 v10, 0, 1, vcc
	v_mul_f32_e32 v33, s0, v12
	v_readlane_b32 s0, v3, 24
	v_cmp_lt_f32_e64 s[52:53], s33, v15
	s_nop 0
	v_mul_f32_e32 v35, s0, v12
	v_readlane_b32 s0, v3, 28
	v_cndmask_b32_e32 v3, v15, v14, vcc
	v_cmp_gt_f32_e32 vcc, v11, v3
	v_mul_f32_e32 v1, s0, v12
	s_nop 0
	v_cndmask_b32_e32 v3, v3, v11, vcc
	v_cndmask_b32_e64 v10, v10, 2, vcc
	v_cmp_gt_f32_e32 vcc, v13, v3
	s_nop 1
	v_cndmask_b32_e32 v3, v3, v13, vcc
	v_cndmask_b32_e64 v10, v10, 3, vcc
	v_cmp_gt_f32_e32 vcc, v31, v3
	s_nop 1
	v_cndmask_b32_e32 v3, v3, v31, vcc
	v_cndmask_b32_e64 v10, v10, 4, vcc
	v_cmp_gt_f32_e32 vcc, v33, v3
	s_nop 1
	v_cndmask_b32_e32 v3, v3, v33, vcc
	v_cndmask_b32_e64 v10, v10, 5, vcc
	v_cmp_ngt_f32_e32 vcc, v35, v3
	s_nop 1
	v_cndmask_b32_e32 v3, v35, v3, vcc
	v_cndmask_b32_e32 v10, 6, v10, vcc
	v_cmp_gt_f32_e64 s[48:49], v1, v3
	s_or_b64 s[0:1], vcc, s[48:49]
	v_cmp_ngt_f32_e64 s[46:47], v1, v3
	v_cndmask_b32_e64 v10, v10, 7, s[48:49]
	v_cmp_ne_u32_e64 s[50:51], 0, v10
	s_and_b64 s[50:51], s[50:51], s[52:53]
	s_nop 0
	v_cndmask_b32_e64 v15, v196, v15, s[50:51]
	v_cmp_ne_u32_e64 s[50:51], 1, v10
	v_cmp_gt_f32_e64 s[52:53], v14, v15
	s_and_b64 s[50:51], s[50:51], s[52:53]
	v_cndmask_b32_e64 v14, v15, v14, s[50:51]
	v_cndmask_b32_e64 v15, 0, 1, s[50:51]
	v_cmp_ne_u32_e64 s[50:51], 2, v10
	v_cmp_gt_f32_e64 s[52:53], v11, v14
	s_and_b64 s[50:51], s[50:51], s[52:53]
	v_cndmask_b32_e64 v11, v14, v11, s[50:51]
	v_cndmask_b32_e64 v14, v15, 2, s[50:51]
	v_cmp_ne_u32_e64 s[50:51], 3, v10
	v_cmp_gt_f32_e64 s[52:53], v13, v11
	s_and_b64 s[50:51], s[50:51], s[52:53]
	v_cndmask_b32_e64 v11, v11, v13, s[50:51]
	v_cndmask_b32_e64 v13, v14, 3, s[50:51]
	v_cmp_ne_u32_e64 s[50:51], 4, v10
	v_cmp_gt_f32_e64 s[52:53], v31, v11
	s_and_b64 s[50:51], s[50:51], s[52:53]
	v_cndmask_b32_e64 v11, v11, v31, s[50:51]
	v_cndmask_b32_e64 v13, v13, 4, s[50:51]
	v_cmp_ne_u32_e64 s[50:51], 5, v10
	v_cmp_gt_f32_e64 s[52:53], v33, v11
	s_and_b64 s[50:51], s[50:51], s[52:53]
	v_cndmask_b32_e64 v11, v11, v33, s[50:51]
	v_cmp_gt_f32_e32 vcc, v35, v11
	v_cndmask_b32_e64 v13, v13, 5, s[50:51]
	s_and_b64 vcc, s[0:1], vcc
	v_cndmask_b32_e32 v35, v11, v35, vcc
	v_cndmask_b32_e64 v13, v13, 6, vcc
	s_and_saveexec_b64 s[0:1], s[46:47]
	s_cbranch_execz .LBB0_1352
	v_cmp_gt_f32_e32 vcc, v1, v35
	s_and_saveexec_b64 s[2:3], vcc
	v_mov_b32_e32 v13, 7
	v_mov_b32_e32 v35, v1
	s_or_b64 exec, exec, s[2:3]
	v_mov_b32_e32 v1, v3
